# nt hint on read-once f32 weight/x loads in prologue and late moe convert
# speedup vs baseline: 1.0051x; 1.0051x over previous
.LBB0_10:
	v_ashrrev_i32_e32 v34, 31, v33
	v_lshrrev_b32_e32 v34, 28, v34
	v_add_u32_e32 v34, v33, v34
	v_ashrrev_i32_e32 v37, 4, v34
	v_lshlrev_b32_e32 v36, 5, v37
	v_mad_u64_u32 v[38:39], s[0:1], v37, s25, v[30:31]
	v_lshlrev_b32_e32 v86, 11, v37
	v_ashrrev_i32_e32 v37, 31, v36
	v_ashrrev_i32_e32 v39, 31, v38
	v_sub_u32_e32 v86, v32, v86
	v_lshl_add_u64 v[88:89], v[36:37], 2, v[28:29]
	v_ashrrev_i32_e32 v87, 31, v86
	v_lshl_add_u64 v[38:39], v[38:39], 2, v[88:89]
	v_lshl_add_u64 v[148:149], v[18:19], 0, v[86:87]
	v_add_co_u32_e64 v86, s[0:1], s26, v38
	v_ashrrev_i32_e32 v34, 6, v34
	s_nop 0
	v_addc_co_u32_e64 v87, s[0:1], 0, v39, s[0:1]
	v_add_co_u32_e64 v90, s[0:1], s27, v38
	v_ashrrev_i32_e32 v35, 31, v34
	s_nop 0
	v_addc_co_u32_e64 v91, s[0:1], 0, v39, s[0:1]
	v_add_co_u32_e64 v94, s[0:1], s28, v38
	v_lshlrev_b64 v[34:35], 8, v[34:35]
	s_nop 0
	v_addc_co_u32_e64 v95, s[0:1], 0, v39, s[0:1]
	v_add_co_u32_e64 v98, s[0:1], s22, v38
	v_lshl_add_u64 v[146:147], v[34:35], 0, s[14:15]
	s_nop 0
	v_addc_co_u32_e64 v99, s[0:1], 0, v39, s[0:1]
	v_add_co_u32_e64 v102, s[0:1], s29, v38
	v_and_or_b32 v154, v36, s24, v146
	s_nop 0
	v_addc_co_u32_e64 v103, s[0:1], 0, v39, s[0:1]
	v_add_co_u32_e64 v106, s[0:1], s30, v38
	global_load_dwordx4 v[34:37], v[38:39], off nt
	s_nop 0
	v_addc_co_u32_e64 v107, s[0:1], 0, v39, s[0:1]
	v_add_co_u32_e64 v110, s[0:1], s31, v38
	v_add_u32_e32 v71, 0x35a0, v40
	s_nop 0
	v_addc_co_u32_e64 v111, s[0:1], 0, v39, s[0:1]
	v_add_co_u32_e64 v114, s[0:1], s33, v38
	v_add_u32_e32 v73, 0x35a8, v40
	s_nop 0
	v_addc_co_u32_e64 v115, s[0:1], 0, v39, s[0:1]
	v_add_co_u32_e64 v118, s[0:1], s34, v38
	v_add_u32_e32 v76, 0x39c0, v40
	s_nop 0
	v_addc_co_u32_e64 v119, s[0:1], 0, v39, s[0:1]
	v_add_co_u32_e64 v122, s[0:1], s35, v38
	v_add_u32_e32 v77, 0x39c8, v40
	s_nop 0
	v_addc_co_u32_e64 v123, s[0:1], 0, v39, s[0:1]
	v_add_co_u32_e64 v126, s[0:1], s60, v38
	v_add_u32_e32 v82, 0x3de0, v40
	s_nop 0
	v_addc_co_u32_e64 v127, s[0:1], 0, v39, s[0:1]
	v_add_co_u32_e64 v130, s[0:1], s61, v38
	v_add_u32_e32 v83, 0x3de8, v40
	s_nop 0
	v_addc_co_u32_e64 v131, s[0:1], 0, v39, s[0:1]
	v_add_co_u32_e64 v134, s[0:1], s62, v38
	v_add_u32_e32 v84, 0x400, v75
	s_nop 0
	v_addc_co_u32_e64 v135, s[0:1], 0, v39, s[0:1]
	v_add_co_u32_e64 v138, s[0:1], s63, v38
	v_add_u32_e32 v85, 0x600, v75
	s_nop 0
	v_addc_co_u32_e64 v139, s[0:1], 0, v39, s[0:1]
	v_add_co_u32_e64 v38, s[0:1], s64, v38
	v_mov_b32_e32 v2, 0
	s_nop 0
	v_addc_co_u32_e64 v39, s[0:1], 0, v39, s[0:1]
	global_load_dwordx4 v[86:89], v[86:87], off nt
	s_nop 0
	global_load_dwordx4 v[90:93], v[90:91], off nt
	s_nop 0
	global_load_dwordx4 v[94:97], v[94:95], off nt
	s_nop 0
	global_load_dwordx4 v[98:101], v[98:99], off nt
	s_nop 0
	global_load_dwordx4 v[102:105], v[102:103], off nt
	s_nop 0
	global_load_dwordx4 v[106:109], v[106:107], off nt
	s_nop 0
	global_load_dwordx4 v[110:113], v[110:111], off nt
	s_nop 0
	global_load_dwordx4 v[114:117], v[114:115], off nt
	s_nop 0
	global_load_dwordx4 v[118:121], v[118:119], off nt
	s_nop 0
	global_load_dwordx4 v[122:125], v[122:123], off nt
	s_nop 0
	global_load_dwordx4 v[126:129], v[126:127], off nt
	s_nop 0
	global_load_dwordx4 v[130:133], v[130:131], off nt
	s_nop 0
	global_load_dwordx4 v[134:137], v[134:135], off nt
	s_nop 0
	global_load_dwordx4 v[138:141], v[138:139], off nt
	s_nop 0
	global_load_dwordx4 v[142:145], v[38:39], off nt
	v_mov_b32_e32 v3, 0
	v_mov_b32_e32 v4, 0
	v_mov_b32_e32 v5, 0
	v_mov_b32_e32 v6, 0
	v_mov_b32_e32 v7, 0
	v_mov_b32_e32 v8, 0
	v_mov_b32_e32 v9, 0
	v_mov_b32_e32 v10, 0
	v_mov_b32_e32 v11, 0
	v_mov_b32_e32 v12, 0
	v_mov_b32_e32 v13, 0
	v_mov_b32_e32 v14, 0
	v_mov_b32_e32 v15, 0
	v_mov_b32_e32 v16, 0
	v_mov_b32_e32 v17, 0
	v_or_b32_e32 v146, v154, v66
	v_lshlrev_b64 v[38:39], 11, v[146:147]
	v_or_b32_e32 v146, v154, v68
	v_lshlrev_b64 v[150:151], 11, v[146:147]
	v_or_b32_e32 v146, v154, v70
	v_lshlrev_b64 v[152:153], 11, v[146:147]
	v_or_b32_e32 v146, v154, v72
	v_lshl_add_u64 v[38:39], v[148:149], 0, v[38:39]
	v_lshlrev_b64 v[146:147], 11, v[146:147]
	v_lshl_add_u64 v[150:151], v[148:149], 0, v[150:151]
	v_lshl_add_u64 v[152:153], v[148:149], 0, v[152:153]
	s_waitcnt vmcnt(15)
	ds_write2_b32 v40, v34, v35 offset1:1
	ds_write2_b32 v40, v36, v37 offset0:2 offset1:3
	s_waitcnt vmcnt(14)
	ds_write2_b32 v41, v86, v87 offset1:1
	ds_write2_b32 v42, v88, v89 offset1:1
	s_waitcnt vmcnt(13)
	ds_write2_b32 v43, v90, v91 offset1:1
	ds_write2_b32 v44, v92, v93 offset1:1
	s_waitcnt vmcnt(12)
	ds_write2_b32 v45, v94, v95 offset1:1
	ds_write2_b32 v46, v96, v97 offset1:1
	s_waitcnt vmcnt(11)
	ds_write2_b32 v47, v98, v99 offset1:1
	ds_write2_b32 v48, v100, v101 offset1:1
	s_waitcnt vmcnt(10)
	ds_write2_b32 v49, v102, v103 offset1:1
	ds_write2_b32 v50, v104, v105 offset1:1
	s_waitcnt vmcnt(9)
	ds_write2_b32 v51, v106, v107 offset1:1
	ds_write2_b32 v52, v108, v109 offset1:1
	s_waitcnt vmcnt(8)
	ds_write2_b32 v53, v110, v111 offset1:1
	ds_write2_b32 v54, v112, v113 offset1:1
	s_waitcnt vmcnt(7)
	ds_write2_b32 v55, v114, v115 offset1:1
	ds_write2_b32 v56, v116, v117 offset1:1
	s_waitcnt vmcnt(6)
	ds_write2_b32 v57, v118, v119 offset1:1
	ds_write2_b32 v58, v120, v121 offset1:1
	s_waitcnt vmcnt(5)
	ds_write2_b32 v59, v122, v123 offset1:1
	ds_write2_b32 v60, v124, v125 offset1:1
	s_waitcnt vmcnt(4)
	ds_write2_b32 v61, v126, v127 offset1:1
	ds_write2_b32 v62, v128, v129 offset1:1
	s_waitcnt vmcnt(3)
	ds_write2_b32 v63, v130, v131 offset1:1
	ds_write2_b32 v64, v132, v133 offset1:1
	s_waitcnt vmcnt(2)
	ds_write2_b32 v71, v134, v135 offset1:1
	ds_write2_b32 v73, v136, v137 offset1:1
	s_waitcnt vmcnt(1)
	ds_write2_b32 v76, v138, v139 offset1:1
	ds_write2_b32 v77, v140, v141 offset1:1
	s_waitcnt vmcnt(0)
	ds_write2_b32 v82, v142, v143 offset1:1
	ds_write2_b32 v83, v144, v145 offset1:1
	s_waitcnt lgkmcnt(0)
	ds_read2_b32 v[34:35], v75 offset1:8
	ds_read2_b32 v[36:37], v75 offset0:33 offset1:41
	ds_read2_b32 v[86:87], v75 offset0:132 offset1:140
	ds_read2_b32 v[88:89], v75 offset0:165 offset1:173
	ds_read2_b32 v[90:91], v84 offset0:8 offset1:16
	ds_read2_b32 v[92:93], v84 offset0:41 offset1:49
	ds_read2_b32 v[94:95], v84 offset0:140 offset1:148
	ds_read2_b32 v[96:97], v84 offset0:173 offset1:181
	ds_read2_b32 v[98:99], v75 offset0:66 offset1:74
	ds_read2_b32 v[100:101], v75 offset0:99 offset1:107
	ds_read2_b32 v[102:103], v75 offset0:198 offset1:206
	ds_read2_b32 v[104:105], v75 offset0:231 offset1:239
	ds_read2_b32 v[106:107], v84 offset0:74 offset1:82
	ds_read2_b32 v[108:109], v84 offset0:107 offset1:115
	ds_read2_b32 v[110:111], v84 offset0:206 offset1:214
	ds_read2_b32 v[112:113], v84 offset0:239 offset1:247
	ds_read2_b32 v[114:115], v75 offset0:16 offset1:24
	ds_read2_b32 v[116:117], v75 offset0:49 offset1:57
	ds_read2_b32 v[118:119], v75 offset0:148 offset1:156
	ds_read2_b32 v[120:121], v75 offset0:181 offset1:189
	ds_read2_b32 v[122:123], v84 offset0:24 offset1:32
	ds_read2_b32 v[124:125], v84 offset0:57 offset1:65
	ds_read2_b32 v[126:127], v84 offset0:156 offset1:164
	ds_read2_b32 v[128:129], v84 offset0:189 offset1:197
	ds_read2_b32 v[130:131], v75 offset0:82 offset1:90
	ds_read2_b32 v[132:133], v75 offset0:115 offset1:123
	ds_read2_b32 v[134:135], v75 offset0:214 offset1:222
	ds_read2_b32 v[136:137], v75 offset0:247 offset1:255
	ds_read2_b32 v[138:139], v84 offset0:90 offset1:98
	ds_read2_b32 v[140:141], v84 offset0:123 offset1:131
	ds_read2_b32 v[142:143], v84 offset0:222 offset1:230
	ds_read2_b32 v[144:145], v85 offset0:127 offset1:135
	s_waitcnt lgkmcnt(14)
	v_mul_f32_e32 v34, 0x43800000, v34
	v_mul_f32_e32 v36, 0x43800000, v36
	v_mul_f32_e32 v86, 0x43800000, v86
	v_mul_f32_e32 v88, 0x43800000, v88
	v_mul_f32_e32 v90, 0x43800000, v90
	v_mul_f32_e32 v92, 0x43800000, v92
	v_mul_f32_e32 v94, 0x43800000, v94
	v_mul_f32_e32 v96, 0x43800000, v96
	v_mul_f32_e32 v35, 0x43800000, v35
	v_mul_f32_e32 v37, 0x43800000, v37
	v_mul_f32_e32 v87, 0x43800000, v87
	v_mul_f32_e32 v89, 0x43800000, v89
	v_mul_f32_e32 v91, 0x43800000, v91
	v_mul_f32_e32 v93, 0x43800000, v93
	v_mul_f32_e32 v95, 0x43800000, v95
	v_mul_f32_e32 v97, 0x43800000, v97
	v_med3_f32 v34, v34, s65, v65
	v_med3_f32 v36, v36, s65, v65
	v_med3_f32 v86, v86, s65, v65
	v_med3_f32 v88, v88, s65, v65
	v_med3_f32 v90, v90, s65, v65
	v_med3_f32 v92, v92, s65, v65
	v_med3_f32 v94, v94, s65, v65
	v_med3_f32 v96, v96, s65, v65
	v_mul_f32_e32 v114, 0x43800000, v114
	v_mul_f32_e32 v116, 0x43800000, v116
	s_waitcnt lgkmcnt(13)
	v_mul_f32_e32 v118, 0x43800000, v118
	s_waitcnt lgkmcnt(12)
	v_mul_f32_e32 v120, 0x43800000, v120
	s_waitcnt lgkmcnt(11)
	v_mul_f32_e32 v122, 0x43800000, v122
	s_waitcnt lgkmcnt(10)
	v_mul_f32_e32 v124, 0x43800000, v124
	s_waitcnt lgkmcnt(9)
	v_mul_f32_e32 v126, 0x43800000, v126
	s_waitcnt lgkmcnt(8)
	v_mul_f32_e32 v128, 0x43800000, v128
	v_med3_f32 v35, v35, s65, v65
	v_med3_f32 v37, v37, s65, v65
	v_med3_f32 v87, v87, s65, v65
	v_med3_f32 v89, v89, s65, v65
	v_med3_f32 v91, v91, s65, v65
	v_med3_f32 v93, v93, s65, v65
	v_med3_f32 v95, v95, s65, v65
	v_med3_f32 v97, v97, s65, v65
	v_cvt_pk_fp8_f32 v2, v34, v36
	v_cvt_pk_fp8_f32 v3, v86, v88
	v_cvt_pk_fp8_f32 v4, v90, v92
	v_cvt_pk_fp8_f32 v5, v94, v96
	v_mul_f32_e32 v115, 0x43800000, v115
	v_mul_f32_e32 v117, 0x43800000, v117
	v_mul_f32_e32 v119, 0x43800000, v119
	v_mul_f32_e32 v121, 0x43800000, v121
	v_mul_f32_e32 v123, 0x43800000, v123
	v_mul_f32_e32 v125, 0x43800000, v125
	v_mul_f32_e32 v127, 0x43800000, v127
	v_mul_f32_e32 v129, 0x43800000, v129
	v_med3_f32 v114, v114, s65, v65
	v_med3_f32 v116, v116, s65, v65
	v_med3_f32 v118, v118, s65, v65
	v_med3_f32 v120, v120, s65, v65
	v_med3_f32 v122, v122, s65, v65
	v_med3_f32 v124, v124, s65, v65
	v_med3_f32 v126, v126, s65, v65
	v_med3_f32 v128, v128, s65, v65
	v_cvt_pk_fp8_f32 v6, v35, v37
	v_cvt_pk_fp8_f32 v7, v87, v89
	v_cvt_pk_fp8_f32 v8, v91, v93
	v_cvt_pk_fp8_f32 v9, v95, v97
	v_mul_f32_e32 v98, 0x43800000, v98
	v_mul_f32_e32 v100, 0x43800000, v100
	v_mul_f32_e32 v102, 0x43800000, v102
	v_mul_f32_e32 v104, 0x43800000, v104
	v_mul_f32_e32 v106, 0x43800000, v106
	v_mul_f32_e32 v108, 0x43800000, v108
	v_mul_f32_e32 v110, 0x43800000, v110
	v_mul_f32_e32 v112, 0x43800000, v112
	v_med3_f32 v115, v115, s65, v65
	v_med3_f32 v117, v117, s65, v65
	v_med3_f32 v119, v119, s65, v65
	v_med3_f32 v121, v121, s65, v65
	v_med3_f32 v123, v123, s65, v65
	v_med3_f32 v125, v125, s65, v65
	v_med3_f32 v127, v127, s65, v65
	v_med3_f32 v129, v129, s65, v65
	v_cvt_pk_fp8_f32 v10, v114, v116
	v_cvt_pk_fp8_f32 v11, v118, v120
	v_cvt_pk_fp8_f32 v12, v122, v124
	v_cvt_pk_fp8_f32 v13, v126, v128
	v_mul_f32_e32 v99, 0x43800000, v99
	v_mul_f32_e32 v101, 0x43800000, v101
	v_mul_f32_e32 v103, 0x43800000, v103
	v_mul_f32_e32 v105, 0x43800000, v105
	v_mul_f32_e32 v107, 0x43800000, v107
	v_mul_f32_e32 v109, 0x43800000, v109
	v_mul_f32_e32 v111, 0x43800000, v111
	v_mul_f32_e32 v113, 0x43800000, v113
	v_med3_f32 v98, v98, s65, v65
	v_med3_f32 v100, v100, s65, v65
	v_med3_f32 v102, v102, s65, v65
	v_med3_f32 v104, v104, s65, v65
	v_med3_f32 v106, v106, s65, v65
	v_med3_f32 v108, v108, s65, v65
	v_med3_f32 v110, v110, s65, v65
	v_med3_f32 v112, v112, s65, v65
	v_cvt_pk_fp8_f32 v14, v115, v117
	v_cvt_pk_fp8_f32 v15, v119, v121
	v_cvt_pk_fp8_f32 v16, v123, v125
	v_cvt_pk_fp8_f32 v17, v127, v129
	s_waitcnt lgkmcnt(7)
	v_mul_f32_e32 v130, 0x43800000, v130
	s_waitcnt lgkmcnt(6)
	v_mul_f32_e32 v132, 0x43800000, v132
	s_waitcnt lgkmcnt(5)
	v_mul_f32_e32 v134, 0x43800000, v134
	s_waitcnt lgkmcnt(4)
	v_mul_f32_e32 v136, 0x43800000, v136
	s_waitcnt lgkmcnt(3)
	v_mul_f32_e32 v138, 0x43800000, v138
	s_waitcnt lgkmcnt(2)
	v_mul_f32_e32 v140, 0x43800000, v140
	s_waitcnt lgkmcnt(1)
	v_mul_f32_e32 v142, 0x43800000, v142
	s_waitcnt lgkmcnt(0)
	v_mul_f32_e32 v144, 0x43800000, v144
	v_med3_f32 v99, v99, s65, v65
	v_med3_f32 v101, v101, s65, v65
	v_med3_f32 v103, v103, s65, v65
	v_med3_f32 v105, v105, s65, v65
	v_med3_f32 v107, v107, s65, v65
	v_med3_f32 v109, v109, s65, v65
	v_med3_f32 v111, v111, s65, v65
	v_med3_f32 v113, v113, s65, v65
	v_cvt_pk_fp8_f32 v2, v98, v100 op_sel:[0,0,1]
	v_cvt_pk_fp8_f32 v3, v102, v104 op_sel:[0,0,1]
	v_cvt_pk_fp8_f32 v4, v106, v108 op_sel:[0,0,1]
	v_cvt_pk_fp8_f32 v5, v110, v112 op_sel:[0,0,1]
	v_mul_f32_e32 v131, 0x43800000, v131
	v_mul_f32_e32 v133, 0x43800000, v133
	v_mul_f32_e32 v135, 0x43800000, v135
	v_mul_f32_e32 v137, 0x43800000, v137
	v_mul_f32_e32 v139, 0x43800000, v139
	v_mul_f32_e32 v141, 0x43800000, v141
	v_mul_f32_e32 v143, 0x43800000, v143
	v_mul_f32_e32 v145, 0x43800000, v145
	v_med3_f32 v130, v130, s65, v65
	v_med3_f32 v132, v132, s65, v65
	v_med3_f32 v134, v134, s65, v65
	v_med3_f32 v136, v136, s65, v65
	v_med3_f32 v138, v138, s65, v65
	v_med3_f32 v140, v140, s65, v65
	v_med3_f32 v142, v142, s65, v65
	v_med3_f32 v144, v144, s65, v65
	v_cvt_pk_fp8_f32 v6, v99, v101 op_sel:[0,0,1]
	v_cvt_pk_fp8_f32 v7, v103, v105 op_sel:[0,0,1]
	v_cvt_pk_fp8_f32 v8, v107, v109 op_sel:[0,0,1]
	v_cvt_pk_fp8_f32 v9, v111, v113 op_sel:[0,0,1]
	v_med3_f32 v131, v131, s65, v65
	v_med3_f32 v133, v133, s65, v65
	v_med3_f32 v135, v135, s65, v65
	v_med3_f32 v137, v137, s65, v65
	v_med3_f32 v139, v139, s65, v65
	v_med3_f32 v141, v141, s65, v65
	v_med3_f32 v143, v143, s65, v65
	v_med3_f32 v145, v145, s65, v65
	v_cvt_pk_fp8_f32 v10, v130, v132 op_sel:[0,0,1]
	v_cvt_pk_fp8_f32 v11, v134, v136 op_sel:[0,0,1]
	v_cvt_pk_fp8_f32 v12, v138, v140 op_sel:[0,0,1]
	v_cvt_pk_fp8_f32 v13, v142, v144 op_sel:[0,0,1]
	v_cvt_pk_fp8_f32 v14, v131, v133 op_sel:[0,0,1]
	v_cvt_pk_fp8_f32 v15, v135, v137 op_sel:[0,0,1]
	v_cvt_pk_fp8_f32 v16, v139, v141 op_sel:[0,0,1]
	v_cvt_pk_fp8_f32 v17, v143, v145 op_sel:[0,0,1]
	v_lshl_add_u64 v[146:147], v[148:149], 0, v[146:147]
	global_store_dwordx4 v[38:39], v[2:5], off
	global_store_dwordx4 v[150:151], v[6:9], off
	global_store_dwordx4 v[152:153], v[10:13], off
	global_store_dwordx4 v[146:147], v[14:17], off
	v_add_u32_e32 v33, s3, v33
	s_waitcnt lgkmcnt(0)
	v_cmp_lt_i32_e64 s[6:7], s66, v33
	v_add_u32_e32 v30, s23, v30
	s_or_b64 s[18:19], s[6:7], s[18:19]
	v_add_u32_e32 v32, s67, v32
	s_andn2_b64 exec, exec, s[18:19]
	s_cbranch_execnz .LBB0_10
	s_or_b64 exec, exec, s[18:19]
	s_bitset1_b32 s14, 7
	v_lshl_add_u64 v[28:29], s[16:17], 2, v[24:25]
	s_mov_b64 s[16:17], 0
	v_mov_b32_e32 v86, v74
	v_mov_b32_e32 v30, v1
	v_mov_b32_e32 v87, v69
.LBB0_12:
	v_ashrrev_i32_e32 v32, 31, v87
	v_lshrrev_b32_e32 v32, 28, v32
	v_add_u32_e32 v32, v87, v32
	v_ashrrev_i32_e32 v33, 4, v32
	v_ashrrev_i32_e32 v32, 6, v32
	v_lshlrev_b32_e32 v34, 5, v33
	v_mad_u64_u32 v[36:37], s[0:1], v33, s25, v[30:31]
	v_lshlrev_b32_e32 v38, 11, v33
	v_ashrrev_i32_e32 v33, 31, v32
	v_ashrrev_i32_e32 v35, 31, v34
	v_ashrrev_i32_e32 v37, 31, v36
	v_lshlrev_b64 v[32:33], 8, v[32:33]
	v_lshl_add_u64 v[88:89], v[34:35], 2, v[28:29]
	v_lshl_add_u64 v[152:153], s[14:15], 0, v[32:33]
	v_lshl_add_u64 v[32:33], v[36:37], 2, v[88:89]
	v_and_or_b32 v154, v34, s24, v152
	v_add_co_u32_e64 v34, s[0:1], s26, v32
	global_load_dwordx4 v[88:91], v[32:33], off nt
	s_nop 0
	v_addc_co_u32_e64 v35, s[0:1], 0, v33, s[0:1]
	v_add_co_u32_e64 v36, s[0:1], s27, v32
	v_mov_b32_e32 v2, 0
	s_nop 0
	v_addc_co_u32_e64 v37, s[0:1], 0, v33, s[0:1]
	v_add_co_u32_e64 v100, s[0:1], s28, v32
	v_mov_b32_e32 v3, 0
	s_nop 0
	v_addc_co_u32_e64 v101, s[0:1], 0, v33, s[0:1]
	v_add_co_u32_e64 v104, s[0:1], s22, v32
	v_mov_b32_e32 v4, 0
	s_nop 0
	v_addc_co_u32_e64 v105, s[0:1], 0, v33, s[0:1]
	v_add_co_u32_e64 v108, s[0:1], s29, v32
	v_mov_b32_e32 v5, 0
	s_nop 0
	v_addc_co_u32_e64 v109, s[0:1], 0, v33, s[0:1]
	v_add_co_u32_e64 v112, s[0:1], s30, v32
	v_mov_b32_e32 v6, 0
	s_nop 0
	v_addc_co_u32_e64 v113, s[0:1], 0, v33, s[0:1]
	v_add_co_u32_e64 v116, s[0:1], s31, v32
	v_mov_b32_e32 v7, 0
	s_nop 0
	v_addc_co_u32_e64 v117, s[0:1], 0, v33, s[0:1]
	v_add_co_u32_e64 v120, s[0:1], s33, v32
	v_mov_b32_e32 v8, 0
	s_nop 0
	v_addc_co_u32_e64 v121, s[0:1], 0, v33, s[0:1]
	v_add_co_u32_e64 v124, s[0:1], s34, v32
	v_mov_b32_e32 v9, 0
	s_nop 0
	v_addc_co_u32_e64 v125, s[0:1], 0, v33, s[0:1]
	v_add_co_u32_e64 v128, s[0:1], s35, v32
	v_mov_b32_e32 v10, 0
	s_nop 0
	v_addc_co_u32_e64 v129, s[0:1], 0, v33, s[0:1]
	v_add_co_u32_e64 v132, s[0:1], s60, v32
	v_mov_b32_e32 v11, 0
	s_nop 0
	v_addc_co_u32_e64 v133, s[0:1], 0, v33, s[0:1]
	v_add_co_u32_e64 v136, s[0:1], s61, v32
	v_mov_b32_e32 v12, 0
	s_nop 0
	v_addc_co_u32_e64 v137, s[0:1], 0, v33, s[0:1]
	v_add_co_u32_e64 v140, s[0:1], s62, v32
	v_mov_b32_e32 v13, 0
	s_nop 0
	v_addc_co_u32_e64 v141, s[0:1], 0, v33, s[0:1]
	v_add_co_u32_e64 v144, s[0:1], s63, v32
	v_mov_b32_e32 v14, 0
	s_nop 0
	v_addc_co_u32_e64 v145, s[0:1], 0, v33, s[0:1]
	v_add_co_u32_e64 v32, s[0:1], s64, v32
	v_mov_b32_e32 v15, 0
	s_nop 0
	v_addc_co_u32_e64 v33, s[0:1], 0, v33, s[0:1]
	global_load_dwordx4 v[92:95], v[34:35], off nt
	global_load_dwordx4 v[96:99], v[36:37], off nt
	s_nop 0
	global_load_dwordx4 v[100:103], v[100:101], off nt
	s_nop 0
	global_load_dwordx4 v[104:107], v[104:105], off nt
	s_nop 0
	global_load_dwordx4 v[108:111], v[108:109], off nt
	s_nop 0
	global_load_dwordx4 v[112:115], v[112:113], off nt
	s_nop 0
	global_load_dwordx4 v[116:119], v[116:117], off nt
	s_nop 0
	global_load_dwordx4 v[120:123], v[120:121], off nt
	s_nop 0
	global_load_dwordx4 v[124:127], v[124:125], off nt
	s_nop 0
	global_load_dwordx4 v[128:131], v[128:129], off nt
	s_nop 0
	global_load_dwordx4 v[132:135], v[132:133], off nt
	s_nop 0
	global_load_dwordx4 v[136:139], v[136:137], off nt
	s_nop 0
	global_load_dwordx4 v[140:143], v[140:141], off nt
	s_nop 0
	global_load_dwordx4 v[144:147], v[144:145], off nt
	s_nop 0
	global_load_dwordx4 v[148:151], v[32:33], off nt
	v_mov_b32_e32 v16, 0
	v_mov_b32_e32 v17, 0
	v_or_b32_e32 v152, v154, v66
	v_sub_u32_e32 v38, v86, v38
	v_lshlrev_b64 v[32:33], 11, v[152:153]
	v_or_b32_e32 v152, v154, v68
	v_ashrrev_i32_e32 v39, 31, v38
	v_lshlrev_b64 v[34:35], 11, v[152:153]
	v_or_b32_e32 v152, v154, v70
	v_lshl_add_u64 v[38:39], v[18:19], 0, v[38:39]
	v_lshlrev_b64 v[36:37], 11, v[152:153]
	v_or_b32_e32 v152, v154, v72
	v_lshl_add_u64 v[32:33], v[38:39], 0, v[32:33]
	v_lshlrev_b64 v[152:153], 11, v[152:153]
	v_lshl_add_u64 v[34:35], v[38:39], 0, v[34:35]
	v_lshl_add_u64 v[36:37], v[38:39], 0, v[36:37]
	v_lshl_add_u64 v[38:39], v[38:39], 0, v[152:153]
	v_add_u32_e32 v87, s3, v87
	v_cmp_lt_i32_e64 s[6:7], s66, v87
	v_add_u32_e32 v30, s23, v30
	s_or_b64 s[16:17], s[6:7], s[16:17]
	v_add_u32_e32 v86, s67, v86
	s_waitcnt vmcnt(15)
	ds_write2_b32 v40, v88, v89 offset1:1
	ds_write2_b32 v40, v90, v91 offset0:2 offset1:3
	s_waitcnt vmcnt(14)
	ds_write2_b32 v41, v92, v93 offset1:1
	ds_write2_b32 v42, v94, v95 offset1:1
	s_waitcnt vmcnt(13)
	ds_write2_b32 v43, v96, v97 offset1:1
	ds_write2_b32 v44, v98, v99 offset1:1
	s_waitcnt vmcnt(12)
	ds_write2_b32 v45, v100, v101 offset1:1
	ds_write2_b32 v46, v102, v103 offset1:1
	s_waitcnt vmcnt(11)
	ds_write2_b32 v47, v104, v105 offset1:1
	ds_write2_b32 v48, v106, v107 offset1:1
	s_waitcnt vmcnt(10)
	ds_write2_b32 v49, v108, v109 offset1:1
	ds_write2_b32 v50, v110, v111 offset1:1
	s_waitcnt vmcnt(9)
	ds_write2_b32 v51, v112, v113 offset1:1
	ds_write2_b32 v52, v114, v115 offset1:1
	s_waitcnt vmcnt(8)
	ds_write2_b32 v53, v116, v117 offset1:1
	ds_write2_b32 v54, v118, v119 offset1:1
	s_waitcnt vmcnt(7)
	ds_write2_b32 v55, v120, v121 offset1:1
	ds_write2_b32 v56, v122, v123 offset1:1
	s_waitcnt vmcnt(6)
	ds_write2_b32 v57, v124, v125 offset1:1
	ds_write2_b32 v58, v126, v127 offset1:1
	s_waitcnt vmcnt(5)
	ds_write2_b32 v59, v128, v129 offset1:1
	ds_write2_b32 v60, v130, v131 offset1:1
	s_waitcnt vmcnt(4)
	ds_write2_b32 v61, v132, v133 offset1:1
	ds_write2_b32 v62, v134, v135 offset1:1
	s_waitcnt vmcnt(3)
	ds_write2_b32 v63, v136, v137 offset1:1
	ds_write2_b32 v64, v138, v139 offset1:1
	s_waitcnt vmcnt(2)
	ds_write2_b32 v71, v140, v141 offset1:1
	ds_write2_b32 v73, v142, v143 offset1:1
	s_waitcnt vmcnt(1)
	ds_write2_b32 v76, v144, v145 offset1:1
	ds_write2_b32 v77, v146, v147 offset1:1
	s_waitcnt vmcnt(0)
	ds_write2_b32 v82, v148, v149 offset1:1
	ds_write2_b32 v83, v150, v151 offset1:1
	s_waitcnt lgkmcnt(0)
	ds_read2_b32 v[88:89], v75 offset1:8
	ds_read2_b32 v[90:91], v75 offset0:33 offset1:41
	ds_read2_b32 v[92:93], v75 offset0:66 offset1:74
	ds_read2_b32 v[94:95], v75 offset0:99 offset1:107
	ds_read2_b32 v[96:97], v75 offset0:132 offset1:140
	ds_read2_b32 v[98:99], v75 offset0:165 offset1:173
	ds_read2_b32 v[100:101], v84 offset0:8 offset1:16
	ds_read2_b32 v[102:103], v84 offset0:41 offset1:49
	ds_read2_b32 v[104:105], v84 offset0:140 offset1:148
	ds_read2_b32 v[106:107], v84 offset0:173 offset1:181
	ds_read2_b32 v[108:109], v75 offset0:16 offset1:24
	ds_read2_b32 v[110:111], v75 offset0:49 offset1:57
	ds_read2_b32 v[112:113], v75 offset0:148 offset1:156
	ds_read2_b32 v[114:115], v75 offset0:181 offset1:189
	ds_read2_b32 v[116:117], v84 offset0:24 offset1:32
	ds_read2_b32 v[118:119], v84 offset0:57 offset1:65
	ds_read2_b32 v[120:121], v84 offset0:156 offset1:164
	ds_read2_b32 v[122:123], v84 offset0:189 offset1:197
	ds_read2_b32 v[124:125], v75 offset0:198 offset1:206
	ds_read2_b32 v[126:127], v75 offset0:231 offset1:239
	ds_read2_b32 v[128:129], v84 offset0:74 offset1:82
	ds_read2_b32 v[130:131], v84 offset0:107 offset1:115
	ds_read2_b32 v[132:133], v84 offset0:206 offset1:214
	ds_read2_b32 v[134:135], v84 offset0:239 offset1:247
	ds_read2_b32 v[136:137], v75 offset0:82 offset1:90
	ds_read2_b32 v[138:139], v75 offset0:115 offset1:123
	ds_read2_b32 v[140:141], v75 offset0:214 offset1:222
	ds_read2_b32 v[142:143], v75 offset0:247 offset1:255
	ds_read2_b32 v[144:145], v84 offset0:90 offset1:98
	ds_read2_b32 v[146:147], v84 offset0:123 offset1:131
	ds_read2_b32 v[148:149], v84 offset0:222 offset1:230
	ds_read2_b32 v[150:151], v85 offset0:127 offset1:135
	s_waitcnt lgkmcnt(14)
	v_mul_f32_e32 v88, 0x43800000, v88
	v_mul_f32_e32 v90, 0x43800000, v90
	v_mul_f32_e32 v96, 0x43800000, v96
	v_mul_f32_e32 v98, 0x43800000, v98
	v_mul_f32_e32 v100, 0x43800000, v100
	v_mul_f32_e32 v102, 0x43800000, v102
	v_mul_f32_e32 v104, 0x43800000, v104
	v_mul_f32_e32 v106, 0x43800000, v106
	v_mul_f32_e32 v89, 0x43800000, v89
	v_mul_f32_e32 v91, 0x43800000, v91
	v_mul_f32_e32 v97, 0x43800000, v97
	v_mul_f32_e32 v99, 0x43800000, v99
	v_mul_f32_e32 v101, 0x43800000, v101
	v_mul_f32_e32 v103, 0x43800000, v103
	v_mul_f32_e32 v105, 0x43800000, v105
	v_mul_f32_e32 v107, 0x43800000, v107
	v_med3_f32 v88, v88, s65, v65
	v_med3_f32 v90, v90, s65, v65
	v_med3_f32 v96, v96, s65, v65
	v_med3_f32 v98, v98, s65, v65
	v_med3_f32 v100, v100, s65, v65
	v_med3_f32 v102, v102, s65, v65
	v_med3_f32 v104, v104, s65, v65
	v_med3_f32 v106, v106, s65, v65
	v_mul_f32_e32 v108, 0x43800000, v108
	v_mul_f32_e32 v110, 0x43800000, v110
	v_mul_f32_e32 v112, 0x43800000, v112
	v_mul_f32_e32 v114, 0x43800000, v114
	v_mul_f32_e32 v116, 0x43800000, v116
	v_mul_f32_e32 v118, 0x43800000, v118
	v_mul_f32_e32 v120, 0x43800000, v120
	v_mul_f32_e32 v122, 0x43800000, v122
	v_med3_f32 v89, v89, s65, v65
	v_med3_f32 v91, v91, s65, v65
	v_med3_f32 v97, v97, s65, v65
	v_med3_f32 v99, v99, s65, v65
	v_med3_f32 v101, v101, s65, v65
	v_med3_f32 v103, v103, s65, v65
	v_med3_f32 v105, v105, s65, v65
	v_med3_f32 v107, v107, s65, v65
	v_cvt_pk_fp8_f32 v2, v88, v90
	v_cvt_pk_fp8_f32 v3, v96, v98
	v_cvt_pk_fp8_f32 v4, v100, v102
	v_cvt_pk_fp8_f32 v5, v104, v106
	v_mul_f32_e32 v109, 0x43800000, v109
	v_mul_f32_e32 v111, 0x43800000, v111
	v_mul_f32_e32 v113, 0x43800000, v113
	v_mul_f32_e32 v115, 0x43800000, v115
	v_mul_f32_e32 v117, 0x43800000, v117
	v_mul_f32_e32 v119, 0x43800000, v119
	v_mul_f32_e32 v121, 0x43800000, v121
	v_mul_f32_e32 v123, 0x43800000, v123
	v_med3_f32 v108, v108, s65, v65
	v_med3_f32 v110, v110, s65, v65
	v_med3_f32 v112, v112, s65, v65
	v_med3_f32 v114, v114, s65, v65
	v_med3_f32 v116, v116, s65, v65
	v_med3_f32 v118, v118, s65, v65
	v_med3_f32 v120, v120, s65, v65
	v_med3_f32 v122, v122, s65, v65
	v_cvt_pk_fp8_f32 v6, v89, v91
	v_cvt_pk_fp8_f32 v7, v97, v99
	v_cvt_pk_fp8_f32 v8, v101, v103
	v_cvt_pk_fp8_f32 v9, v105, v107
	v_mul_f32_e32 v92, 0x43800000, v92
	v_mul_f32_e32 v94, 0x43800000, v94
	s_waitcnt lgkmcnt(13)
	v_mul_f32_e32 v124, 0x43800000, v124
	s_waitcnt lgkmcnt(12)
	v_mul_f32_e32 v126, 0x43800000, v126
	s_waitcnt lgkmcnt(11)
	v_mul_f32_e32 v128, 0x43800000, v128
	s_waitcnt lgkmcnt(10)
	v_mul_f32_e32 v130, 0x43800000, v130
	s_waitcnt lgkmcnt(9)
	v_mul_f32_e32 v132, 0x43800000, v132
	s_waitcnt lgkmcnt(8)
	v_mul_f32_e32 v134, 0x43800000, v134
	v_med3_f32 v109, v109, s65, v65
	v_med3_f32 v111, v111, s65, v65
	v_med3_f32 v113, v113, s65, v65
	v_med3_f32 v115, v115, s65, v65
	v_med3_f32 v117, v117, s65, v65
	v_med3_f32 v119, v119, s65, v65
	v_med3_f32 v121, v121, s65, v65
	v_med3_f32 v123, v123, s65, v65
	v_cvt_pk_fp8_f32 v10, v108, v110
	v_cvt_pk_fp8_f32 v11, v112, v114
	v_cvt_pk_fp8_f32 v12, v116, v118
	v_cvt_pk_fp8_f32 v13, v120, v122
	v_mul_f32_e32 v93, 0x43800000, v93
	v_mul_f32_e32 v95, 0x43800000, v95
	v_mul_f32_e32 v125, 0x43800000, v125
	v_mul_f32_e32 v127, 0x43800000, v127
	v_mul_f32_e32 v129, 0x43800000, v129
	v_mul_f32_e32 v131, 0x43800000, v131
	v_mul_f32_e32 v133, 0x43800000, v133
	v_mul_f32_e32 v135, 0x43800000, v135
	v_med3_f32 v92, v92, s65, v65
	v_med3_f32 v94, v94, s65, v65
	v_med3_f32 v124, v124, s65, v65
	v_med3_f32 v126, v126, s65, v65
	v_med3_f32 v128, v128, s65, v65
	v_med3_f32 v130, v130, s65, v65
	v_med3_f32 v132, v132, s65, v65
	v_med3_f32 v134, v134, s65, v65
	v_cvt_pk_fp8_f32 v14, v109, v111
	v_cvt_pk_fp8_f32 v15, v113, v115
	v_cvt_pk_fp8_f32 v16, v117, v119
	v_cvt_pk_fp8_f32 v17, v121, v123
	s_waitcnt lgkmcnt(7)
	v_mul_f32_e32 v136, 0x43800000, v136
	s_waitcnt lgkmcnt(6)
	v_mul_f32_e32 v138, 0x43800000, v138
	s_waitcnt lgkmcnt(5)
	v_mul_f32_e32 v140, 0x43800000, v140
	s_waitcnt lgkmcnt(4)
	v_mul_f32_e32 v142, 0x43800000, v142
	s_waitcnt lgkmcnt(3)
	v_mul_f32_e32 v144, 0x43800000, v144
	s_waitcnt lgkmcnt(2)
	v_mul_f32_e32 v146, 0x43800000, v146
	s_waitcnt lgkmcnt(1)
	v_mul_f32_e32 v148, 0x43800000, v148
	s_waitcnt lgkmcnt(0)
	v_mul_f32_e32 v150, 0x43800000, v150
	v_med3_f32 v93, v93, s65, v65
	v_med3_f32 v95, v95, s65, v65
	v_med3_f32 v125, v125, s65, v65
	v_med3_f32 v127, v127, s65, v65
	v_med3_f32 v129, v129, s65, v65
	v_med3_f32 v131, v131, s65, v65
	v_med3_f32 v133, v133, s65, v65
	v_med3_f32 v135, v135, s65, v65
	v_cvt_pk_fp8_f32 v2, v92, v94 op_sel:[0,0,1]
	v_cvt_pk_fp8_f32 v3, v124, v126 op_sel:[0,0,1]
	v_cvt_pk_fp8_f32 v4, v128, v130 op_sel:[0,0,1]
	v_cvt_pk_fp8_f32 v5, v132, v134 op_sel:[0,0,1]
	v_mul_f32_e32 v137, 0x43800000, v137
	v_mul_f32_e32 v139, 0x43800000, v139
	v_mul_f32_e32 v141, 0x43800000, v141
	v_mul_f32_e32 v143, 0x43800000, v143
	v_mul_f32_e32 v145, 0x43800000, v145
	v_mul_f32_e32 v147, 0x43800000, v147
	v_mul_f32_e32 v149, 0x43800000, v149
	v_mul_f32_e32 v151, 0x43800000, v151
	v_med3_f32 v136, v136, s65, v65
	v_med3_f32 v138, v138, s65, v65
	v_med3_f32 v140, v140, s65, v65
	v_med3_f32 v142, v142, s65, v65
	v_med3_f32 v144, v144, s65, v65
	v_med3_f32 v146, v146, s65, v65
	v_med3_f32 v148, v148, s65, v65
	v_med3_f32 v150, v150, s65, v65
	v_cvt_pk_fp8_f32 v6, v93, v95 op_sel:[0,0,1]
	v_cvt_pk_fp8_f32 v7, v125, v127 op_sel:[0,0,1]
	v_cvt_pk_fp8_f32 v8, v129, v131 op_sel:[0,0,1]
	v_cvt_pk_fp8_f32 v9, v133, v135 op_sel:[0,0,1]
	v_med3_f32 v137, v137, s65, v65
	v_med3_f32 v139, v139, s65, v65
	v_med3_f32 v141, v141, s65, v65
	v_med3_f32 v143, v143, s65, v65
	v_med3_f32 v145, v145, s65, v65
	v_med3_f32 v147, v147, s65, v65
	v_med3_f32 v149, v149, s65, v65
	v_med3_f32 v151, v151, s65, v65
	v_cvt_pk_fp8_f32 v10, v136, v138 op_sel:[0,0,1]
	v_cvt_pk_fp8_f32 v11, v140, v142 op_sel:[0,0,1]
	v_cvt_pk_fp8_f32 v12, v144, v146 op_sel:[0,0,1]
	v_cvt_pk_fp8_f32 v13, v148, v150 op_sel:[0,0,1]
	v_cvt_pk_fp8_f32 v14, v137, v139 op_sel:[0,0,1]
	v_cvt_pk_fp8_f32 v15, v141, v143 op_sel:[0,0,1]
	v_cvt_pk_fp8_f32 v16, v145, v147 op_sel:[0,0,1]
	v_cvt_pk_fp8_f32 v17, v149, v151 op_sel:[0,0,1]
	global_store_dwordx4 v[32:33], v[2:5], off
	global_store_dwordx4 v[34:35], v[6:9], off
	global_store_dwordx4 v[36:37], v[10:13], off
	global_store_dwordx4 v[38:39], v[14:17], off
	s_waitcnt lgkmcnt(0)
	s_andn2_b64 exec, exec, s[16:17]
	s_cbranch_execnz .LBB0_12
	s_or_b64 exec, exec, s[16:17]
	s_lshl_b64 s[6:7], s[8:9], 11
	v_mad_u64_u32 v[28:29], s[0:1], s8, v67, v[26:27]
	s_mov_b64 s[14:15], 0
	v_mov_b32_e32 v30, v74
	v_mov_b32_e32 v86, v69
.LBB0_14:
	s_mov_b32 s0, 0x92492493
	v_mul_hi_i32 v32, v86, s0
	v_add_u32_e32 v32, v32, v86
	v_lshrrev_b32_e32 v33, 31, v32
	v_ashrrev_i32_e32 v32, 5, v32
	v_add_u32_e32 v33, v32, v33
	s_movk_i32 s0, 0xe400
	v_lshlrev_b32_e32 v32, 5, v33
	v_mad_u64_u32 v[34:35], s[0:1], v33, s0, v[30:31]
	v_ashrrev_i32_e32 v33, 31, v32
	v_add_u32_e32 v36, v34, v66
	v_ashrrev_i32_e32 v35, 31, v34
	v_lshl_add_u64 v[92:93], s[6:7], 0, v[32:33]
	v_lshl_add_u64 v[94:95], v[32:33], 2, v[28:29]
	v_ashrrev_i32_e32 v37, 31, v36
	v_add_u32_e32 v32, 8, v36
	v_add_u32_e32 v38, 16, v36
	v_add_u32_e32 v88, 24, v36
	v_add_u32_e32 v90, 32, v36
	v_add_u32_e32 v96, 40, v36
	v_add_u32_e32 v98, 48, v36
	v_add_u32_e32 v100, 56, v36
	v_add_u32_e32 v102, 64, v36
	v_add_u32_e32 v104, 0x48, v36
	v_add_u32_e32 v106, 0x50, v36
	v_add_u32_e32 v108, 0x58, v36
	v_add_u32_e32 v110, 0x60, v36
	v_add_u32_e32 v112, 0x68, v36
	v_add_u32_e32 v114, 0x70, v36
	v_add_u32_e32 v116, 0x78, v36
	v_lshl_add_u64 v[118:119], v[20:21], 0, v[34:35]
	v_lshlrev_b64 v[34:35], 13, v[36:37]
	v_ashrrev_i32_e32 v33, 31, v32
	v_ashrrev_i32_e32 v39, 31, v38
	v_ashrrev_i32_e32 v89, 31, v88
	v_ashrrev_i32_e32 v91, 31, v90
	v_ashrrev_i32_e32 v97, 31, v96
	v_ashrrev_i32_e32 v99, 31, v98
	v_ashrrev_i32_e32 v101, 31, v100
	v_ashrrev_i32_e32 v103, 31, v102
	v_ashrrev_i32_e32 v105, 31, v104
	v_ashrrev_i32_e32 v107, 31, v106
	v_ashrrev_i32_e32 v109, 31, v108
	v_ashrrev_i32_e32 v111, 31, v110
	v_ashrrev_i32_e32 v113, 31, v112
	v_ashrrev_i32_e32 v115, 31, v114
	v_ashrrev_i32_e32 v117, 31, v116
	v_or_b32_e32 v36, v92, v66
	v_or_b32_e32 v37, v92, v68
	v_or_b32_e32 v87, v92, v70
	v_or_b32_e32 v92, v92, v72
	v_lshl_add_u64 v[120:121], v[94:95], 0, v[34:35]
	v_lshlrev_b64 v[122:123], 13, v[32:33]
	v_lshlrev_b64 v[124:125], 13, v[38:39]
	v_lshlrev_b64 v[126:127], 13, v[88:89]
	v_lshlrev_b64 v[128:129], 13, v[90:91]
	v_lshlrev_b64 v[96:97], 13, v[96:97]
	v_lshlrev_b64 v[98:99], 13, v[98:99]
	v_lshlrev_b64 v[100:101], 13, v[100:101]
	v_lshlrev_b64 v[102:103], 13, v[102:103]
	v_lshlrev_b64 v[104:105], 13, v[104:105]
	v_lshlrev_b64 v[106:107], 13, v[106:107]
	v_lshlrev_b64 v[108:109], 13, v[108:109]
	v_lshlrev_b64 v[110:111], 13, v[110:111]
	v_lshlrev_b64 v[112:113], 13, v[112:113]
	v_lshlrev_b64 v[114:115], 13, v[114:115]
	v_lshlrev_b64 v[116:117], 13, v[116:117]
	v_mad_u64_u32 v[38:39], s[0:1], v36, s21, v[118:119]
	v_mad_u64_u32 v[36:37], s[0:1], v37, s21, v[118:119]
	v_mad_u64_u32 v[34:35], s[0:1], v87, s21, v[118:119]
	v_mad_u64_u32 v[32:33], s[0:1], v92, s21, v[118:119]
	global_load_dwordx4 v[88:91], v[120:121], off nt
	v_lshl_add_u64 v[118:119], v[94:95], 0, v[122:123]
	v_lshl_add_u64 v[120:121], v[94:95], 0, v[124:125]
	v_lshl_add_u64 v[122:123], v[94:95], 0, v[126:127]
	v_lshl_add_u64 v[124:125], v[94:95], 0, v[128:129]
	v_lshl_add_u64 v[126:127], v[94:95], 0, v[96:97]
	v_lshl_add_u64 v[128:129], v[94:95], 0, v[98:99]
	v_lshl_add_u64 v[130:131], v[94:95], 0, v[100:101]
	v_lshl_add_u64 v[132:133], v[94:95], 0, v[102:103]
	v_lshl_add_u64 v[134:135], v[94:95], 0, v[104:105]
	v_lshl_add_u64 v[136:137], v[94:95], 0, v[106:107]
	v_lshl_add_u64 v[138:139], v[94:95], 0, v[108:109]
	v_lshl_add_u64 v[140:141], v[94:95], 0, v[110:111]
	v_lshl_add_u64 v[142:143], v[94:95], 0, v[112:113]
	v_lshl_add_u64 v[144:145], v[94:95], 0, v[114:115]
	v_lshl_add_u64 v[148:149], v[94:95], 0, v[116:117]
	v_mad_i32_i24 v39, v93, s21, v39
	v_mad_i32_i24 v37, v93, s21, v37
	v_mad_i32_i24 v35, v93, s21, v35
	v_mad_i32_i24 v33, v93, s21, v33
	global_load_dwordx4 v[92:95], v[118:119], off nt
	global_load_dwordx4 v[96:99], v[120:121], off nt
	global_load_dwordx4 v[100:103], v[122:123], off nt
	global_load_dwordx4 v[104:107], v[124:125], off nt
	global_load_dwordx4 v[108:111], v[126:127], off nt
	global_load_dwordx4 v[112:115], v[128:129], off nt
	global_load_dwordx4 v[116:119], v[130:131], off nt
	s_nop 0
	global_load_dwordx4 v[120:123], v[132:133], off nt
	global_load_dwordx4 v[124:127], v[134:135], off nt
	global_load_dwordx4 v[128:131], v[136:137], off nt
	s_nop 0
	global_load_dwordx4 v[132:135], v[138:139], off nt
	s_nop 0
	global_load_dwordx4 v[136:139], v[140:141], off nt
	s_nop 0
	global_load_dwordx4 v[140:143], v[142:143], off nt
	s_nop 0
	global_load_dwordx4 v[144:147], v[144:145], off nt
	s_nop 0
	global_load_dwordx4 v[148:151], v[148:149], off nt
	s_waitcnt vmcnt(15)
	ds_write2_b32 v40, v88, v89 offset1:1
	ds_write2_b32 v40, v90, v91 offset0:2 offset1:3
	s_waitcnt vmcnt(14)
	ds_write2_b32 v41, v92, v93 offset1:1
	ds_write2_b32 v42, v94, v95 offset1:1
	s_waitcnt vmcnt(13)
	ds_write2_b32 v43, v96, v97 offset1:1
	ds_write2_b32 v44, v98, v99 offset1:1
	s_waitcnt vmcnt(12)
	ds_write2_b32 v45, v100, v101 offset1:1
	ds_write2_b32 v46, v102, v103 offset1:1
	s_waitcnt vmcnt(11)
	ds_write2_b32 v47, v104, v105 offset1:1
	ds_write2_b32 v48, v106, v107 offset1:1
	s_waitcnt vmcnt(10)
	ds_write2_b32 v49, v108, v109 offset1:1
	ds_write2_b32 v50, v110, v111 offset1:1
	s_waitcnt vmcnt(9)
	ds_write2_b32 v51, v112, v113 offset1:1
	ds_write2_b32 v52, v114, v115 offset1:1
	s_waitcnt vmcnt(8)
	ds_write2_b32 v53, v116, v117 offset1:1
	ds_write2_b32 v54, v118, v119 offset1:1
	s_waitcnt vmcnt(7)
	ds_write2_b32 v55, v120, v121 offset1:1
	ds_write2_b32 v56, v122, v123 offset1:1
	s_waitcnt vmcnt(6)
	ds_write2_b32 v57, v124, v125 offset1:1
	ds_write2_b32 v58, v126, v127 offset1:1
	s_waitcnt vmcnt(5)
	ds_write2_b32 v59, v128, v129 offset1:1
	ds_write2_b32 v60, v130, v131 offset1:1
	s_waitcnt vmcnt(4)
	ds_write2_b32 v61, v132, v133 offset1:1
	ds_write2_b32 v62, v134, v135 offset1:1
	s_waitcnt vmcnt(3)
	ds_write2_b32 v63, v136, v137 offset1:1
	ds_write2_b32 v64, v138, v139 offset1:1
	s_waitcnt vmcnt(2)
	ds_write2_b32 v71, v140, v141 offset1:1
	ds_write2_b32 v73, v142, v143 offset1:1
	s_waitcnt vmcnt(1)
	ds_write2_b32 v76, v144, v145 offset1:1
	ds_write2_b32 v77, v146, v147 offset1:1
	s_waitcnt vmcnt(0)
	ds_write2_b32 v82, v148, v149 offset1:1
	ds_write2_b32 v83, v150, v151 offset1:1
	s_waitcnt lgkmcnt(0)
	ds_read2_b32 v[88:89], v75 offset1:8
	ds_read2_b32 v[90:91], v75 offset0:33 offset1:41
	ds_read2_b32 v[92:93], v75 offset0:66 offset1:74
	ds_read2_b32 v[94:95], v75 offset0:99 offset1:107
	ds_read2_b32 v[96:97], v75 offset0:132 offset1:140
	ds_read2_b32 v[98:99], v75 offset0:165 offset1:173
	ds_read2_b32 v[100:101], v75 offset0:198 offset1:206
	ds_read2_b32 v[102:103], v75 offset0:231 offset1:239
	ds_read2_b32 v[104:105], v84 offset0:8 offset1:16
	ds_read2_b32 v[106:107], v84 offset0:41 offset1:49
	ds_read2_b32 v[108:109], v84 offset0:74 offset1:82
	ds_read2_b32 v[110:111], v84 offset0:107 offset1:115
	ds_read2_b32 v[112:113], v84 offset0:140 offset1:148
	ds_read2_b32 v[114:115], v84 offset0:173 offset1:181
	ds_read2_b32 v[116:117], v84 offset0:206 offset1:214
	ds_read2_b32 v[118:119], v84 offset0:239 offset1:247
	ds_read2_b32 v[120:121], v75 offset0:16 offset1:24
	ds_read2_b32 v[122:123], v75 offset0:49 offset1:57
	ds_read2_b32 v[124:125], v75 offset0:82 offset1:90
	ds_read2_b32 v[126:127], v75 offset0:115 offset1:123
	ds_read2_b32 v[128:129], v75 offset0:148 offset1:156
	ds_read2_b32 v[130:131], v75 offset0:181 offset1:189
	ds_read2_b32 v[132:133], v75 offset0:214 offset1:222
	ds_read2_b32 v[134:135], v75 offset0:247 offset1:255
	ds_read2_b32 v[136:137], v84 offset0:24 offset1:32
	ds_read2_b32 v[138:139], v84 offset0:57 offset1:65
	ds_read2_b32 v[140:141], v84 offset0:90 offset1:98
	ds_read2_b32 v[142:143], v84 offset0:123 offset1:131
	ds_read2_b32 v[144:145], v84 offset0:156 offset1:164
	ds_read2_b32 v[146:147], v84 offset0:189 offset1:197
	ds_read2_b32 v[148:149], v84 offset0:222 offset1:230
	ds_read2_b32 v[150:151], v85 offset0:127 offset1:135
	s_waitcnt lgkmcnt(14)
	v_mul_f32_e32 v87, 0x43800000, v88
	v_mul_f32_e32 v88, 0x43800000, v90
	v_mul_f32_e32 v90, 0x43800000, v92
	v_mul_f32_e32 v92, 0x43800000, v94
	v_mul_f32_e32 v94, 0x43800000, v96
	v_mul_f32_e32 v96, 0x43800000, v98
	v_mul_f32_e32 v98, 0x43800000, v100
	v_mul_f32_e32 v100, 0x43800000, v102
	v_mul_f32_e32 v102, 0x43800000, v104
	v_mul_f32_e32 v104, 0x43800000, v106
	v_mul_f32_e32 v106, 0x43800000, v108
	v_mul_f32_e32 v108, 0x43800000, v110
	v_mul_f32_e32 v110, 0x43800000, v112
	v_mul_f32_e32 v112, 0x43800000, v114
	v_mov_b32_e32 v2, 0
	v_mov_b32_e32 v3, 0
	v_mov_b32_e32 v4, 0
	v_mov_b32_e32 v5, 0
	v_mul_f32_e32 v89, 0x43800000, v89
	v_mul_f32_e32 v91, 0x43800000, v91
	v_mul_f32_e32 v97, 0x43800000, v97
	v_mul_f32_e32 v99, 0x43800000, v99
	v_mul_f32_e32 v105, 0x43800000, v105
	v_mul_f32_e32 v107, 0x43800000, v107
	v_mul_f32_e32 v113, 0x43800000, v113
	v_mul_f32_e32 v115, 0x43800000, v115
	v_med3_f32 v87, v87, s65, v65
	v_med3_f32 v88, v88, s65, v65
	v_med3_f32 v94, v94, s65, v65
	v_med3_f32 v96, v96, s65, v65
	v_med3_f32 v102, v102, s65, v65
	v_med3_f32 v104, v104, s65, v65
	v_med3_f32 v110, v110, s65, v65
	v_med3_f32 v112, v112, s65, v65
	v_mov_b32_e32 v6, 0
	v_mov_b32_e32 v7, 0
	v_mov_b32_e32 v8, 0
	v_mov_b32_e32 v9, 0
	v_mul_f32_e32 v114, 0x43800000, v116
	v_mul_f32_e32 v116, 0x43800000, v118
	v_mul_f32_e32 v118, 0x43800000, v119
	v_mul_f32_e32 v119, 0x43800000, v120
	v_mul_f32_e32 v120, 0x43800000, v122
	s_waitcnt lgkmcnt(13)
	v_mul_f32_e32 v122, 0x43800000, v124
	s_waitcnt lgkmcnt(12)
	v_mul_f32_e32 v124, 0x43800000, v126
	s_waitcnt lgkmcnt(11)
	v_mul_f32_e32 v126, 0x43800000, v128
	s_waitcnt lgkmcnt(10)
	v_mul_f32_e32 v128, 0x43800000, v130
	s_waitcnt lgkmcnt(9)
	v_mul_f32_e32 v130, 0x43800000, v132
	s_waitcnt lgkmcnt(8)
	v_mul_f32_e32 v132, 0x43800000, v134
	s_waitcnt lgkmcnt(7)
	v_mul_f32_e32 v134, 0x43800000, v136
	s_waitcnt lgkmcnt(6)
	v_mul_f32_e32 v136, 0x43800000, v138
	s_waitcnt lgkmcnt(5)
	v_mul_f32_e32 v138, 0x43800000, v140
	s_waitcnt lgkmcnt(4)
	v_mul_f32_e32 v140, 0x43800000, v142
	s_waitcnt lgkmcnt(3)
	v_mul_f32_e32 v142, 0x43800000, v144
	s_waitcnt lgkmcnt(2)
	v_mul_f32_e32 v144, 0x43800000, v146
	v_med3_f32 v89, v89, s65, v65
	v_med3_f32 v91, v91, s65, v65
	v_med3_f32 v97, v97, s65, v65
	v_med3_f32 v99, v99, s65, v65
	v_med3_f32 v105, v105, s65, v65
	v_med3_f32 v107, v107, s65, v65
	v_med3_f32 v113, v113, s65, v65
	v_med3_f32 v115, v115, s65, v65
	v_cvt_pk_fp8_f32 v2, v87, v88
	v_cvt_pk_fp8_f32 v3, v94, v96
	v_cvt_pk_fp8_f32 v4, v102, v104
	v_cvt_pk_fp8_f32 v5, v110, v112
	v_mov_b32_e32 v10, 0
	v_mov_b32_e32 v11, 0
	v_mov_b32_e32 v12, 0
	v_mov_b32_e32 v13, 0
	v_mul_f32_e32 v121, 0x43800000, v121
	v_mul_f32_e32 v123, 0x43800000, v123
	v_mul_f32_e32 v129, 0x43800000, v129
	v_mul_f32_e32 v131, 0x43800000, v131
	v_mul_f32_e32 v137, 0x43800000, v137
	v_mul_f32_e32 v139, 0x43800000, v139
	v_mul_f32_e32 v145, 0x43800000, v145
	v_mul_f32_e32 v147, 0x43800000, v147
	v_med3_f32 v119, v119, s65, v65
	v_med3_f32 v120, v120, s65, v65
	v_med3_f32 v126, v126, s65, v65
	v_med3_f32 v128, v128, s65, v65
	v_med3_f32 v134, v134, s65, v65
	v_med3_f32 v136, v136, s65, v65
	v_med3_f32 v142, v142, s65, v65
	v_med3_f32 v144, v144, s65, v65
	v_cvt_pk_fp8_f32 v6, v89, v91
	v_cvt_pk_fp8_f32 v7, v97, v99
	v_cvt_pk_fp8_f32 v8, v105, v107
	v_cvt_pk_fp8_f32 v9, v113, v115
	v_mov_b32_e32 v14, 0
	v_mov_b32_e32 v15, 0
	v_mov_b32_e32 v16, 0
	v_mov_b32_e32 v17, 0
	v_med3_f32 v121, v121, s65, v65
	v_med3_f32 v123, v123, s65, v65
	v_med3_f32 v129, v129, s65, v65
	v_med3_f32 v131, v131, s65, v65
	v_med3_f32 v137, v137, s65, v65
	v_med3_f32 v139, v139, s65, v65
	v_med3_f32 v145, v145, s65, v65
	v_med3_f32 v147, v147, s65, v65
	v_cvt_pk_fp8_f32 v10, v119, v120
	v_cvt_pk_fp8_f32 v11, v126, v128
	v_cvt_pk_fp8_f32 v12, v134, v136
	v_cvt_pk_fp8_f32 v13, v142, v144
	v_mul_f32_e32 v93, 0x43800000, v93
	v_mul_f32_e32 v95, 0x43800000, v95
	v_mul_f32_e32 v101, 0x43800000, v101
	v_mul_f32_e32 v103, 0x43800000, v103
	v_mul_f32_e32 v109, 0x43800000, v109
	v_mul_f32_e32 v111, 0x43800000, v111
	v_mul_f32_e32 v117, 0x43800000, v117
	v_med3_f32 v90, v90, s65, v65
	v_med3_f32 v92, v92, s65, v65
	v_med3_f32 v98, v98, s65, v65
	v_med3_f32 v100, v100, s65, v65
	v_med3_f32 v106, v106, s65, v65
	v_med3_f32 v108, v108, s65, v65
	v_med3_f32 v114, v114, s65, v65
	v_med3_f32 v116, v116, s65, v65
	v_cvt_pk_fp8_f32 v14, v121, v123
	v_cvt_pk_fp8_f32 v15, v129, v131
	v_cvt_pk_fp8_f32 v16, v137, v139
	v_cvt_pk_fp8_f32 v17, v145, v147
	s_waitcnt lgkmcnt(1)
	v_mul_f32_e32 v146, 0x43800000, v148
	v_mul_f32_e32 v148, 0x43800000, v149
	s_waitcnt lgkmcnt(0)
	v_mul_f32_e32 v149, 0x43800000, v150
	v_med3_f32 v93, v93, s65, v65
	v_med3_f32 v95, v95, s65, v65
	v_med3_f32 v101, v101, s65, v65
	v_med3_f32 v103, v103, s65, v65
	v_med3_f32 v109, v109, s65, v65
	v_med3_f32 v111, v111, s65, v65
	v_med3_f32 v117, v117, s65, v65
	v_med3_f32 v118, v118, s65, v65
	v_cvt_pk_fp8_f32 v2, v90, v92 op_sel:[0,0,1]
	v_cvt_pk_fp8_f32 v3, v98, v100 op_sel:[0,0,1]
	v_cvt_pk_fp8_f32 v4, v106, v108 op_sel:[0,0,1]
	v_cvt_pk_fp8_f32 v5, v114, v116 op_sel:[0,0,1]
	v_mul_f32_e32 v125, 0x43800000, v125
	v_mul_f32_e32 v127, 0x43800000, v127
	v_mul_f32_e32 v133, 0x43800000, v133
	v_mul_f32_e32 v135, 0x43800000, v135
	v_mul_f32_e32 v141, 0x43800000, v141
	v_mul_f32_e32 v143, 0x43800000, v143
	v_mul_f32_e32 v150, 0x43800000, v151
	v_med3_f32 v122, v122, s65, v65
	v_med3_f32 v124, v124, s65, v65
	v_med3_f32 v130, v130, s65, v65
	v_med3_f32 v132, v132, s65, v65
	v_med3_f32 v138, v138, s65, v65
	v_med3_f32 v140, v140, s65, v65
	v_med3_f32 v146, v146, s65, v65
	v_med3_f32 v149, v149, s65, v65
	v_cvt_pk_fp8_f32 v6, v93, v95 op_sel:[0,0,1]
	v_cvt_pk_fp8_f32 v7, v101, v103 op_sel:[0,0,1]
	v_cvt_pk_fp8_f32 v8, v109, v111 op_sel:[0,0,1]
	v_cvt_pk_fp8_f32 v9, v117, v118 op_sel:[0,0,1]
	v_med3_f32 v125, v125, s65, v65
	v_med3_f32 v127, v127, s65, v65
	v_med3_f32 v133, v133, s65, v65
	v_med3_f32 v135, v135, s65, v65
	v_med3_f32 v141, v141, s65, v65
	v_med3_f32 v143, v143, s65, v65
	v_med3_f32 v148, v148, s65, v65
	v_med3_f32 v150, v150, s65, v65
	v_cvt_pk_fp8_f32 v10, v122, v124 op_sel:[0,0,1]
	v_cvt_pk_fp8_f32 v11, v130, v132 op_sel:[0,0,1]
	v_cvt_pk_fp8_f32 v12, v138, v140 op_sel:[0,0,1]
	v_cvt_pk_fp8_f32 v13, v146, v149 op_sel:[0,0,1]
	v_cvt_pk_fp8_f32 v14, v125, v127 op_sel:[0,0,1]
	v_cvt_pk_fp8_f32 v15, v133, v135 op_sel:[0,0,1]
	v_cvt_pk_fp8_f32 v16, v141, v143 op_sel:[0,0,1]
	v_cvt_pk_fp8_f32 v17, v148, v150 op_sel:[0,0,1]
	global_store_dwordx4 v[38:39], v[2:5], off
	global_store_dwordx4 v[36:37], v[6:9], off
	global_store_dwordx4 v[34:35], v[10:13], off
	global_store_dwordx4 v[32:33], v[14:17], off
	v_add_u32_e32 v86, s3, v86
	s_waitcnt lgkmcnt(0)
	v_cmp_lt_i32_e64 s[0:1], s66, v86
	s_or_b64 s[14:15], s[0:1], s[14:15]
	v_add_u32_e32 v30, s67, v30
	s_andn2_b64 exec, exec, s[14:15]
	s_cbranch_execnz .LBB0_14
	s_branch .LBB0_7

.LBB0_18:
	v_ashrrev_i32_e32 v2, 31, v95
	v_lshrrev_b32_e32 v2, 27, v2
	v_add_u32_e32 v2, v95, v2
	v_ashrrev_i32_e32 v2, 5, v2
	v_lshlrev_b32_e32 v96, 6, v2
	v_lshlrev_b32_e32 v97, 11, v2
	v_or_b32_e32 v2, v96, v71
	v_add_u32_e32 v3, v93, v77
	v_sub_u32_e32 v86, v3, v97
	v_ashrrev_i32_e32 v3, 31, v2
	v_cmp_gt_i32_e32 vcc, s15, v2
	v_lshl_add_u64 v[84:85], v[2:3], 2, s[82:83]
	v_mov_b32_e32 v2, 0
	v_mov_b32_e32 v6, 0
	v_mov_b32_e32 v7, 0
	v_mov_b32_e32 v8, 0
	v_mov_b32_e32 v9, 0
	s_and_saveexec_b64 s[12:13], vcc
	s_cbranch_execz .LBB0_20
	v_ashrrev_i32_e32 v87, 31, v86
	v_lshlrev_b64 v[4:5], 13, v[86:87]
	v_lshl_add_u64 v[4:5], v[84:85], 0, v[4:5]
	global_load_dwordx4 v[6:9], v[4:5], off nt
.LBB0_20:
	s_or_b64 exec, exec, s[12:13]
	v_mov_b32_e32 v3, 0
	v_mov_b32_e32 v4, 0
	v_mov_b32_e32 v5, 0
	s_and_saveexec_b64 s[12:13], vcc
	s_cbranch_execz .LBB0_22
	v_add_u32_e32 v2, 4, v86
	v_ashrrev_i32_e32 v3, 31, v2
	v_lshlrev_b64 v[2:3], 13, v[2:3]
	v_lshl_add_u64 v[2:3], v[84:85], 0, v[2:3]
	global_load_dwordx4 v[2:5], v[2:3], off nt
.LBB0_22:
	s_or_b64 exec, exec, s[12:13]
	v_mov_b32_e32 v10, 0
	v_mov_b32_e32 v14, 0
	v_mov_b32_e32 v15, 0
	v_mov_b32_e32 v16, 0
	v_mov_b32_e32 v17, 0
	s_and_saveexec_b64 s[12:13], vcc
	s_cbranch_execz .LBB0_24
	v_add_u32_e32 v12, 8, v86
	v_ashrrev_i32_e32 v13, 31, v12
	v_lshlrev_b64 v[12:13], 13, v[12:13]
	v_lshl_add_u64 v[12:13], v[84:85], 0, v[12:13]
	global_load_dwordx4 v[14:17], v[12:13], off nt
.LBB0_24:
	s_or_b64 exec, exec, s[12:13]
	v_mov_b32_e32 v11, 0
	v_mov_b32_e32 v12, 0
	v_mov_b32_e32 v13, 0
	s_and_saveexec_b64 s[12:13], vcc
	s_cbranch_execz .LBB0_26
	v_add_u32_e32 v10, 12, v86
	v_ashrrev_i32_e32 v11, 31, v10
	v_lshlrev_b64 v[10:11], 13, v[10:11]
	v_lshl_add_u64 v[10:11], v[84:85], 0, v[10:11]
	global_load_dwordx4 v[10:13], v[10:11], off nt
.LBB0_26:
	s_or_b64 exec, exec, s[12:13]
	v_mov_b32_e32 v18, 0
	v_mov_b32_e32 v22, 0
	v_mov_b32_e32 v23, 0
	v_mov_b32_e32 v24, 0
	v_mov_b32_e32 v25, 0
	s_and_saveexec_b64 s[12:13], vcc
	s_cbranch_execz .LBB0_28
	v_add_u32_e32 v20, 16, v86
	v_ashrrev_i32_e32 v21, 31, v20
	v_lshlrev_b64 v[20:21], 13, v[20:21]
	v_lshl_add_u64 v[20:21], v[84:85], 0, v[20:21]
	global_load_dwordx4 v[22:25], v[20:21], off nt
.LBB0_28:
	s_or_b64 exec, exec, s[12:13]
	v_mov_b32_e32 v19, 0
	v_mov_b32_e32 v20, 0
	v_mov_b32_e32 v21, 0
	s_and_saveexec_b64 s[12:13], vcc
	s_cbranch_execz .LBB0_30
	v_add_u32_e32 v18, 20, v86
	v_ashrrev_i32_e32 v19, 31, v18
	v_lshlrev_b64 v[18:19], 13, v[18:19]
	v_lshl_add_u64 v[18:19], v[84:85], 0, v[18:19]
	global_load_dwordx4 v[18:21], v[18:19], off nt
.LBB0_30:
	s_or_b64 exec, exec, s[12:13]
	v_mov_b32_e32 v26, 0
	v_mov_b32_e32 v30, 0
	v_mov_b32_e32 v31, 0
	v_mov_b32_e32 v32, 0
	v_mov_b32_e32 v33, 0
	s_and_saveexec_b64 s[12:13], vcc
	s_cbranch_execz .LBB0_32
	v_add_u32_e32 v28, 24, v86
	v_ashrrev_i32_e32 v29, 31, v28
	v_lshlrev_b64 v[28:29], 13, v[28:29]
	v_lshl_add_u64 v[28:29], v[84:85], 0, v[28:29]
	global_load_dwordx4 v[30:33], v[28:29], off nt
.LBB0_32:
	s_or_b64 exec, exec, s[12:13]
	v_mov_b32_e32 v27, 0
	v_mov_b32_e32 v28, 0
	v_mov_b32_e32 v29, 0
	s_and_saveexec_b64 s[12:13], vcc
	s_cbranch_execz .LBB0_34
	v_add_u32_e32 v26, 28, v86
	v_ashrrev_i32_e32 v27, 31, v26
	v_lshlrev_b64 v[26:27], 13, v[26:27]
	v_lshl_add_u64 v[26:27], v[84:85], 0, v[26:27]
	global_load_dwordx4 v[26:29], v[26:27], off nt
.LBB0_34:
	s_or_b64 exec, exec, s[12:13]
	v_mov_b32_e32 v34, 0
	v_mov_b32_e32 v38, 0
	v_mov_b32_e32 v39, 0
	v_mov_b32_e32 v40, 0
	v_mov_b32_e32 v41, 0
	s_and_saveexec_b64 s[12:13], vcc
	s_cbranch_execz .LBB0_36
	v_add_u32_e32 v36, 32, v86
	v_ashrrev_i32_e32 v37, 31, v36
	v_lshlrev_b64 v[36:37], 13, v[36:37]
	v_lshl_add_u64 v[36:37], v[84:85], 0, v[36:37]
	global_load_dwordx4 v[38:41], v[36:37], off nt
.LBB0_36:
	s_or_b64 exec, exec, s[12:13]
	v_mov_b32_e32 v35, 0
	v_mov_b32_e32 v36, 0
	v_mov_b32_e32 v37, 0
	s_and_saveexec_b64 s[12:13], vcc
	s_cbranch_execz .LBB0_38
	v_add_u32_e32 v34, 36, v86
	v_ashrrev_i32_e32 v35, 31, v34
	v_lshlrev_b64 v[34:35], 13, v[34:35]
	v_lshl_add_u64 v[34:35], v[84:85], 0, v[34:35]
	global_load_dwordx4 v[34:37], v[34:35], off nt
.LBB0_38:
	s_or_b64 exec, exec, s[12:13]
	v_mov_b32_e32 v42, 0
	v_mov_b32_e32 v46, 0
	v_mov_b32_e32 v47, 0
	v_mov_b32_e32 v48, 0
	v_mov_b32_e32 v49, 0
	s_and_saveexec_b64 s[12:13], vcc
	s_cbranch_execz .LBB0_40
	v_add_u32_e32 v44, 40, v86
	v_ashrrev_i32_e32 v45, 31, v44
	v_lshlrev_b64 v[44:45], 13, v[44:45]
	v_lshl_add_u64 v[44:45], v[84:85], 0, v[44:45]
	global_load_dwordx4 v[46:49], v[44:45], off nt
.LBB0_40:
	s_or_b64 exec, exec, s[12:13]
	v_mov_b32_e32 v43, 0
	v_mov_b32_e32 v44, 0
	v_mov_b32_e32 v45, 0
	s_and_saveexec_b64 s[12:13], vcc
	s_cbranch_execz .LBB0_42
	v_add_u32_e32 v42, 44, v86
	v_ashrrev_i32_e32 v43, 31, v42
	v_lshlrev_b64 v[42:43], 13, v[42:43]
	v_lshl_add_u64 v[42:43], v[84:85], 0, v[42:43]
	global_load_dwordx4 v[42:45], v[42:43], off nt
.LBB0_42:
	s_or_b64 exec, exec, s[12:13]
	v_mov_b32_e32 v50, 0
	v_mov_b32_e32 v54, 0
	v_mov_b32_e32 v55, 0
	v_mov_b32_e32 v56, 0
	v_mov_b32_e32 v57, 0
	s_and_saveexec_b64 s[12:13], vcc
	s_cbranch_execz .LBB0_44
	v_add_u32_e32 v52, 48, v86
	v_ashrrev_i32_e32 v53, 31, v52
	v_lshlrev_b64 v[52:53], 13, v[52:53]
	v_lshl_add_u64 v[52:53], v[84:85], 0, v[52:53]
	global_load_dwordx4 v[54:57], v[52:53], off nt
.LBB0_44:
	s_or_b64 exec, exec, s[12:13]
	v_mov_b32_e32 v51, 0
	v_mov_b32_e32 v52, 0
	v_mov_b32_e32 v53, 0
	s_and_saveexec_b64 s[12:13], vcc
	s_cbranch_execz .LBB0_46
	v_add_u32_e32 v50, 52, v86
	v_ashrrev_i32_e32 v51, 31, v50
	v_lshlrev_b64 v[50:51], 13, v[50:51]
	v_lshl_add_u64 v[50:51], v[84:85], 0, v[50:51]
	global_load_dwordx4 v[50:53], v[50:51], off nt
.LBB0_46:
	s_or_b64 exec, exec, s[12:13]
	v_mov_b32_e32 v58, 0
	v_mov_b32_e32 v62, 0
	v_mov_b32_e32 v63, 0
	v_mov_b32_e32 v64, 0
	v_mov_b32_e32 v65, 0
	s_and_saveexec_b64 s[12:13], vcc
	s_cbranch_execz .LBB0_48
	v_add_u32_e32 v60, 56, v86
	v_ashrrev_i32_e32 v61, 31, v60
	v_lshlrev_b64 v[60:61], 13, v[60:61]
	v_lshl_add_u64 v[60:61], v[84:85], 0, v[60:61]
	global_load_dwordx4 v[62:65], v[60:61], off nt
.LBB0_48:
	s_or_b64 exec, exec, s[12:13]
	v_mov_b32_e32 v59, 0
	v_mov_b32_e32 v60, 0
	v_mov_b32_e32 v61, 0
	s_and_saveexec_b64 s[12:13], vcc
	s_cbranch_execz .LBB0_17
	v_add_u32_e32 v58, 60, v86
	v_ashrrev_i32_e32 v59, 31, v58
	v_lshlrev_b64 v[58:59], 13, v[58:59]
	v_lshl_add_u64 v[58:59], v[84:85], 0, v[58:59]
	global_load_dwordx4 v[58:61], v[58:59], off nt
	s_branch .LBB0_17

.LBB0_53:
	v_ashrrev_i32_e32 v2, 31, v95
	v_lshrrev_b32_e32 v2, 28, v2
	v_add_u32_e32 v2, v95, v2
	v_ashrrev_i32_e32 v2, 4, v2
	v_lshlrev_b32_e32 v96, 6, v2
	v_lshlrev_b32_e32 v97, 10, v2
	v_or_b32_e32 v2, v96, v71
	v_add_u32_e32 v3, v93, v77
	v_readlane_b32 s60, v239, 18
	v_sub_u32_e32 v84, v3, v97
	v_ashrrev_i32_e32 v3, 31, v2
	v_readlane_b32 s66, v239, 24
	v_readlane_b32 s67, v239, 25
	v_cmp_gt_i32_e32 vcc, s15, v2
	v_mov_b32_e32 v4, 0
	v_lshl_add_u64 v[86:87], v[2:3], 2, s[66:67]
	v_mov_b32_e32 v2, 0
	v_mov_b32_e32 v3, 0
	v_mov_b32_e32 v5, 0
	v_readlane_b32 s61, v239, 19
	v_readlane_b32 s62, v239, 20
	v_readlane_b32 s63, v239, 21
	v_readlane_b32 s64, v239, 22
	v_readlane_b32 s65, v239, 23
	v_readlane_b32 s68, v239, 26
	v_readlane_b32 s69, v239, 27
	v_readlane_b32 s70, v239, 28
	v_readlane_b32 s71, v239, 29
	v_readlane_b32 s72, v239, 30
	v_readlane_b32 s73, v239, 31
	v_readlane_b32 s74, v239, 32
	v_readlane_b32 s75, v239, 33
	s_and_saveexec_b64 s[12:13], vcc
	s_cbranch_execz .LBB0_55
	v_ashrrev_i32_e32 v85, 31, v84
	v_lshlrev_b64 v[2:3], 12, v[84:85]
	v_lshl_add_u64 v[2:3], v[86:87], 0, v[2:3]
	global_load_dwordx4 v[2:5], v[2:3], off nt
.LBB0_55:
	s_or_b64 exec, exec, s[12:13]
	v_mov_b32_e32 v6, 0
	v_mov_b32_e32 v10, 0
	v_mov_b32_e32 v11, 0
	v_mov_b32_e32 v12, 0
	v_mov_b32_e32 v13, 0
	s_and_saveexec_b64 s[12:13], vcc
	s_cbranch_execz .LBB0_57
	v_add_u32_e32 v8, 4, v84
	v_ashrrev_i32_e32 v9, 31, v8
	v_lshlrev_b64 v[8:9], 12, v[8:9]
	v_lshl_add_u64 v[8:9], v[86:87], 0, v[8:9]
	global_load_dwordx4 v[10:13], v[8:9], off nt
.LBB0_57:
	s_or_b64 exec, exec, s[12:13]
	v_mov_b32_e32 v7, 0
	v_mov_b32_e32 v8, 0
	v_mov_b32_e32 v9, 0
	s_and_saveexec_b64 s[12:13], vcc
	s_cbranch_execz .LBB0_59
	v_add_u32_e32 v6, 8, v84
	v_ashrrev_i32_e32 v7, 31, v6
	v_lshlrev_b64 v[6:7], 12, v[6:7]
	v_lshl_add_u64 v[6:7], v[86:87], 0, v[6:7]
	global_load_dwordx4 v[6:9], v[6:7], off nt
.LBB0_59:
	s_or_b64 exec, exec, s[12:13]
	v_mov_b32_e32 v14, 0
	v_mov_b32_e32 v18, 0
	v_mov_b32_e32 v19, 0
	v_mov_b32_e32 v20, 0
	v_mov_b32_e32 v21, 0
	s_and_saveexec_b64 s[12:13], vcc
	s_cbranch_execz .LBB0_61
	v_add_u32_e32 v16, 12, v84
	v_ashrrev_i32_e32 v17, 31, v16
	v_lshlrev_b64 v[16:17], 12, v[16:17]
	v_lshl_add_u64 v[16:17], v[86:87], 0, v[16:17]
	global_load_dwordx4 v[18:21], v[16:17], off nt
.LBB0_61:
	s_or_b64 exec, exec, s[12:13]
	v_mov_b32_e32 v15, 0
	v_mov_b32_e32 v16, 0
	v_mov_b32_e32 v17, 0
	s_and_saveexec_b64 s[12:13], vcc
	s_cbranch_execz .LBB0_63
	v_add_u32_e32 v14, 16, v84
	v_ashrrev_i32_e32 v15, 31, v14
	v_lshlrev_b64 v[14:15], 12, v[14:15]
	v_lshl_add_u64 v[14:15], v[86:87], 0, v[14:15]
	global_load_dwordx4 v[14:17], v[14:15], off nt
.LBB0_63:
	s_or_b64 exec, exec, s[12:13]
	v_mov_b32_e32 v22, 0
	v_mov_b32_e32 v26, 0
	v_mov_b32_e32 v27, 0
	v_mov_b32_e32 v28, 0
	v_mov_b32_e32 v29, 0
	s_and_saveexec_b64 s[12:13], vcc
	s_cbranch_execz .LBB0_65
	v_add_u32_e32 v24, 20, v84
	v_ashrrev_i32_e32 v25, 31, v24
	v_lshlrev_b64 v[24:25], 12, v[24:25]
	v_lshl_add_u64 v[24:25], v[86:87], 0, v[24:25]
	global_load_dwordx4 v[26:29], v[24:25], off nt
.LBB0_65:
	s_or_b64 exec, exec, s[12:13]
	v_mov_b32_e32 v23, 0
	v_mov_b32_e32 v24, 0
	v_mov_b32_e32 v25, 0
	s_and_saveexec_b64 s[12:13], vcc
	s_cbranch_execz .LBB0_67
	v_add_u32_e32 v22, 24, v84
	v_ashrrev_i32_e32 v23, 31, v22
	v_lshlrev_b64 v[22:23], 12, v[22:23]
	v_lshl_add_u64 v[22:23], v[86:87], 0, v[22:23]
	global_load_dwordx4 v[22:25], v[22:23], off nt
.LBB0_67:
	s_or_b64 exec, exec, s[12:13]
	v_mov_b32_e32 v30, 0
	v_mov_b32_e32 v34, 0
	v_mov_b32_e32 v35, 0
	v_mov_b32_e32 v36, 0
	v_mov_b32_e32 v37, 0
	s_and_saveexec_b64 s[12:13], vcc
	s_cbranch_execz .LBB0_69
	v_add_u32_e32 v32, 28, v84
	v_ashrrev_i32_e32 v33, 31, v32
	v_lshlrev_b64 v[32:33], 12, v[32:33]
	v_lshl_add_u64 v[32:33], v[86:87], 0, v[32:33]
	global_load_dwordx4 v[34:37], v[32:33], off nt
.LBB0_69:
	s_or_b64 exec, exec, s[12:13]
	v_mov_b32_e32 v31, 0
	v_mov_b32_e32 v32, 0
	v_mov_b32_e32 v33, 0
	s_and_saveexec_b64 s[12:13], vcc
	s_cbranch_execz .LBB0_71
	v_add_u32_e32 v30, 32, v84
	v_ashrrev_i32_e32 v31, 31, v30
	v_lshlrev_b64 v[30:31], 12, v[30:31]
	v_lshl_add_u64 v[30:31], v[86:87], 0, v[30:31]
	global_load_dwordx4 v[30:33], v[30:31], off nt
.LBB0_71:
	s_or_b64 exec, exec, s[12:13]
	v_mov_b32_e32 v38, 0
	v_mov_b32_e32 v42, 0
	v_mov_b32_e32 v43, 0
	v_mov_b32_e32 v44, 0
	v_mov_b32_e32 v45, 0
	s_and_saveexec_b64 s[12:13], vcc
	s_cbranch_execz .LBB0_73
	v_add_u32_e32 v40, 36, v84
	v_ashrrev_i32_e32 v41, 31, v40
	v_lshlrev_b64 v[40:41], 12, v[40:41]
	v_lshl_add_u64 v[40:41], v[86:87], 0, v[40:41]
	global_load_dwordx4 v[42:45], v[40:41], off nt
.LBB0_73:
	s_or_b64 exec, exec, s[12:13]
	v_mov_b32_e32 v39, 0
	v_mov_b32_e32 v40, 0
	v_mov_b32_e32 v41, 0
	s_and_saveexec_b64 s[12:13], vcc
	s_cbranch_execz .LBB0_75
	v_add_u32_e32 v38, 40, v84
	v_ashrrev_i32_e32 v39, 31, v38
	v_lshlrev_b64 v[38:39], 12, v[38:39]
	v_lshl_add_u64 v[38:39], v[86:87], 0, v[38:39]
	global_load_dwordx4 v[38:41], v[38:39], off nt
.LBB0_75:
	s_or_b64 exec, exec, s[12:13]
	v_mov_b32_e32 v46, 0
	v_mov_b32_e32 v50, 0
	v_mov_b32_e32 v51, 0
	v_mov_b32_e32 v52, 0
	v_mov_b32_e32 v53, 0
	s_and_saveexec_b64 s[12:13], vcc
	s_cbranch_execz .LBB0_77
	v_add_u32_e32 v48, 44, v84
	v_ashrrev_i32_e32 v49, 31, v48
	v_lshlrev_b64 v[48:49], 12, v[48:49]
	v_lshl_add_u64 v[48:49], v[86:87], 0, v[48:49]
	global_load_dwordx4 v[50:53], v[48:49], off nt
.LBB0_77:
	s_or_b64 exec, exec, s[12:13]
	v_mov_b32_e32 v47, 0
	v_mov_b32_e32 v48, 0
	v_mov_b32_e32 v49, 0
	s_and_saveexec_b64 s[12:13], vcc
	s_cbranch_execz .LBB0_79
	v_add_u32_e32 v46, 48, v84
	v_ashrrev_i32_e32 v47, 31, v46
	v_lshlrev_b64 v[46:47], 12, v[46:47]
	v_lshl_add_u64 v[46:47], v[86:87], 0, v[46:47]
	global_load_dwordx4 v[46:49], v[46:47], off nt
.LBB0_79:
	s_or_b64 exec, exec, s[12:13]
	v_mov_b32_e32 v54, 0
	v_mov_b32_e32 v58, 0
	v_mov_b32_e32 v59, 0
	v_mov_b32_e32 v60, 0
	v_mov_b32_e32 v61, 0
	s_and_saveexec_b64 s[12:13], vcc
	s_cbranch_execz .LBB0_81
	v_add_u32_e32 v56, 52, v84
	v_ashrrev_i32_e32 v57, 31, v56
	v_lshlrev_b64 v[56:57], 12, v[56:57]
	v_lshl_add_u64 v[56:57], v[86:87], 0, v[56:57]
	global_load_dwordx4 v[58:61], v[56:57], off nt
.LBB0_81:
	s_or_b64 exec, exec, s[12:13]
	v_mov_b32_e32 v55, 0
	v_mov_b32_e32 v56, 0
	v_mov_b32_e32 v57, 0
	s_and_saveexec_b64 s[12:13], vcc
	s_cbranch_execz .LBB0_83
	v_add_u32_e32 v54, 56, v84
	v_ashrrev_i32_e32 v55, 31, v54
	v_lshlrev_b64 v[54:55], 12, v[54:55]
	v_lshl_add_u64 v[54:55], v[86:87], 0, v[54:55]
	global_load_dwordx4 v[54:57], v[54:55], off nt
.LBB0_83:
	s_or_b64 exec, exec, s[12:13]
	v_mov_b32_e32 v62, 0
	v_mov_b32_e32 v63, 0
	v_mov_b32_e32 v64, 0
	v_mov_b32_e32 v65, 0
	s_and_saveexec_b64 s[12:13], vcc
	s_cbranch_execz .LBB0_52
	v_add_u32_e32 v62, 60, v84
	v_ashrrev_i32_e32 v63, 31, v62
	v_lshlrev_b64 v[62:63], 12, v[62:63]
	v_lshl_add_u64 v[62:63], v[86:87], 0, v[62:63]
	global_load_dwordx4 v[62:65], v[62:63], off nt
	s_branch .LBB0_52

.LBB0_88:
	v_ashrrev_i32_e32 v2, 31, v85
	v_lshrrev_b32_e32 v2, 27, v2
	v_add_u32_e32 v2, v85, v2
	v_ashrrev_i32_e32 v96, 5, v2
	v_lshlrev_b32_e32 v95, 6, v96
	v_or_b32_e32 v2, v95, v71
	v_readlane_b32 s60, v239, 0
	v_ashrrev_i32_e32 v3, 31, v2
	v_readlane_b32 s64, v239, 4
	v_readlane_b32 s65, v239, 5
	v_cmp_gt_i32_e64 s[8:9], s17, v2
	v_mov_b32_e32 v4, 0
	v_lshl_add_u64 v[86:87], v[2:3], 2, s[64:65]
	v_mov_b32_e32 v2, 0
	v_mov_b32_e32 v3, 0
	v_mov_b32_e32 v5, 0
	v_readlane_b32 s61, v239, 1
	v_readlane_b32 s62, v239, 2
	v_readlane_b32 s63, v239, 3
	v_readlane_b32 s66, v239, 6
	v_readlane_b32 s67, v239, 7
	v_readlane_b32 s68, v239, 8
	v_readlane_b32 s69, v239, 9
	v_readlane_b32 s70, v239, 10
	v_readlane_b32 s71, v239, 11
	v_readlane_b32 s72, v239, 12
	v_readlane_b32 s73, v239, 13
	v_readlane_b32 s74, v239, 14
	v_readlane_b32 s75, v239, 15
	s_and_saveexec_b64 s[14:15], s[8:9]
	s_cbranch_execz .LBB0_90
	v_mad_u64_u32 v[2:3], s[22:23], v96, s19, v[84:85]
	v_ashrrev_i32_e32 v3, 31, v2
	v_lshl_add_u64 v[2:3], v[2:3], 2, v[86:87]
	global_load_dwordx4 v[2:5], v[2:3], off nt
.LBB0_90:
	s_or_b64 exec, exec, s[14:15]
	v_mov_b32_e32 v6, 0
	v_mov_b32_e32 v10, 0
	v_mov_b32_e32 v11, 0
	v_mov_b32_e32 v12, 0
	v_mov_b32_e32 v13, 0
	s_and_saveexec_b64 s[14:15], s[8:9]
	s_cbranch_execz .LBB0_92
	v_mad_u64_u32 v[8:9], s[22:23], v96, s19, v[84:85]
	v_ashrrev_i32_e32 v9, 31, v8
	v_lshl_add_u64 v[8:9], v[8:9], 2, v[86:87]
	v_add_co_u32_e32 v8, vcc, 0x14000, v8
	s_nop 1
	v_addc_co_u32_e32 v9, vcc, 0, v9, vcc
	global_load_dwordx4 v[10:13], v[8:9], off offset:256 nt
.LBB0_92:
	s_or_b64 exec, exec, s[14:15]
	v_mov_b32_e32 v7, 0
	v_mov_b32_e32 v8, 0
	v_mov_b32_e32 v9, 0
	s_and_saveexec_b64 s[14:15], s[8:9]
	s_cbranch_execz .LBB0_94
	v_mad_u64_u32 v[6:7], s[22:23], v96, s19, v[84:85]
	v_ashrrev_i32_e32 v7, 31, v6
	v_lshl_add_u64 v[6:7], v[6:7], 2, v[86:87]
	v_add_co_u32_e32 v6, vcc, 0x28000, v6
	s_nop 1
	v_addc_co_u32_e32 v7, vcc, 0, v7, vcc
	global_load_dwordx4 v[6:9], v[6:7], off offset:512 nt
.LBB0_94:
	s_or_b64 exec, exec, s[14:15]
	v_mov_b32_e32 v14, 0
	v_mov_b32_e32 v18, 0
	v_mov_b32_e32 v19, 0
	v_mov_b32_e32 v20, 0
	v_mov_b32_e32 v21, 0
	s_and_saveexec_b64 s[14:15], s[8:9]
	s_cbranch_execz .LBB0_96
	v_mad_u64_u32 v[16:17], s[22:23], v96, s19, v[84:85]
	v_ashrrev_i32_e32 v17, 31, v16
	v_lshl_add_u64 v[16:17], v[16:17], 2, v[86:87]
	v_add_co_u32_e32 v16, vcc, 0x3c000, v16
	s_nop 1
	v_addc_co_u32_e32 v17, vcc, 0, v17, vcc
	global_load_dwordx4 v[18:21], v[16:17], off offset:768 nt
.LBB0_96:
	s_or_b64 exec, exec, s[14:15]
	v_mov_b32_e32 v15, 0
	v_mov_b32_e32 v16, 0
	v_mov_b32_e32 v17, 0
	s_and_saveexec_b64 s[14:15], s[8:9]
	s_cbranch_execz .LBB0_98
	v_mad_u64_u32 v[14:15], s[22:23], v96, s19, v[84:85]
	v_ashrrev_i32_e32 v15, 31, v14
	v_lshl_add_u64 v[14:15], v[14:15], 2, v[86:87]
	v_add_co_u32_e32 v14, vcc, 0x50000, v14
	s_nop 1
	v_addc_co_u32_e32 v15, vcc, 0, v15, vcc
	global_load_dwordx4 v[14:17], v[14:15], off offset:1024 nt
.LBB0_98:
	s_or_b64 exec, exec, s[14:15]
	v_mov_b32_e32 v22, 0
	v_mov_b32_e32 v26, 0
	v_mov_b32_e32 v27, 0
	v_mov_b32_e32 v28, 0
	v_mov_b32_e32 v29, 0
	s_and_saveexec_b64 s[14:15], s[8:9]
	s_cbranch_execz .LBB0_100
	v_mad_u64_u32 v[24:25], s[22:23], v96, s19, v[84:85]
	v_ashrrev_i32_e32 v25, 31, v24
	v_lshl_add_u64 v[24:25], v[24:25], 2, v[86:87]
	v_add_co_u32_e32 v24, vcc, 0x64000, v24
	s_nop 1
	v_addc_co_u32_e32 v25, vcc, 0, v25, vcc
	global_load_dwordx4 v[26:29], v[24:25], off offset:1280 nt
.LBB0_100:
	s_or_b64 exec, exec, s[14:15]
	v_mov_b32_e32 v23, 0
	v_mov_b32_e32 v24, 0
	v_mov_b32_e32 v25, 0
	s_and_saveexec_b64 s[14:15], s[8:9]
	s_cbranch_execz .LBB0_102
	v_mad_u64_u32 v[22:23], s[22:23], v96, s19, v[84:85]
	v_ashrrev_i32_e32 v23, 31, v22
	v_lshl_add_u64 v[22:23], v[22:23], 2, v[86:87]
	v_add_co_u32_e32 v22, vcc, 0x78000, v22
	s_nop 1
	v_addc_co_u32_e32 v23, vcc, 0, v23, vcc
	global_load_dwordx4 v[22:25], v[22:23], off offset:1536 nt
.LBB0_102:
	s_or_b64 exec, exec, s[14:15]
	v_mov_b32_e32 v30, 0
	v_mov_b32_e32 v34, 0
	v_mov_b32_e32 v35, 0
	v_mov_b32_e32 v36, 0
	v_mov_b32_e32 v37, 0
	s_and_saveexec_b64 s[14:15], s[8:9]
	s_cbranch_execz .LBB0_104
	v_mad_u64_u32 v[32:33], s[22:23], v96, s19, v[84:85]
	v_ashrrev_i32_e32 v33, 31, v32
	v_lshl_add_u64 v[32:33], v[32:33], 2, v[86:87]
	v_add_co_u32_e32 v32, vcc, 0x8c000, v32
	s_nop 1
	v_addc_co_u32_e32 v33, vcc, 0, v33, vcc
	global_load_dwordx4 v[34:37], v[32:33], off offset:1792 nt
.LBB0_104:
	s_or_b64 exec, exec, s[14:15]
	v_mov_b32_e32 v31, 0
	v_mov_b32_e32 v32, 0
	v_mov_b32_e32 v33, 0
	s_and_saveexec_b64 s[14:15], s[8:9]
	s_cbranch_execz .LBB0_106
	v_mad_u64_u32 v[30:31], s[22:23], v96, s19, v[84:85]
	v_ashrrev_i32_e32 v31, 31, v30
	v_lshl_add_u64 v[30:31], v[30:31], 2, v[86:87]
	v_add_co_u32_e32 v30, vcc, 0xa0000, v30
	s_nop 1
	v_addc_co_u32_e32 v31, vcc, 0, v31, vcc
	global_load_dwordx4 v[30:33], v[30:31], off offset:2048 nt
.LBB0_106:
	s_or_b64 exec, exec, s[14:15]
	v_mov_b32_e32 v38, 0
	v_mov_b32_e32 v42, 0
	v_mov_b32_e32 v43, 0
	v_mov_b32_e32 v44, 0
	v_mov_b32_e32 v45, 0
	s_and_saveexec_b64 s[14:15], s[8:9]
	s_cbranch_execz .LBB0_108
	v_mad_u64_u32 v[40:41], s[22:23], v96, s19, v[84:85]
	v_ashrrev_i32_e32 v41, 31, v40
	v_lshl_add_u64 v[40:41], v[40:41], 2, v[86:87]
	v_add_co_u32_e32 v40, vcc, 0xb4000, v40
	s_nop 1
	v_addc_co_u32_e32 v41, vcc, 0, v41, vcc
	global_load_dwordx4 v[42:45], v[40:41], off offset:2304 nt
.LBB0_108:
	s_or_b64 exec, exec, s[14:15]
	v_mov_b32_e32 v39, 0
	v_mov_b32_e32 v40, 0
	v_mov_b32_e32 v41, 0
	s_and_saveexec_b64 s[14:15], s[8:9]
	s_cbranch_execz .LBB0_110
	v_mad_u64_u32 v[38:39], s[22:23], v96, s19, v[84:85]
	v_ashrrev_i32_e32 v39, 31, v38
	v_lshl_add_u64 v[38:39], v[38:39], 2, v[86:87]
	v_add_co_u32_e32 v38, vcc, 0xc8000, v38
	s_nop 1
	v_addc_co_u32_e32 v39, vcc, 0, v39, vcc
	global_load_dwordx4 v[38:41], v[38:39], off offset:2560 nt
.LBB0_110:
	s_or_b64 exec, exec, s[14:15]
	v_mov_b32_e32 v46, 0
	v_mov_b32_e32 v50, 0
	v_mov_b32_e32 v51, 0
	v_mov_b32_e32 v52, 0
	v_mov_b32_e32 v53, 0
	s_and_saveexec_b64 s[14:15], s[8:9]
	s_cbranch_execz .LBB0_112
	v_mad_u64_u32 v[48:49], s[22:23], v96, s19, v[84:85]
	v_ashrrev_i32_e32 v49, 31, v48
	v_lshl_add_u64 v[48:49], v[48:49], 2, v[86:87]
	v_add_co_u32_e32 v48, vcc, 0xdc000, v48
	s_nop 1
	v_addc_co_u32_e32 v49, vcc, 0, v49, vcc
	global_load_dwordx4 v[50:53], v[48:49], off offset:2816 nt
.LBB0_112:
	s_or_b64 exec, exec, s[14:15]
	v_mov_b32_e32 v47, 0
	v_mov_b32_e32 v48, 0
	v_mov_b32_e32 v49, 0
	s_and_saveexec_b64 s[14:15], s[8:9]
	s_cbranch_execz .LBB0_114
	v_mad_u64_u32 v[46:47], s[22:23], v96, s19, v[84:85]
	v_ashrrev_i32_e32 v47, 31, v46
	v_lshl_add_u64 v[46:47], v[46:47], 2, v[86:87]
	v_add_co_u32_e32 v46, vcc, 0xf0000, v46
	s_nop 1
	v_addc_co_u32_e32 v47, vcc, 0, v47, vcc
	global_load_dwordx4 v[46:49], v[46:47], off offset:3072 nt
.LBB0_114:
	s_or_b64 exec, exec, s[14:15]
	v_mov_b32_e32 v54, 0
	v_mov_b32_e32 v58, 0
	v_mov_b32_e32 v59, 0
	v_mov_b32_e32 v60, 0
	v_mov_b32_e32 v61, 0
	s_and_saveexec_b64 s[14:15], s[8:9]
	s_cbranch_execz .LBB0_116
	v_mad_u64_u32 v[56:57], s[22:23], v96, s19, v[84:85]
	v_ashrrev_i32_e32 v57, 31, v56
	v_lshl_add_u64 v[56:57], v[56:57], 2, v[86:87]
	v_add_co_u32_e32 v56, vcc, 0x104000, v56
	s_nop 1
	v_addc_co_u32_e32 v57, vcc, 0, v57, vcc
	global_load_dwordx4 v[58:61], v[56:57], off offset:3328 nt
.LBB0_116:
	s_or_b64 exec, exec, s[14:15]
	v_mov_b32_e32 v55, 0
	v_mov_b32_e32 v56, 0
	v_mov_b32_e32 v57, 0
	s_and_saveexec_b64 s[14:15], s[8:9]
	s_cbranch_execz .LBB0_118
	v_mad_u64_u32 v[54:55], s[22:23], v96, s19, v[84:85]
	v_ashrrev_i32_e32 v55, 31, v54
	v_lshl_add_u64 v[54:55], v[54:55], 2, v[86:87]
	v_add_co_u32_e32 v54, vcc, 0x118000, v54
	s_nop 1
	v_addc_co_u32_e32 v55, vcc, 0, v55, vcc
	global_load_dwordx4 v[54:57], v[54:55], off offset:3584 nt
.LBB0_118:
	s_or_b64 exec, exec, s[14:15]
	v_mov_b32_e32 v62, 0
	v_mov_b32_e32 v63, 0
	v_mov_b32_e32 v64, 0
	v_mov_b32_e32 v65, 0
	s_and_saveexec_b64 s[14:15], s[8:9]
	s_cbranch_execz .LBB0_87
	v_mad_u64_u32 v[62:63], s[8:9], v96, s19, v[84:85]
	v_ashrrev_i32_e32 v63, 31, v62
	v_lshl_add_u64 v[62:63], v[62:63], 2, v[86:87]
	v_add_co_u32_e32 v62, vcc, 0x12c000, v62
	s_nop 1
	v_addc_co_u32_e32 v63, vcc, 0, v63, vcc
	global_load_dwordx4 v[62:65], v[62:63], off offset:3840 nt
	s_branch .LBB0_87

.LBB0_122:
	v_mul_hi_i32 v22, v64, s13
	v_lshrrev_b32_e32 v23, 31, v22
	v_ashrrev_i32_e32 v22, 3, v22
	v_add_u32_e32 v23, v22, v23
	v_mad_u64_u32 v[24:25], s[18:19], v23, s14, v[74:75]
	v_lshlrev_b32_e32 v22, 5, v23
	v_add_u32_e32 v26, v24, v66
	v_ashrrev_i32_e32 v23, 31, v22
	v_ashrrev_i32_e32 v25, 31, v24
	v_ashrrev_i32_e32 v27, 31, v26
	v_add_u32_e32 v78, 8, v26
	v_add_u32_e32 v80, 16, v26
	v_add_u32_e32 v84, 24, v26
	v_add_u32_e32 v96, 40, v26
	v_add_u32_e32 v98, 48, v26
	v_add_u32_e32 v100, 56, v26
	v_add_u32_e32 v102, 64, v26
	v_add_u32_e32 v104, 0x48, v26
	v_add_u32_e32 v106, 0x50, v26
	v_add_u32_e32 v108, 0x58, v26
	v_add_u32_e32 v110, 0x60, v26
	v_add_u32_e32 v112, 0x68, v26
	v_add_u32_e32 v114, 0x70, v26
	v_add_u32_e32 v116, 0x78, v26
	v_or_b32_e32 v65, v22, v66
	v_or_b32_e32 v77, v22, v68
	v_or_b32_e32 v95, v22, v70
	v_or_b32_e32 v120, v22, v72
	v_lshl_add_u64 v[82:83], v[22:23], 2, v[18:19]
	v_add_u32_e32 v86, 32, v26
	v_lshl_add_u64 v[28:29], v[20:21], 0, v[24:25]
	v_lshlrev_b64 v[118:119], 13, v[26:27]
	v_ashrrev_i32_e32 v79, 31, v78
	v_ashrrev_i32_e32 v81, 31, v80
	v_ashrrev_i32_e32 v85, 31, v84
	v_ashrrev_i32_e32 v97, 31, v96
	v_ashrrev_i32_e32 v99, 31, v98
	v_ashrrev_i32_e32 v101, 31, v100
	v_ashrrev_i32_e32 v103, 31, v102
	v_ashrrev_i32_e32 v105, 31, v104
	v_ashrrev_i32_e32 v107, 31, v106
	v_ashrrev_i32_e32 v109, 31, v108
	v_ashrrev_i32_e32 v111, 31, v110
	v_ashrrev_i32_e32 v113, 31, v112
	v_ashrrev_i32_e32 v115, 31, v114
	v_ashrrev_i32_e32 v117, 31, v116
	v_ashrrev_i32_e32 v87, 31, v86
	v_mad_i64_i32 v[22:23], s[18:19], v65, s16, v[28:29]
	v_mad_i64_i32 v[24:25], s[18:19], v77, s16, v[28:29]
	v_mad_i64_i32 v[26:27], s[18:19], v95, s16, v[28:29]
	v_mad_i64_i32 v[28:29], s[18:19], v120, s16, v[28:29]
	v_lshl_add_u64 v[118:119], v[82:83], 0, v[118:119]
	v_lshlrev_b64 v[120:121], 13, v[78:79]
	v_lshlrev_b64 v[122:123], 13, v[80:81]
	v_lshlrev_b64 v[84:85], 13, v[84:85]
	v_lshlrev_b64 v[96:97], 13, v[96:97]
	v_lshlrev_b64 v[98:99], 13, v[98:99]
	v_lshlrev_b64 v[100:101], 13, v[100:101]
	v_lshlrev_b64 v[102:103], 13, v[102:103]
	v_lshlrev_b64 v[104:105], 13, v[104:105]
	v_lshlrev_b64 v[106:107], 13, v[106:107]
	v_lshlrev_b64 v[108:109], 13, v[108:109]
	v_lshlrev_b64 v[110:111], 13, v[110:111]
	v_lshlrev_b64 v[112:113], 13, v[112:113]
	v_lshlrev_b64 v[114:115], 13, v[114:115]
	v_lshlrev_b64 v[116:117], 13, v[116:117]
	v_lshlrev_b64 v[86:87], 13, v[86:87]
	global_load_dwordx4 v[78:81], v[118:119], off nt
	v_lshl_add_u64 v[118:119], v[82:83], 0, v[120:121]
	v_lshl_add_u64 v[120:121], v[82:83], 0, v[122:123]
	v_lshl_add_u64 v[122:123], v[82:83], 0, v[84:85]
	v_lshl_add_u64 v[124:125], v[82:83], 0, v[96:97]
	v_lshl_add_u64 v[126:127], v[82:83], 0, v[98:99]
	v_lshl_add_u64 v[128:129], v[82:83], 0, v[100:101]
	v_lshl_add_u64 v[130:131], v[82:83], 0, v[102:103]
	v_lshl_add_u64 v[132:133], v[82:83], 0, v[104:105]
	v_lshl_add_u64 v[134:135], v[82:83], 0, v[106:107]
	v_lshl_add_u64 v[136:137], v[82:83], 0, v[108:109]
	v_lshl_add_u64 v[138:139], v[82:83], 0, v[110:111]
	v_lshl_add_u64 v[140:141], v[82:83], 0, v[112:113]
	v_lshl_add_u64 v[144:145], v[82:83], 0, v[114:115]
	v_lshl_add_u64 v[148:149], v[82:83], 0, v[116:117]
	v_lshl_add_u64 v[86:87], v[82:83], 0, v[86:87]
	global_load_dwordx4 v[82:85], v[118:119], off nt
	global_load_dwordx4 v[96:99], v[120:121], off nt
	global_load_dwordx4 v[100:103], v[122:123], off nt
	global_load_dwordx4 v[104:107], v[86:87], off nt
	global_load_dwordx4 v[108:111], v[124:125], off nt
	global_load_dwordx4 v[112:115], v[126:127], off nt
	global_load_dwordx4 v[116:119], v[128:129], off nt
	s_nop 0
	global_load_dwordx4 v[120:123], v[130:131], off nt
	global_load_dwordx4 v[124:127], v[132:133], off nt
	s_nop 0
	global_load_dwordx4 v[128:131], v[134:135], off nt
	s_nop 0
	global_load_dwordx4 v[132:135], v[136:137], off nt
	s_nop 0
	global_load_dwordx4 v[136:139], v[138:139], off nt
	s_nop 0
	global_load_dwordx4 v[140:143], v[140:141], off nt
	s_nop 0
	global_load_dwordx4 v[144:147], v[144:145], off nt
	s_nop 0
	global_load_dwordx4 v[148:151], v[148:149], off nt
	s_waitcnt vmcnt(15)
	ds_write2_b32 v30, v78, v79 offset1:1
	ds_write2_b32 v30, v80, v81 offset0:2 offset1:3
	s_waitcnt vmcnt(14)
	ds_write2_b32 v31, v82, v83 offset1:1
	ds_write2_b32 v32, v84, v85 offset1:1
	s_waitcnt vmcnt(13)
	ds_write2_b32 v33, v96, v97 offset1:1
	ds_write2_b32 v34, v98, v99 offset1:1
	s_waitcnt vmcnt(12)
	ds_write2_b32 v35, v100, v101 offset1:1
	ds_write2_b32 v36, v102, v103 offset1:1
	s_waitcnt vmcnt(11)
	ds_write2_b32 v37, v104, v105 offset1:1
	ds_write2_b32 v38, v106, v107 offset1:1
	s_waitcnt vmcnt(10)
	ds_write2_b32 v39, v108, v109 offset1:1
	ds_write2_b32 v40, v110, v111 offset1:1
	s_waitcnt vmcnt(9)
	ds_write2_b32 v41, v112, v113 offset1:1
	ds_write2_b32 v42, v114, v115 offset1:1
	s_waitcnt vmcnt(8)
	ds_write2_b32 v43, v116, v117 offset1:1
	ds_write2_b32 v44, v118, v119 offset1:1
	s_waitcnt vmcnt(7)
	ds_write2_b32 v45, v120, v121 offset1:1
	ds_write2_b32 v46, v122, v123 offset1:1
	s_waitcnt vmcnt(6)
	ds_write2_b32 v47, v124, v125 offset1:1
	ds_write2_b32 v48, v126, v127 offset1:1
	s_waitcnt vmcnt(5)
	ds_write2_b32 v49, v128, v129 offset1:1
	ds_write2_b32 v50, v130, v131 offset1:1
	s_waitcnt vmcnt(4)
	ds_write2_b32 v51, v132, v133 offset1:1
	ds_write2_b32 v52, v134, v135 offset1:1
	s_waitcnt vmcnt(3)
	ds_write2_b32 v53, v136, v137 offset1:1
	ds_write2_b32 v54, v138, v139 offset1:1
	s_waitcnt vmcnt(2)
	ds_write2_b32 v55, v140, v141 offset1:1
	ds_write2_b32 v56, v142, v143 offset1:1
	s_waitcnt vmcnt(1)
	ds_write2_b32 v57, v144, v145 offset1:1
	ds_write2_b32 v58, v146, v147 offset1:1
	s_waitcnt vmcnt(0)
	ds_write2_b32 v59, v148, v149 offset1:1
	ds_write2_b32 v60, v150, v151 offset1:1
	s_waitcnt lgkmcnt(0)
	ds_read2_b32 v[78:79], v75 offset1:8
	ds_read2_b32 v[80:81], v75 offset0:33 offset1:41
	ds_read2_b32 v[82:83], v75 offset0:66 offset1:74
	ds_read2_b32 v[84:85], v75 offset0:99 offset1:107
	ds_read2_b32 v[86:87], v75 offset0:132 offset1:140
	ds_read2_b32 v[96:97], v75 offset0:165 offset1:173
	ds_read2_b32 v[98:99], v75 offset0:198 offset1:206
	ds_read2_b32 v[100:101], v75 offset0:231 offset1:239
	ds_read2_b32 v[102:103], v62 offset0:8 offset1:16
	ds_read2_b32 v[104:105], v62 offset0:41 offset1:49
	ds_read2_b32 v[106:107], v62 offset0:74 offset1:82
	ds_read2_b32 v[108:109], v62 offset0:107 offset1:115
	ds_read2_b32 v[110:111], v62 offset0:140 offset1:148
	ds_read2_b32 v[112:113], v62 offset0:173 offset1:181
	ds_read2_b32 v[114:115], v62 offset0:206 offset1:214
	ds_read2_b32 v[116:117], v62 offset0:239 offset1:247
	ds_read2_b32 v[118:119], v75 offset0:16 offset1:24
	ds_read2_b32 v[120:121], v75 offset0:49 offset1:57
	ds_read2_b32 v[122:123], v75 offset0:82 offset1:90
	ds_read2_b32 v[124:125], v75 offset0:115 offset1:123
	ds_read2_b32 v[126:127], v75 offset0:148 offset1:156
	ds_read2_b32 v[128:129], v75 offset0:181 offset1:189
	ds_read2_b32 v[130:131], v75 offset0:214 offset1:222
	ds_read2_b32 v[132:133], v75 offset0:247 offset1:255
	ds_read2_b32 v[134:135], v62 offset0:24 offset1:32
	ds_read2_b32 v[136:137], v62 offset0:57 offset1:65
	ds_read2_b32 v[138:139], v62 offset0:90 offset1:98
	ds_read2_b32 v[140:141], v62 offset0:123 offset1:131
	ds_read2_b32 v[142:143], v62 offset0:156 offset1:164
	ds_read2_b32 v[144:145], v62 offset0:189 offset1:197
	ds_read2_b32 v[146:147], v62 offset0:222 offset1:230
	ds_read2_b32 v[148:149], v63 offset0:127 offset1:135
	s_waitcnt lgkmcnt(14)
	v_mul_f32_e32 v65, 0x43800000, v78
	v_mul_f32_e32 v77, 0x43800000, v80
	v_mul_f32_e32 v78, 0x43800000, v82
	v_mul_f32_e32 v80, 0x43800000, v84
	v_mul_f32_e32 v82, 0x43800000, v86
	v_mul_f32_e32 v84, 0x43800000, v96
	v_mul_f32_e32 v86, 0x43800000, v98
	v_mul_f32_e32 v95, 0x43800000, v100
	v_mul_f32_e32 v96, 0x43800000, v102
	v_mul_f32_e32 v98, 0x43800000, v104
	v_mul_f32_e32 v100, 0x43800000, v106
	v_mul_f32_e32 v104, 0x43800000, v110
	v_mul_f32_e32 v106, 0x43800000, v112
	v_mov_b32_e32 v2, 0
	v_mov_b32_e32 v3, 0
	v_mov_b32_e32 v4, 0
	v_mov_b32_e32 v5, 0
	v_mul_f32_e32 v79, 0x43800000, v79
	v_mul_f32_e32 v81, 0x43800000, v81
	v_mul_f32_e32 v87, 0x43800000, v87
	v_mul_f32_e32 v97, 0x43800000, v97
	v_mul_f32_e32 v103, 0x43800000, v103
	v_mul_f32_e32 v105, 0x43800000, v105
	v_mul_f32_e32 v111, 0x43800000, v111
	v_mul_f32_e32 v112, 0x43800000, v113
	v_med3_f32 v65, v65, s15, v61
	v_med3_f32 v77, v77, s15, v61
	v_med3_f32 v82, v82, s15, v61
	v_med3_f32 v84, v84, s15, v61
	v_med3_f32 v96, v96, s15, v61
	v_med3_f32 v98, v98, s15, v61
	v_med3_f32 v104, v104, s15, v61
	v_med3_f32 v106, v106, s15, v61
	v_mov_b32_e32 v6, 0
	v_mov_b32_e32 v7, 0
	v_mov_b32_e32 v8, 0
	v_mov_b32_e32 v9, 0
	v_mul_f32_e32 v102, 0x43800000, v108
	v_mul_f32_e32 v108, 0x43800000, v114
	v_mul_f32_e32 v110, 0x43800000, v116
	v_mul_f32_e32 v113, 0x43800000, v115
	v_mul_f32_e32 v114, 0x43800000, v117
	v_mul_f32_e32 v115, 0x43800000, v118
	v_mul_f32_e32 v116, 0x43800000, v120
	s_waitcnt lgkmcnt(13)
	v_mul_f32_e32 v117, 0x43800000, v122
	s_waitcnt lgkmcnt(12)
	v_mul_f32_e32 v118, 0x43800000, v124
	s_waitcnt lgkmcnt(11)
	v_mul_f32_e32 v120, 0x43800000, v126
	s_waitcnt lgkmcnt(10)
	v_mul_f32_e32 v122, 0x43800000, v128
	s_waitcnt lgkmcnt(9)
	v_mul_f32_e32 v124, 0x43800000, v130
	s_waitcnt lgkmcnt(8)
	v_mul_f32_e32 v126, 0x43800000, v132
	s_waitcnt lgkmcnt(7)
	v_mul_f32_e32 v128, 0x43800000, v134
	s_waitcnt lgkmcnt(6)
	v_mul_f32_e32 v130, 0x43800000, v136
	s_waitcnt lgkmcnt(5)
	v_mul_f32_e32 v132, 0x43800000, v138
	s_waitcnt lgkmcnt(3)
	v_mul_f32_e32 v136, 0x43800000, v142
	s_waitcnt lgkmcnt(2)
	v_mul_f32_e32 v138, 0x43800000, v144
	v_med3_f32 v79, v79, s15, v61
	v_med3_f32 v81, v81, s15, v61
	v_med3_f32 v87, v87, s15, v61
	v_med3_f32 v97, v97, s15, v61
	v_med3_f32 v103, v103, s15, v61
	v_med3_f32 v105, v105, s15, v61
	v_med3_f32 v111, v111, s15, v61
	v_med3_f32 v112, v112, s15, v61
	v_cvt_pk_fp8_f32 v2, v65, v77
	v_cvt_pk_fp8_f32 v3, v82, v84
	v_cvt_pk_fp8_f32 v4, v96, v98
	v_cvt_pk_fp8_f32 v5, v104, v106
	v_mov_b32_e32 v10, 0
	v_mov_b32_e32 v11, 0
	v_mov_b32_e32 v12, 0
	v_mov_b32_e32 v13, 0
	v_mul_f32_e32 v119, 0x43800000, v119
	v_mul_f32_e32 v121, 0x43800000, v121
	v_mul_f32_e32 v127, 0x43800000, v127
	v_mul_f32_e32 v129, 0x43800000, v129
	v_mul_f32_e32 v135, 0x43800000, v135
	v_mul_f32_e32 v137, 0x43800000, v137
	v_mul_f32_e32 v143, 0x43800000, v143
	v_mul_f32_e32 v144, 0x43800000, v145
	v_med3_f32 v115, v115, s15, v61
	v_med3_f32 v116, v116, s15, v61
	v_med3_f32 v120, v120, s15, v61
	v_med3_f32 v122, v122, s15, v61
	v_med3_f32 v128, v128, s15, v61
	v_med3_f32 v130, v130, s15, v61
	v_med3_f32 v136, v136, s15, v61
	v_med3_f32 v138, v138, s15, v61
	v_cvt_pk_fp8_f32 v6, v79, v81
	v_cvt_pk_fp8_f32 v7, v87, v97
	v_cvt_pk_fp8_f32 v8, v103, v105
	v_cvt_pk_fp8_f32 v9, v111, v112
	v_mov_b32_e32 v14, 0
	v_mov_b32_e32 v15, 0
	v_mov_b32_e32 v16, 0
	v_mov_b32_e32 v17, 0
	v_med3_f32 v119, v119, s15, v61
	v_med3_f32 v121, v121, s15, v61
	v_med3_f32 v127, v127, s15, v61
	v_med3_f32 v129, v129, s15, v61
	v_med3_f32 v135, v135, s15, v61
	v_med3_f32 v137, v137, s15, v61
	v_med3_f32 v143, v143, s15, v61
	v_med3_f32 v144, v144, s15, v61
	v_cvt_pk_fp8_f32 v10, v115, v116
	v_cvt_pk_fp8_f32 v11, v120, v122
	v_cvt_pk_fp8_f32 v12, v128, v130
	v_cvt_pk_fp8_f32 v13, v136, v138
	v_mul_f32_e32 v83, 0x43800000, v83
	v_mul_f32_e32 v85, 0x43800000, v85
	v_mul_f32_e32 v99, 0x43800000, v99
	v_mul_f32_e32 v101, 0x43800000, v101
	v_mul_f32_e32 v107, 0x43800000, v107
	v_mul_f32_e32 v109, 0x43800000, v109
	v_med3_f32 v78, v78, s15, v61
	v_med3_f32 v80, v80, s15, v61
	v_med3_f32 v86, v86, s15, v61
	v_med3_f32 v95, v95, s15, v61
	v_med3_f32 v100, v100, s15, v61
	v_med3_f32 v102, v102, s15, v61
	v_med3_f32 v108, v108, s15, v61
	v_med3_f32 v110, v110, s15, v61
	v_cvt_pk_fp8_f32 v14, v119, v121
	v_cvt_pk_fp8_f32 v15, v127, v129
	v_cvt_pk_fp8_f32 v16, v135, v137
	v_cvt_pk_fp8_f32 v17, v143, v144
	v_mul_f32_e32 v134, 0x43800000, v140
	s_waitcnt lgkmcnt(1)
	v_mul_f32_e32 v140, 0x43800000, v146
	s_waitcnt lgkmcnt(0)
	v_mul_f32_e32 v142, 0x43800000, v148
	v_med3_f32 v83, v83, s15, v61
	v_med3_f32 v85, v85, s15, v61
	v_med3_f32 v99, v99, s15, v61
	v_med3_f32 v101, v101, s15, v61
	v_med3_f32 v107, v107, s15, v61
	v_med3_f32 v109, v109, s15, v61
	v_med3_f32 v113, v113, s15, v61
	v_med3_f32 v114, v114, s15, v61
	v_cvt_pk_fp8_f32 v2, v78, v80 op_sel:[0,0,1]
	v_cvt_pk_fp8_f32 v3, v86, v95 op_sel:[0,0,1]
	v_cvt_pk_fp8_f32 v4, v100, v102 op_sel:[0,0,1]
	v_cvt_pk_fp8_f32 v5, v108, v110 op_sel:[0,0,1]
	v_mul_f32_e32 v123, 0x43800000, v123
	v_mul_f32_e32 v125, 0x43800000, v125
	v_mul_f32_e32 v131, 0x43800000, v131
	v_mul_f32_e32 v133, 0x43800000, v133
	v_mul_f32_e32 v139, 0x43800000, v139
	v_mul_f32_e32 v141, 0x43800000, v141
	v_mul_f32_e32 v145, 0x43800000, v147
	v_mul_f32_e32 v146, 0x43800000, v149
	v_med3_f32 v117, v117, s15, v61
	v_med3_f32 v118, v118, s15, v61
	v_med3_f32 v124, v124, s15, v61
	v_med3_f32 v126, v126, s15, v61
	v_med3_f32 v132, v132, s15, v61
	v_med3_f32 v134, v134, s15, v61
	v_med3_f32 v140, v140, s15, v61
	v_med3_f32 v142, v142, s15, v61
	v_cvt_pk_fp8_f32 v6, v83, v85 op_sel:[0,0,1]
	v_cvt_pk_fp8_f32 v7, v99, v101 op_sel:[0,0,1]
	v_cvt_pk_fp8_f32 v8, v107, v109 op_sel:[0,0,1]
	v_cvt_pk_fp8_f32 v9, v113, v114 op_sel:[0,0,1]
	v_med3_f32 v123, v123, s15, v61
	v_med3_f32 v125, v125, s15, v61
	v_med3_f32 v131, v131, s15, v61
	v_med3_f32 v133, v133, s15, v61
	v_med3_f32 v139, v139, s15, v61
	v_med3_f32 v141, v141, s15, v61
	v_med3_f32 v145, v145, s15, v61
	v_med3_f32 v146, v146, s15, v61
	v_cvt_pk_fp8_f32 v10, v117, v118 op_sel:[0,0,1]
	v_cvt_pk_fp8_f32 v11, v124, v126 op_sel:[0,0,1]
	v_cvt_pk_fp8_f32 v12, v132, v134 op_sel:[0,0,1]
	v_cvt_pk_fp8_f32 v13, v140, v142 op_sel:[0,0,1]
	v_cvt_pk_fp8_f32 v14, v123, v125 op_sel:[0,0,1]
	v_cvt_pk_fp8_f32 v15, v131, v133 op_sel:[0,0,1]
	v_cvt_pk_fp8_f32 v16, v139, v141 op_sel:[0,0,1]
	v_cvt_pk_fp8_f32 v17, v145, v146 op_sel:[0,0,1]
	global_store_dwordx4 v[22:23], v[2:5], off
	global_store_dwordx4 v[24:25], v[6:9], off
	global_store_dwordx4 v[26:27], v[10:13], off
	global_store_dwordx4 v[28:29], v[14:17], off
	v_add_u32_e32 v64, s3, v64
	s_waitcnt lgkmcnt(0)
	v_cmp_lt_i32_e32 vcc, s17, v64
	s_or_b64 s[8:9], vcc, s[8:9]
	v_add_u32_e32 v74, s12, v74
	s_andn2_b64 exec, exec, s[8:9]
	s_cbranch_execnz .LBB0_122
	s_or_b64 exec, exec, s[8:9]
	v_mov_b32_e32 v77, 0
	v_lshl_add_u64 v[2:3], s[58:59], 0, v[76:77]
	s_mov_b64 s[8:9], 0x38100000
	v_lshl_or_b32 v77, s96, 9, v94
	v_lshl_add_u64 v[74:75], v[2:3], 0, s[8:9]
	v_or_b32_e32 v2, v77, v93
	s_movk_i32 s18, 0x1600
	v_mul_lo_u32 v78, v2, s18
	s_lshl_b32 s16, s3, 6
	s_mul_i32 s17, s3, 0x58000
	s_mov_b64 s[12:13], 0
	s_mov_b32 s19, 0xff500000
	s_movk_i32 s21, 0xaff
	v_mov_b32_e32 v80, v78
	v_mov_b32_e32 v79, v77
	v_mov_b32_e32 v81, v69
	s_branch .LBB0_125

.LBB0_125:
	v_ashrrev_i32_e32 v2, 31, v81
	v_lshrrev_b32_e32 v2, 27, v2
	v_add_u32_e32 v2, v81, v2
	v_ashrrev_i32_e32 v84, 5, v2
	v_lshlrev_b32_e32 v85, 6, v84
	v_or_b32_e32 v2, v85, v71
	v_ashrrev_i32_e32 v3, 31, v2
	v_cmp_gt_i32_e64 s[8:9], s18, v2
	v_lshl_add_u64 v[82:83], v[2:3], 2, s[46:47]
	v_mov_b32_e32 v2, 0
	v_mov_b32_e32 v3, 0
	v_mov_b32_e32 v4, 0
	v_mov_b32_e32 v5, 0
	s_and_saveexec_b64 s[14:15], s[8:9]
	s_cbranch_execz .LBB0_127
	v_mad_u64_u32 v[2:3], s[22:23], v84, s19, v[80:81]
	v_ashrrev_i32_e32 v3, 31, v2
	v_lshl_add_u64 v[2:3], v[2:3], 2, v[82:83]
	global_load_dwordx4 v[2:5], v[2:3], off nt
.LBB0_127:
	s_or_b64 exec, exec, s[14:15]
	v_mov_b32_e32 v6, 0
	v_mov_b32_e32 v10, 0
	v_mov_b32_e32 v11, 0
	v_mov_b32_e32 v12, 0
	v_mov_b32_e32 v13, 0
	s_and_saveexec_b64 s[14:15], s[8:9]
	s_cbranch_execz .LBB0_129
	v_mad_u64_u32 v[8:9], s[22:23], v84, s19, v[80:81]
	v_ashrrev_i32_e32 v9, 31, v8
	v_lshl_add_u64 v[8:9], v[8:9], 2, v[82:83]
	v_add_co_u32_e32 v8, vcc, 0x16000, v8
	s_nop 1
	v_addc_co_u32_e32 v9, vcc, 0, v9, vcc
	global_load_dwordx4 v[10:13], v[8:9], off nt
.LBB0_129:
	s_or_b64 exec, exec, s[14:15]
	v_mov_b32_e32 v7, 0
	v_mov_b32_e32 v8, 0
	v_mov_b32_e32 v9, 0
	s_and_saveexec_b64 s[14:15], s[8:9]
	s_cbranch_execz .LBB0_131
	v_mad_u64_u32 v[6:7], s[22:23], v84, s19, v[80:81]
	v_ashrrev_i32_e32 v7, 31, v6
	v_lshl_add_u64 v[6:7], v[6:7], 2, v[82:83]
	v_add_co_u32_e32 v6, vcc, 0x2c000, v6
	s_nop 1
	v_addc_co_u32_e32 v7, vcc, 0, v7, vcc
	global_load_dwordx4 v[6:9], v[6:7], off nt
.LBB0_131:
	s_or_b64 exec, exec, s[14:15]
	v_mov_b32_e32 v14, 0
	v_mov_b32_e32 v18, 0
	v_mov_b32_e32 v19, 0
	v_mov_b32_e32 v20, 0
	v_mov_b32_e32 v21, 0
	s_and_saveexec_b64 s[14:15], s[8:9]
	s_cbranch_execz .LBB0_133
	v_mad_u64_u32 v[16:17], s[22:23], v84, s19, v[80:81]
	v_ashrrev_i32_e32 v17, 31, v16
	v_lshl_add_u64 v[16:17], v[16:17], 2, v[82:83]
	v_add_co_u32_e32 v16, vcc, 0x42000, v16
	s_nop 1
	v_addc_co_u32_e32 v17, vcc, 0, v17, vcc
	global_load_dwordx4 v[18:21], v[16:17], off nt
.LBB0_133:
	s_or_b64 exec, exec, s[14:15]
	v_mov_b32_e32 v15, 0
	v_mov_b32_e32 v16, 0
	v_mov_b32_e32 v17, 0
	s_and_saveexec_b64 s[14:15], s[8:9]
	s_cbranch_execz .LBB0_135
	v_mad_u64_u32 v[14:15], s[22:23], v84, s19, v[80:81]
	v_ashrrev_i32_e32 v15, 31, v14
	v_lshl_add_u64 v[14:15], v[14:15], 2, v[82:83]
	v_add_co_u32_e32 v14, vcc, 0x58000, v14
	s_nop 1
	v_addc_co_u32_e32 v15, vcc, 0, v15, vcc
	global_load_dwordx4 v[14:17], v[14:15], off nt
.LBB0_135:
	s_or_b64 exec, exec, s[14:15]
	v_mov_b32_e32 v22, 0
	v_mov_b32_e32 v26, 0
	v_mov_b32_e32 v27, 0
	v_mov_b32_e32 v28, 0
	v_mov_b32_e32 v29, 0
	s_and_saveexec_b64 s[14:15], s[8:9]
	s_cbranch_execz .LBB0_137
	v_mad_u64_u32 v[24:25], s[22:23], v84, s19, v[80:81]
	v_ashrrev_i32_e32 v25, 31, v24
	v_lshl_add_u64 v[24:25], v[24:25], 2, v[82:83]
	v_add_co_u32_e32 v24, vcc, 0x6e000, v24
	s_nop 1
	v_addc_co_u32_e32 v25, vcc, 0, v25, vcc
	global_load_dwordx4 v[26:29], v[24:25], off nt
.LBB0_137:
	s_or_b64 exec, exec, s[14:15]
	v_mov_b32_e32 v23, 0
	v_mov_b32_e32 v24, 0
	v_mov_b32_e32 v25, 0
	s_and_saveexec_b64 s[14:15], s[8:9]
	s_cbranch_execz .LBB0_139
	v_mad_u64_u32 v[22:23], s[22:23], v84, s19, v[80:81]
	v_ashrrev_i32_e32 v23, 31, v22
	v_lshl_add_u64 v[22:23], v[22:23], 2, v[82:83]
	v_add_co_u32_e32 v22, vcc, 0x84000, v22
	s_nop 1
	v_addc_co_u32_e32 v23, vcc, 0, v23, vcc
	global_load_dwordx4 v[22:25], v[22:23], off nt
.LBB0_139:
	s_or_b64 exec, exec, s[14:15]
	v_mov_b32_e32 v30, 0
	v_mov_b32_e32 v34, 0
	v_mov_b32_e32 v35, 0
	v_mov_b32_e32 v36, 0
	v_mov_b32_e32 v37, 0
	s_and_saveexec_b64 s[14:15], s[8:9]
	s_cbranch_execz .LBB0_141
	v_mad_u64_u32 v[32:33], s[22:23], v84, s19, v[80:81]
	v_ashrrev_i32_e32 v33, 31, v32
	v_lshl_add_u64 v[32:33], v[32:33], 2, v[82:83]
	v_add_co_u32_e32 v32, vcc, 0x9a000, v32
	s_nop 1
	v_addc_co_u32_e32 v33, vcc, 0, v33, vcc
	global_load_dwordx4 v[34:37], v[32:33], off nt
.LBB0_141:
	s_or_b64 exec, exec, s[14:15]
	v_mov_b32_e32 v31, 0
	v_mov_b32_e32 v32, 0
	v_mov_b32_e32 v33, 0
	s_and_saveexec_b64 s[14:15], s[8:9]
	s_cbranch_execz .LBB0_143
	v_mad_u64_u32 v[30:31], s[22:23], v84, s19, v[80:81]
	v_ashrrev_i32_e32 v31, 31, v30
	v_lshl_add_u64 v[30:31], v[30:31], 2, v[82:83]
	v_add_co_u32_e32 v30, vcc, 0xb0000, v30
	s_nop 1
	v_addc_co_u32_e32 v31, vcc, 0, v31, vcc
	global_load_dwordx4 v[30:33], v[30:31], off nt
.LBB0_143:
	s_or_b64 exec, exec, s[14:15]
	v_mov_b32_e32 v38, 0
	v_mov_b32_e32 v42, 0
	v_mov_b32_e32 v43, 0
	v_mov_b32_e32 v44, 0
	v_mov_b32_e32 v45, 0
	s_and_saveexec_b64 s[14:15], s[8:9]
	s_cbranch_execz .LBB0_145
	v_mad_u64_u32 v[40:41], s[22:23], v84, s19, v[80:81]
	v_ashrrev_i32_e32 v41, 31, v40
	v_lshl_add_u64 v[40:41], v[40:41], 2, v[82:83]
	v_add_co_u32_e32 v40, vcc, 0xc6000, v40
	s_nop 1
	v_addc_co_u32_e32 v41, vcc, 0, v41, vcc
	global_load_dwordx4 v[42:45], v[40:41], off nt
.LBB0_145:
	s_or_b64 exec, exec, s[14:15]
	v_mov_b32_e32 v39, 0
	v_mov_b32_e32 v40, 0
	v_mov_b32_e32 v41, 0
	s_and_saveexec_b64 s[14:15], s[8:9]
	s_cbranch_execz .LBB0_147
	v_mad_u64_u32 v[38:39], s[22:23], v84, s19, v[80:81]
	v_ashrrev_i32_e32 v39, 31, v38
	v_lshl_add_u64 v[38:39], v[38:39], 2, v[82:83]
	v_add_co_u32_e32 v38, vcc, 0xdc000, v38
	s_nop 1
	v_addc_co_u32_e32 v39, vcc, 0, v39, vcc
	global_load_dwordx4 v[38:41], v[38:39], off nt
.LBB0_147:
	s_or_b64 exec, exec, s[14:15]
	v_mov_b32_e32 v46, 0
	v_mov_b32_e32 v50, 0
	v_mov_b32_e32 v51, 0
	v_mov_b32_e32 v52, 0
	v_mov_b32_e32 v53, 0
	s_and_saveexec_b64 s[14:15], s[8:9]
	s_cbranch_execz .LBB0_149
	v_mad_u64_u32 v[48:49], s[22:23], v84, s19, v[80:81]
	v_ashrrev_i32_e32 v49, 31, v48
	v_lshl_add_u64 v[48:49], v[48:49], 2, v[82:83]
	v_add_co_u32_e32 v48, vcc, 0xf2000, v48
	s_nop 1
	v_addc_co_u32_e32 v49, vcc, 0, v49, vcc
	global_load_dwordx4 v[50:53], v[48:49], off nt
.LBB0_149:
	s_or_b64 exec, exec, s[14:15]
	v_mov_b32_e32 v47, 0
	v_mov_b32_e32 v48, 0
	v_mov_b32_e32 v49, 0
	s_and_saveexec_b64 s[14:15], s[8:9]
	s_cbranch_execz .LBB0_151
	v_mad_u64_u32 v[46:47], s[22:23], v84, s19, v[80:81]
	v_ashrrev_i32_e32 v47, 31, v46
	v_lshl_add_u64 v[46:47], v[46:47], 2, v[82:83]
	v_add_co_u32_e32 v46, vcc, 0x108000, v46
	s_nop 1
	v_addc_co_u32_e32 v47, vcc, 0, v47, vcc
	global_load_dwordx4 v[46:49], v[46:47], off nt
.LBB0_151:
	s_or_b64 exec, exec, s[14:15]
	v_mov_b32_e32 v54, 0
	v_mov_b32_e32 v58, 0
	v_mov_b32_e32 v59, 0
	v_mov_b32_e32 v60, 0
	v_mov_b32_e32 v61, 0
	s_and_saveexec_b64 s[14:15], s[8:9]
	s_cbranch_execz .LBB0_153
	v_mad_u64_u32 v[56:57], s[22:23], v84, s19, v[80:81]
	v_ashrrev_i32_e32 v57, 31, v56
	v_lshl_add_u64 v[56:57], v[56:57], 2, v[82:83]
	v_add_co_u32_e32 v56, vcc, 0x11e000, v56
	s_nop 1
	v_addc_co_u32_e32 v57, vcc, 0, v57, vcc
	global_load_dwordx4 v[58:61], v[56:57], off nt
.LBB0_153:
	s_or_b64 exec, exec, s[14:15]
	v_mov_b32_e32 v55, 0
	v_mov_b32_e32 v56, 0
	v_mov_b32_e32 v57, 0
	s_and_saveexec_b64 s[14:15], s[8:9]
	s_cbranch_execz .LBB0_155
	v_mad_u64_u32 v[54:55], s[22:23], v84, s19, v[80:81]
	v_ashrrev_i32_e32 v55, 31, v54
	v_lshl_add_u64 v[54:55], v[54:55], 2, v[82:83]
	v_add_co_u32_e32 v54, vcc, 0x134000, v54
	s_nop 1
	v_addc_co_u32_e32 v55, vcc, 0, v55, vcc
	global_load_dwordx4 v[54:57], v[54:55], off nt
.LBB0_155:
	s_or_b64 exec, exec, s[14:15]
	v_mov_b32_e32 v62, 0
	v_mov_b32_e32 v63, 0
	v_mov_b32_e32 v64, 0
	v_mov_b32_e32 v65, 0
	s_and_saveexec_b64 s[14:15], s[8:9]
	s_cbranch_execz .LBB0_124
	v_mad_u64_u32 v[62:63], s[8:9], v84, s19, v[80:81]
	v_ashrrev_i32_e32 v63, 31, v62
	v_lshl_add_u64 v[62:63], v[62:63], 2, v[82:83]
	v_add_co_u32_e32 v62, vcc, 0x14a000, v62
	s_nop 1
	v_addc_co_u32_e32 v63, vcc, 0, v63, vcc
	global_load_dwordx4 v[62:65], v[62:63], off nt
	s_branch .LBB0_124

.LBB0_159:
	v_ashrrev_i32_e32 v2, 31, v79
	v_lshrrev_b32_e32 v2, 27, v2
	v_add_u32_e32 v2, v79, v2
	v_ashrrev_i32_e32 v82, 5, v2
	v_lshlrev_b32_e32 v83, 6, v82
	v_or_b32_e32 v2, v83, v71
	v_ashrrev_i32_e32 v3, 31, v2
	v_cmp_gt_i32_e64 s[8:9], s18, v2
	v_lshl_add_u64 v[80:81], v[2:3], 2, s[48:49]
	v_mov_b32_e32 v6, 0
	v_mov_b32_e32 v2, 0
	v_mov_b32_e32 v3, 0
	v_mov_b32_e32 v4, 0
	v_mov_b32_e32 v5, 0
	s_and_saveexec_b64 s[14:15], s[8:9]
	s_cbranch_execz .LBB0_161
	v_mad_u64_u32 v[2:3], s[24:25], v82, s19, v[78:79]
	v_ashrrev_i32_e32 v3, 31, v2
	v_lshl_add_u64 v[2:3], v[2:3], 2, v[80:81]
	global_load_dwordx4 v[2:5], v[2:3], off nt
.LBB0_161:
	s_or_b64 exec, exec, s[14:15]
	v_mov_b32_e32 v7, 0
	v_mov_b32_e32 v8, 0
	v_mov_b32_e32 v9, 0
	s_and_saveexec_b64 s[14:15], s[8:9]
	s_cbranch_execz .LBB0_163
	v_mad_u64_u32 v[6:7], s[24:25], v82, s19, v[78:79]
	v_ashrrev_i32_e32 v7, 31, v6
	v_lshl_add_u64 v[6:7], v[6:7], 2, v[80:81]
	v_add_co_u32_e32 v6, vcc, 0x16000, v6
	s_nop 1
	v_addc_co_u32_e32 v7, vcc, 0, v7, vcc
	global_load_dwordx4 v[6:9], v[6:7], off nt
.LBB0_163:
	s_or_b64 exec, exec, s[14:15]
	v_mov_b32_e32 v10, 0
	v_mov_b32_e32 v14, 0
	v_mov_b32_e32 v15, 0
	v_mov_b32_e32 v16, 0
	v_mov_b32_e32 v17, 0
	s_and_saveexec_b64 s[14:15], s[8:9]
	s_cbranch_execz .LBB0_165
	v_mad_u64_u32 v[12:13], s[24:25], v82, s19, v[78:79]
	v_ashrrev_i32_e32 v13, 31, v12
	v_lshl_add_u64 v[12:13], v[12:13], 2, v[80:81]
	v_add_co_u32_e32 v12, vcc, 0x2c000, v12
	s_nop 1
	v_addc_co_u32_e32 v13, vcc, 0, v13, vcc
	global_load_dwordx4 v[14:17], v[12:13], off nt
.LBB0_165:
	s_or_b64 exec, exec, s[14:15]
	v_mov_b32_e32 v11, 0
	v_mov_b32_e32 v12, 0
	v_mov_b32_e32 v13, 0
	s_and_saveexec_b64 s[14:15], s[8:9]
	s_cbranch_execz .LBB0_167
	v_mad_u64_u32 v[10:11], s[24:25], v82, s19, v[78:79]
	v_ashrrev_i32_e32 v11, 31, v10
	v_lshl_add_u64 v[10:11], v[10:11], 2, v[80:81]
	v_add_co_u32_e32 v10, vcc, 0x42000, v10
	s_nop 1
	v_addc_co_u32_e32 v11, vcc, 0, v11, vcc
	global_load_dwordx4 v[10:13], v[10:11], off nt
.LBB0_167:
	s_or_b64 exec, exec, s[14:15]
	v_mov_b32_e32 v18, 0
	v_mov_b32_e32 v22, 0
	v_mov_b32_e32 v23, 0
	v_mov_b32_e32 v24, 0
	v_mov_b32_e32 v25, 0
	s_and_saveexec_b64 s[14:15], s[8:9]
	s_cbranch_execz .LBB0_169
	v_mad_u64_u32 v[20:21], s[24:25], v82, s19, v[78:79]
	v_ashrrev_i32_e32 v21, 31, v20
	v_lshl_add_u64 v[20:21], v[20:21], 2, v[80:81]
	v_add_co_u32_e32 v20, vcc, 0x58000, v20
	s_nop 1
	v_addc_co_u32_e32 v21, vcc, 0, v21, vcc
	global_load_dwordx4 v[22:25], v[20:21], off nt
.LBB0_169:
	s_or_b64 exec, exec, s[14:15]
	v_mov_b32_e32 v19, 0
	v_mov_b32_e32 v20, 0
	v_mov_b32_e32 v21, 0
	s_and_saveexec_b64 s[14:15], s[8:9]
	s_cbranch_execz .LBB0_171
	v_mad_u64_u32 v[18:19], s[24:25], v82, s19, v[78:79]
	v_ashrrev_i32_e32 v19, 31, v18
	v_lshl_add_u64 v[18:19], v[18:19], 2, v[80:81]
	v_add_co_u32_e32 v18, vcc, 0x6e000, v18
	s_nop 1
	v_addc_co_u32_e32 v19, vcc, 0, v19, vcc
	global_load_dwordx4 v[18:21], v[18:19], off nt
.LBB0_171:
	s_or_b64 exec, exec, s[14:15]
	v_mov_b32_e32 v26, 0
	v_mov_b32_e32 v30, 0
	v_mov_b32_e32 v31, 0
	v_mov_b32_e32 v32, 0
	v_mov_b32_e32 v33, 0
	s_and_saveexec_b64 s[14:15], s[8:9]
	s_cbranch_execz .LBB0_173
	v_mad_u64_u32 v[28:29], s[24:25], v82, s19, v[78:79]
	v_ashrrev_i32_e32 v29, 31, v28
	v_lshl_add_u64 v[28:29], v[28:29], 2, v[80:81]
	v_add_co_u32_e32 v28, vcc, 0x84000, v28
	s_nop 1
	v_addc_co_u32_e32 v29, vcc, 0, v29, vcc
	global_load_dwordx4 v[30:33], v[28:29], off nt
.LBB0_173:
	s_or_b64 exec, exec, s[14:15]
	v_mov_b32_e32 v27, 0
	v_mov_b32_e32 v28, 0
	v_mov_b32_e32 v29, 0
	s_and_saveexec_b64 s[14:15], s[8:9]
	s_cbranch_execz .LBB0_175
	v_mad_u64_u32 v[26:27], s[24:25], v82, s19, v[78:79]
	v_ashrrev_i32_e32 v27, 31, v26
	v_lshl_add_u64 v[26:27], v[26:27], 2, v[80:81]
	v_add_co_u32_e32 v26, vcc, 0x9a000, v26
	s_nop 1
	v_addc_co_u32_e32 v27, vcc, 0, v27, vcc
	global_load_dwordx4 v[26:29], v[26:27], off nt
.LBB0_175:
	s_or_b64 exec, exec, s[14:15]
	v_mov_b32_e32 v34, 0
	v_mov_b32_e32 v38, 0
	v_mov_b32_e32 v39, 0
	v_mov_b32_e32 v40, 0
	v_mov_b32_e32 v41, 0
	s_and_saveexec_b64 s[14:15], s[8:9]
	s_cbranch_execz .LBB0_177
	v_mad_u64_u32 v[36:37], s[24:25], v82, s19, v[78:79]
	v_ashrrev_i32_e32 v37, 31, v36
	v_lshl_add_u64 v[36:37], v[36:37], 2, v[80:81]
	v_add_co_u32_e32 v36, vcc, 0xb0000, v36
	s_nop 1
	v_addc_co_u32_e32 v37, vcc, 0, v37, vcc
	global_load_dwordx4 v[38:41], v[36:37], off nt
.LBB0_177:
	s_or_b64 exec, exec, s[14:15]
	v_mov_b32_e32 v35, 0
	v_mov_b32_e32 v36, 0
	v_mov_b32_e32 v37, 0
	s_and_saveexec_b64 s[14:15], s[8:9]
	s_cbranch_execz .LBB0_179
	v_mad_u64_u32 v[34:35], s[24:25], v82, s19, v[78:79]
	v_ashrrev_i32_e32 v35, 31, v34
	v_lshl_add_u64 v[34:35], v[34:35], 2, v[80:81]
	v_add_co_u32_e32 v34, vcc, 0xc6000, v34
	s_nop 1
	v_addc_co_u32_e32 v35, vcc, 0, v35, vcc
	global_load_dwordx4 v[34:37], v[34:35], off nt
.LBB0_179:
	s_or_b64 exec, exec, s[14:15]
	v_mov_b32_e32 v42, 0
	v_mov_b32_e32 v46, 0
	v_mov_b32_e32 v47, 0
	v_mov_b32_e32 v48, 0
	v_mov_b32_e32 v49, 0
	s_and_saveexec_b64 s[14:15], s[8:9]
	s_cbranch_execz .LBB0_181
	v_mad_u64_u32 v[44:45], s[24:25], v82, s19, v[78:79]
	v_ashrrev_i32_e32 v45, 31, v44
	v_lshl_add_u64 v[44:45], v[44:45], 2, v[80:81]
	v_add_co_u32_e32 v44, vcc, 0xdc000, v44
	s_nop 1
	v_addc_co_u32_e32 v45, vcc, 0, v45, vcc
	global_load_dwordx4 v[46:49], v[44:45], off nt
.LBB0_181:
	s_or_b64 exec, exec, s[14:15]
	v_mov_b32_e32 v43, 0
	v_mov_b32_e32 v44, 0
	v_mov_b32_e32 v45, 0
	s_and_saveexec_b64 s[14:15], s[8:9]
	s_cbranch_execz .LBB0_183
	v_mad_u64_u32 v[42:43], s[24:25], v82, s19, v[78:79]
	v_ashrrev_i32_e32 v43, 31, v42
	v_lshl_add_u64 v[42:43], v[42:43], 2, v[80:81]
	v_add_co_u32_e32 v42, vcc, 0xf2000, v42
	s_nop 1
	v_addc_co_u32_e32 v43, vcc, 0, v43, vcc
	global_load_dwordx4 v[42:45], v[42:43], off nt
.LBB0_183:
	s_or_b64 exec, exec, s[14:15]
	v_mov_b32_e32 v50, 0
	v_mov_b32_e32 v54, 0
	v_mov_b32_e32 v55, 0
	v_mov_b32_e32 v56, 0
	v_mov_b32_e32 v57, 0
	s_and_saveexec_b64 s[14:15], s[8:9]
	s_cbranch_execz .LBB0_185
	v_mad_u64_u32 v[52:53], s[24:25], v82, s19, v[78:79]
	v_ashrrev_i32_e32 v53, 31, v52
	v_lshl_add_u64 v[52:53], v[52:53], 2, v[80:81]
	v_add_co_u32_e32 v52, vcc, 0x108000, v52
	s_nop 1
	v_addc_co_u32_e32 v53, vcc, 0, v53, vcc
	global_load_dwordx4 v[54:57], v[52:53], off nt
.LBB0_185:
	s_or_b64 exec, exec, s[14:15]
	v_mov_b32_e32 v51, 0
	v_mov_b32_e32 v52, 0
	v_mov_b32_e32 v53, 0
	s_and_saveexec_b64 s[14:15], s[8:9]
	s_cbranch_execz .LBB0_187
	v_mad_u64_u32 v[50:51], s[24:25], v82, s19, v[78:79]
	v_ashrrev_i32_e32 v51, 31, v50
	v_lshl_add_u64 v[50:51], v[50:51], 2, v[80:81]
	v_add_co_u32_e32 v50, vcc, 0x11e000, v50
	s_nop 1
	v_addc_co_u32_e32 v51, vcc, 0, v51, vcc
	global_load_dwordx4 v[50:53], v[50:51], off nt
.LBB0_187:
	s_or_b64 exec, exec, s[14:15]
	v_mov_b32_e32 v58, 0
	v_mov_b32_e32 v62, 0
	v_mov_b32_e32 v63, 0
	v_mov_b32_e32 v64, 0
	v_mov_b32_e32 v65, 0
	s_and_saveexec_b64 s[14:15], s[8:9]
	s_cbranch_execz .LBB0_189
	v_mad_u64_u32 v[60:61], s[24:25], v82, s19, v[78:79]
	v_ashrrev_i32_e32 v61, 31, v60
	v_lshl_add_u64 v[60:61], v[60:61], 2, v[80:81]
	v_add_co_u32_e32 v60, vcc, 0x134000, v60
	s_nop 1
	v_addc_co_u32_e32 v61, vcc, 0, v61, vcc
	global_load_dwordx4 v[62:65], v[60:61], off nt
.LBB0_189:
	s_or_b64 exec, exec, s[14:15]
	v_mov_b32_e32 v59, 0
	v_mov_b32_e32 v60, 0
	v_mov_b32_e32 v61, 0
	s_and_saveexec_b64 s[14:15], s[8:9]
	s_cbranch_execz .LBB0_158
	v_mad_u64_u32 v[58:59], s[8:9], v82, s19, v[78:79]
	v_ashrrev_i32_e32 v59, 31, v58
	v_lshl_add_u64 v[58:59], v[58:59], 2, v[80:81]
	v_add_co_u32_e32 v58, vcc, 0x14a000, v58
	s_nop 1
	v_addc_co_u32_e32 v59, vcc, 0, v59, vcc
	global_load_dwordx4 v[58:61], v[58:59], off nt
	s_branch .LBB0_158

.LBB0_194:
	v_ashrrev_i32_e32 v2, 31, v82
	v_lshrrev_b32_e32 v2, 27, v2
	v_add_u32_e32 v2, v82, v2
	v_ashrrev_i32_e32 v2, 5, v2
	v_lshlrev_b32_e32 v83, 6, v2
	v_lshlrev_b32_e32 v84, 11, v2
	v_or_b32_e32 v2, v83, v71
	v_add_u32_e32 v3, v93, v77
	v_sub_u32_e32 v80, v3, v84
	v_ashrrev_i32_e32 v3, 31, v2
	v_cmp_gt_i32_e32 vcc, s13, v2
	v_lshl_add_u64 v[78:79], v[2:3], 2, s[40:41]
	v_mov_b32_e32 v2, 0
	v_mov_b32_e32 v3, 0
	v_mov_b32_e32 v4, 0
	v_mov_b32_e32 v5, 0
	s_and_saveexec_b64 s[8:9], vcc
	s_cbranch_execz .LBB0_196
	v_ashrrev_i32_e32 v81, 31, v80
	v_lshlrev_b64 v[2:3], 13, v[80:81]
	v_lshl_add_u64 v[2:3], v[78:79], 0, v[2:3]
	global_load_dwordx4 v[2:5], v[2:3], off nt
.LBB0_196:
	s_or_b64 exec, exec, s[8:9]
	v_mov_b32_e32 v6, 0
	v_mov_b32_e32 v10, 0
	v_mov_b32_e32 v11, 0
	v_mov_b32_e32 v12, 0
	v_mov_b32_e32 v13, 0
	s_and_saveexec_b64 s[8:9], vcc
	s_cbranch_execz .LBB0_198
	v_add_u32_e32 v8, 4, v80
	v_ashrrev_i32_e32 v9, 31, v8
	v_lshlrev_b64 v[8:9], 13, v[8:9]
	v_lshl_add_u64 v[8:9], v[78:79], 0, v[8:9]
	global_load_dwordx4 v[10:13], v[8:9], off nt
.LBB0_198:
	s_or_b64 exec, exec, s[8:9]
	v_mov_b32_e32 v7, 0
	v_mov_b32_e32 v8, 0
	v_mov_b32_e32 v9, 0
	s_and_saveexec_b64 s[8:9], vcc
	s_cbranch_execz .LBB0_200
	v_add_u32_e32 v6, 8, v80
	v_ashrrev_i32_e32 v7, 31, v6
	v_lshlrev_b64 v[6:7], 13, v[6:7]
	v_lshl_add_u64 v[6:7], v[78:79], 0, v[6:7]
	global_load_dwordx4 v[6:9], v[6:7], off nt
.LBB0_200:
	s_or_b64 exec, exec, s[8:9]
	v_mov_b32_e32 v14, 0
	v_mov_b32_e32 v18, 0
	v_mov_b32_e32 v19, 0
	v_mov_b32_e32 v20, 0
	v_mov_b32_e32 v21, 0
	s_and_saveexec_b64 s[8:9], vcc
	s_cbranch_execz .LBB0_202
	v_add_u32_e32 v16, 12, v80
	v_ashrrev_i32_e32 v17, 31, v16
	v_lshlrev_b64 v[16:17], 13, v[16:17]
	v_lshl_add_u64 v[16:17], v[78:79], 0, v[16:17]
	global_load_dwordx4 v[18:21], v[16:17], off nt
.LBB0_202:
	s_or_b64 exec, exec, s[8:9]
	v_mov_b32_e32 v15, 0
	v_mov_b32_e32 v16, 0
	v_mov_b32_e32 v17, 0
	s_and_saveexec_b64 s[8:9], vcc
	s_cbranch_execz .LBB0_204
	v_add_u32_e32 v14, 16, v80
	v_ashrrev_i32_e32 v15, 31, v14
	v_lshlrev_b64 v[14:15], 13, v[14:15]
	v_lshl_add_u64 v[14:15], v[78:79], 0, v[14:15]
	global_load_dwordx4 v[14:17], v[14:15], off nt
.LBB0_204:
	s_or_b64 exec, exec, s[8:9]
	v_mov_b32_e32 v22, 0
	v_mov_b32_e32 v26, 0
	v_mov_b32_e32 v27, 0
	v_mov_b32_e32 v28, 0
	v_mov_b32_e32 v29, 0
	s_and_saveexec_b64 s[8:9], vcc
	s_cbranch_execz .LBB0_206
	v_add_u32_e32 v24, 20, v80
	v_ashrrev_i32_e32 v25, 31, v24
	v_lshlrev_b64 v[24:25], 13, v[24:25]
	v_lshl_add_u64 v[24:25], v[78:79], 0, v[24:25]
	global_load_dwordx4 v[26:29], v[24:25], off nt
.LBB0_206:
	s_or_b64 exec, exec, s[8:9]
	v_mov_b32_e32 v23, 0
	v_mov_b32_e32 v24, 0
	v_mov_b32_e32 v25, 0
	s_and_saveexec_b64 s[8:9], vcc
	s_cbranch_execz .LBB0_208
	v_add_u32_e32 v22, 24, v80
	v_ashrrev_i32_e32 v23, 31, v22
	v_lshlrev_b64 v[22:23], 13, v[22:23]
	v_lshl_add_u64 v[22:23], v[78:79], 0, v[22:23]
	global_load_dwordx4 v[22:25], v[22:23], off nt
.LBB0_208:
	s_or_b64 exec, exec, s[8:9]
	v_mov_b32_e32 v30, 0
	v_mov_b32_e32 v34, 0
	v_mov_b32_e32 v35, 0
	v_mov_b32_e32 v36, 0
	v_mov_b32_e32 v37, 0
	s_and_saveexec_b64 s[8:9], vcc
	s_cbranch_execz .LBB0_210
	v_add_u32_e32 v32, 28, v80
	v_ashrrev_i32_e32 v33, 31, v32
	v_lshlrev_b64 v[32:33], 13, v[32:33]
	v_lshl_add_u64 v[32:33], v[78:79], 0, v[32:33]
	global_load_dwordx4 v[34:37], v[32:33], off nt
.LBB0_210:
	s_or_b64 exec, exec, s[8:9]
	v_mov_b32_e32 v31, 0
	v_mov_b32_e32 v32, 0
	v_mov_b32_e32 v33, 0
	s_and_saveexec_b64 s[8:9], vcc
	s_cbranch_execz .LBB0_212
	v_add_u32_e32 v30, 32, v80
	v_ashrrev_i32_e32 v31, 31, v30
	v_lshlrev_b64 v[30:31], 13, v[30:31]
	v_lshl_add_u64 v[30:31], v[78:79], 0, v[30:31]
	global_load_dwordx4 v[30:33], v[30:31], off nt
.LBB0_212:
	s_or_b64 exec, exec, s[8:9]
	v_mov_b32_e32 v38, 0
	v_mov_b32_e32 v42, 0
	v_mov_b32_e32 v43, 0
	v_mov_b32_e32 v44, 0
	v_mov_b32_e32 v45, 0
	s_and_saveexec_b64 s[8:9], vcc
	s_cbranch_execz .LBB0_214
	v_add_u32_e32 v40, 36, v80
	v_ashrrev_i32_e32 v41, 31, v40
	v_lshlrev_b64 v[40:41], 13, v[40:41]
	v_lshl_add_u64 v[40:41], v[78:79], 0, v[40:41]
	global_load_dwordx4 v[42:45], v[40:41], off nt
.LBB0_214:
	s_or_b64 exec, exec, s[8:9]
	v_mov_b32_e32 v39, 0
	v_mov_b32_e32 v40, 0
	v_mov_b32_e32 v41, 0
	s_and_saveexec_b64 s[8:9], vcc
	s_cbranch_execz .LBB0_216
	v_add_u32_e32 v38, 40, v80
	v_ashrrev_i32_e32 v39, 31, v38
	v_lshlrev_b64 v[38:39], 13, v[38:39]
	v_lshl_add_u64 v[38:39], v[78:79], 0, v[38:39]
	global_load_dwordx4 v[38:41], v[38:39], off nt
.LBB0_216:
	s_or_b64 exec, exec, s[8:9]
	v_mov_b32_e32 v46, 0
	v_mov_b32_e32 v50, 0
	v_mov_b32_e32 v51, 0
	v_mov_b32_e32 v52, 0
	v_mov_b32_e32 v53, 0
	s_and_saveexec_b64 s[8:9], vcc
	s_cbranch_execz .LBB0_218
	v_add_u32_e32 v48, 44, v80
	v_ashrrev_i32_e32 v49, 31, v48
	v_lshlrev_b64 v[48:49], 13, v[48:49]
	v_lshl_add_u64 v[48:49], v[78:79], 0, v[48:49]
	global_load_dwordx4 v[50:53], v[48:49], off nt
.LBB0_218:
	s_or_b64 exec, exec, s[8:9]
	v_mov_b32_e32 v47, 0
	v_mov_b32_e32 v48, 0
	v_mov_b32_e32 v49, 0
	s_and_saveexec_b64 s[8:9], vcc
	s_cbranch_execz .LBB0_220
	v_add_u32_e32 v46, 48, v80
	v_ashrrev_i32_e32 v47, 31, v46
	v_lshlrev_b64 v[46:47], 13, v[46:47]
	v_lshl_add_u64 v[46:47], v[78:79], 0, v[46:47]
	global_load_dwordx4 v[46:49], v[46:47], off nt
.LBB0_220:
	s_or_b64 exec, exec, s[8:9]
	v_mov_b32_e32 v54, 0
	v_mov_b32_e32 v58, 0
	v_mov_b32_e32 v59, 0
	v_mov_b32_e32 v60, 0
	v_mov_b32_e32 v61, 0
	s_and_saveexec_b64 s[8:9], vcc
	s_cbranch_execz .LBB0_222
	v_add_u32_e32 v56, 52, v80
	v_ashrrev_i32_e32 v57, 31, v56
	v_lshlrev_b64 v[56:57], 13, v[56:57]
	v_lshl_add_u64 v[56:57], v[78:79], 0, v[56:57]
	global_load_dwordx4 v[58:61], v[56:57], off nt
.LBB0_222:
	s_or_b64 exec, exec, s[8:9]
	v_mov_b32_e32 v55, 0
	v_mov_b32_e32 v56, 0
	v_mov_b32_e32 v57, 0
	s_and_saveexec_b64 s[8:9], vcc
	s_cbranch_execz .LBB0_224
	v_add_u32_e32 v54, 56, v80
	v_ashrrev_i32_e32 v55, 31, v54
	v_lshlrev_b64 v[54:55], 13, v[54:55]
	v_lshl_add_u64 v[54:55], v[78:79], 0, v[54:55]
	global_load_dwordx4 v[54:57], v[54:55], off nt
.LBB0_224:
	s_or_b64 exec, exec, s[8:9]
	v_mov_b32_e32 v62, 0
	v_mov_b32_e32 v63, 0
	v_mov_b32_e32 v64, 0
	v_mov_b32_e32 v65, 0
	s_and_saveexec_b64 s[8:9], vcc
	s_cbranch_execz .LBB0_193
	v_add_u32_e32 v62, 60, v80
	v_ashrrev_i32_e32 v63, 31, v62
	v_lshlrev_b64 v[62:63], 13, v[62:63]
	v_lshl_add_u64 v[62:63], v[78:79], 0, v[62:63]
	global_load_dwordx4 v[62:65], v[62:63], off nt
	s_branch .LBB0_193

.LBB0_229:
	v_ashrrev_i32_e32 v2, 31, v69
	v_lshrrev_b32_e32 v2, 27, v2
	v_add_u32_e32 v2, v69, v2
	v_ashrrev_i32_e32 v81, 5, v2
	v_lshlrev_b32_e32 v80, 6, v81
	v_or_b32_e32 v2, v80, v71
	v_ashrrev_i32_e32 v3, 31, v2
	v_cmp_gt_i32_e64 s[6:7], s15, v2
	v_lshl_add_u64 v[78:79], v[2:3], 2, s[38:39]
	v_mov_b32_e32 v2, 0
	v_mov_b32_e32 v3, 0
	v_mov_b32_e32 v4, 0
	v_mov_b32_e32 v5, 0
	s_and_saveexec_b64 s[12:13], s[6:7]
	s_cbranch_execz .LBB0_231
	v_mad_u64_u32 v[2:3], s[22:23], v81, s17, v[76:77]
	v_ashrrev_i32_e32 v3, 31, v2
	v_lshl_add_u64 v[2:3], v[2:3], 2, v[78:79]
	global_load_dwordx4 v[2:5], v[2:3], off nt
.LBB0_231:
	s_or_b64 exec, exec, s[12:13]
	v_mov_b32_e32 v6, 0
	v_mov_b32_e32 v10, 0
	v_mov_b32_e32 v11, 0
	v_mov_b32_e32 v12, 0
	v_mov_b32_e32 v13, 0
	s_and_saveexec_b64 s[12:13], s[6:7]
	s_cbranch_execz .LBB0_233
	v_mad_u64_u32 v[8:9], s[22:23], v81, s17, v[76:77]
	v_ashrrev_i32_e32 v9, 31, v8
	v_lshl_add_u64 v[8:9], v[8:9], 2, v[78:79]
	v_add_co_u32_e32 v8, vcc, 0x18000, v8
	s_nop 1
	v_addc_co_u32_e32 v9, vcc, 0, v9, vcc
	global_load_dwordx4 v[10:13], v[8:9], off nt
.LBB0_233:
	s_or_b64 exec, exec, s[12:13]
	v_mov_b32_e32 v7, 0
	v_mov_b32_e32 v8, 0
	v_mov_b32_e32 v9, 0
	s_and_saveexec_b64 s[12:13], s[6:7]
	s_cbranch_execz .LBB0_235
	v_mad_u64_u32 v[6:7], s[22:23], v81, s17, v[76:77]
	v_ashrrev_i32_e32 v7, 31, v6
	v_lshl_add_u64 v[6:7], v[6:7], 2, v[78:79]
	v_add_co_u32_e32 v6, vcc, 0x30000, v6
	s_nop 1
	v_addc_co_u32_e32 v7, vcc, 0, v7, vcc
	global_load_dwordx4 v[6:9], v[6:7], off nt
.LBB0_235:
	s_or_b64 exec, exec, s[12:13]
	v_mov_b32_e32 v14, 0
	v_mov_b32_e32 v18, 0
	v_mov_b32_e32 v19, 0
	v_mov_b32_e32 v20, 0
	v_mov_b32_e32 v21, 0
	s_and_saveexec_b64 s[12:13], s[6:7]
	s_cbranch_execz .LBB0_237
	v_mad_u64_u32 v[16:17], s[22:23], v81, s17, v[76:77]
	v_ashrrev_i32_e32 v17, 31, v16
	v_lshl_add_u64 v[16:17], v[16:17], 2, v[78:79]
	v_add_co_u32_e32 v16, vcc, 0x48000, v16
	s_nop 1
	v_addc_co_u32_e32 v17, vcc, 0, v17, vcc
	global_load_dwordx4 v[18:21], v[16:17], off nt
.LBB0_237:
	s_or_b64 exec, exec, s[12:13]
	v_mov_b32_e32 v15, 0
	v_mov_b32_e32 v16, 0
	v_mov_b32_e32 v17, 0
	s_and_saveexec_b64 s[12:13], s[6:7]
	s_cbranch_execz .LBB0_239
	v_mad_u64_u32 v[14:15], s[22:23], v81, s17, v[76:77]
	v_ashrrev_i32_e32 v15, 31, v14
	v_lshl_add_u64 v[14:15], v[14:15], 2, v[78:79]
	v_add_co_u32_e32 v14, vcc, 0x60000, v14
	s_nop 1
	v_addc_co_u32_e32 v15, vcc, 0, v15, vcc
	global_load_dwordx4 v[14:17], v[14:15], off nt
.LBB0_239:
	s_or_b64 exec, exec, s[12:13]
	v_mov_b32_e32 v22, 0
	v_mov_b32_e32 v26, 0
	v_mov_b32_e32 v27, 0
	v_mov_b32_e32 v28, 0
	v_mov_b32_e32 v29, 0
	s_and_saveexec_b64 s[12:13], s[6:7]
	s_cbranch_execz .LBB0_241
	v_mad_u64_u32 v[24:25], s[22:23], v81, s17, v[76:77]
	v_ashrrev_i32_e32 v25, 31, v24
	v_lshl_add_u64 v[24:25], v[24:25], 2, v[78:79]
	v_add_co_u32_e32 v24, vcc, 0x78000, v24
	s_nop 1
	v_addc_co_u32_e32 v25, vcc, 0, v25, vcc
	global_load_dwordx4 v[26:29], v[24:25], off nt
.LBB0_241:
	s_or_b64 exec, exec, s[12:13]
	v_mov_b32_e32 v23, 0
	v_mov_b32_e32 v24, 0
	v_mov_b32_e32 v25, 0
	s_and_saveexec_b64 s[12:13], s[6:7]
	s_cbranch_execz .LBB0_243
	v_mad_u64_u32 v[22:23], s[22:23], v81, s17, v[76:77]
	v_ashrrev_i32_e32 v23, 31, v22
	v_lshl_add_u64 v[22:23], v[22:23], 2, v[78:79]
	v_add_co_u32_e32 v22, vcc, 0x90000, v22
	s_nop 1
	v_addc_co_u32_e32 v23, vcc, 0, v23, vcc
	global_load_dwordx4 v[22:25], v[22:23], off nt
.LBB0_243:
	s_or_b64 exec, exec, s[12:13]
	v_mov_b32_e32 v30, 0
	v_mov_b32_e32 v34, 0
	v_mov_b32_e32 v35, 0
	v_mov_b32_e32 v36, 0
	v_mov_b32_e32 v37, 0
	s_and_saveexec_b64 s[12:13], s[6:7]
	s_cbranch_execz .LBB0_245
	v_mad_u64_u32 v[32:33], s[22:23], v81, s17, v[76:77]
	v_ashrrev_i32_e32 v33, 31, v32
	v_lshl_add_u64 v[32:33], v[32:33], 2, v[78:79]
	v_add_co_u32_e32 v32, vcc, 0xa8000, v32
	s_nop 1
	v_addc_co_u32_e32 v33, vcc, 0, v33, vcc
	global_load_dwordx4 v[34:37], v[32:33], off nt
.LBB0_245:
	s_or_b64 exec, exec, s[12:13]
	v_mov_b32_e32 v31, 0
	v_mov_b32_e32 v32, 0
	v_mov_b32_e32 v33, 0
	s_and_saveexec_b64 s[12:13], s[6:7]
	s_cbranch_execz .LBB0_247
	v_mad_u64_u32 v[30:31], s[22:23], v81, s17, v[76:77]
	v_ashrrev_i32_e32 v31, 31, v30
	v_lshl_add_u64 v[30:31], v[30:31], 2, v[78:79]
	v_add_co_u32_e32 v30, vcc, 0xc0000, v30
	s_nop 1
	v_addc_co_u32_e32 v31, vcc, 0, v31, vcc
	global_load_dwordx4 v[30:33], v[30:31], off nt
.LBB0_247:
	s_or_b64 exec, exec, s[12:13]
	v_mov_b32_e32 v38, 0
	v_mov_b32_e32 v42, 0
	v_mov_b32_e32 v43, 0
	v_mov_b32_e32 v44, 0
	v_mov_b32_e32 v45, 0
	s_and_saveexec_b64 s[12:13], s[6:7]
	s_cbranch_execz .LBB0_249
	v_mad_u64_u32 v[40:41], s[22:23], v81, s17, v[76:77]
	v_ashrrev_i32_e32 v41, 31, v40
	v_lshl_add_u64 v[40:41], v[40:41], 2, v[78:79]
	v_add_co_u32_e32 v40, vcc, 0xd8000, v40
	s_nop 1
	v_addc_co_u32_e32 v41, vcc, 0, v41, vcc
	global_load_dwordx4 v[42:45], v[40:41], off nt
.LBB0_249:
	s_or_b64 exec, exec, s[12:13]
	v_mov_b32_e32 v39, 0
	v_mov_b32_e32 v40, 0
	v_mov_b32_e32 v41, 0
	s_and_saveexec_b64 s[12:13], s[6:7]
	s_cbranch_execz .LBB0_251
	v_mad_u64_u32 v[38:39], s[22:23], v81, s17, v[76:77]
	v_ashrrev_i32_e32 v39, 31, v38
	v_lshl_add_u64 v[38:39], v[38:39], 2, v[78:79]
	v_add_co_u32_e32 v38, vcc, 0xf0000, v38
	s_nop 1
	v_addc_co_u32_e32 v39, vcc, 0, v39, vcc
	global_load_dwordx4 v[38:41], v[38:39], off nt
.LBB0_251:
	s_or_b64 exec, exec, s[12:13]
	v_mov_b32_e32 v46, 0
	v_mov_b32_e32 v50, 0
	v_mov_b32_e32 v51, 0
	v_mov_b32_e32 v52, 0
	v_mov_b32_e32 v53, 0
	s_and_saveexec_b64 s[12:13], s[6:7]
	s_cbranch_execz .LBB0_253
	v_mad_u64_u32 v[48:49], s[22:23], v81, s17, v[76:77]
	v_ashrrev_i32_e32 v49, 31, v48
	v_lshl_add_u64 v[48:49], v[48:49], 2, v[78:79]
	v_add_co_u32_e32 v48, vcc, 0x108000, v48
	s_nop 1
	v_addc_co_u32_e32 v49, vcc, 0, v49, vcc
	global_load_dwordx4 v[50:53], v[48:49], off nt
.LBB0_253:
	s_or_b64 exec, exec, s[12:13]
	v_mov_b32_e32 v47, 0
	v_mov_b32_e32 v48, 0
	v_mov_b32_e32 v49, 0
	s_and_saveexec_b64 s[12:13], s[6:7]
	s_cbranch_execz .LBB0_255
	v_mad_u64_u32 v[46:47], s[22:23], v81, s17, v[76:77]
	v_ashrrev_i32_e32 v47, 31, v46
	v_lshl_add_u64 v[46:47], v[46:47], 2, v[78:79]
	v_add_co_u32_e32 v46, vcc, 0x120000, v46
	s_nop 1
	v_addc_co_u32_e32 v47, vcc, 0, v47, vcc
	global_load_dwordx4 v[46:49], v[46:47], off nt
.LBB0_255:
	s_or_b64 exec, exec, s[12:13]
	v_mov_b32_e32 v54, 0
	v_mov_b32_e32 v58, 0
	v_mov_b32_e32 v59, 0
	v_mov_b32_e32 v60, 0
	v_mov_b32_e32 v61, 0
	s_and_saveexec_b64 s[12:13], s[6:7]
	s_cbranch_execz .LBB0_257
	v_mad_u64_u32 v[56:57], s[22:23], v81, s17, v[76:77]
	v_ashrrev_i32_e32 v57, 31, v56
	v_lshl_add_u64 v[56:57], v[56:57], 2, v[78:79]
	v_add_co_u32_e32 v56, vcc, 0x138000, v56
	s_nop 1
	v_addc_co_u32_e32 v57, vcc, 0, v57, vcc
	global_load_dwordx4 v[58:61], v[56:57], off nt
.LBB0_257:
	s_or_b64 exec, exec, s[12:13]
	v_mov_b32_e32 v55, 0
	v_mov_b32_e32 v56, 0
	v_mov_b32_e32 v57, 0
	s_and_saveexec_b64 s[12:13], s[6:7]
	s_cbranch_execz .LBB0_259
	v_mad_u64_u32 v[54:55], s[22:23], v81, s17, v[76:77]
	v_ashrrev_i32_e32 v55, 31, v54
	v_lshl_add_u64 v[54:55], v[54:55], 2, v[78:79]
	v_add_co_u32_e32 v54, vcc, 0x150000, v54
	s_nop 1
	v_addc_co_u32_e32 v55, vcc, 0, v55, vcc
	global_load_dwordx4 v[54:57], v[54:55], off nt
.LBB0_259:
	s_or_b64 exec, exec, s[12:13]
	v_mov_b32_e32 v62, 0
	v_mov_b32_e32 v63, 0
	v_mov_b32_e32 v64, 0
	v_mov_b32_e32 v65, 0
	s_and_saveexec_b64 s[12:13], s[6:7]
	s_cbranch_execz .LBB0_228
	v_mad_u64_u32 v[62:63], s[6:7], v81, s17, v[76:77]
	v_ashrrev_i32_e32 v63, 31, v62
	v_lshl_add_u64 v[62:63], v[62:63], 2, v[78:79]
	v_add_co_u32_e32 v62, vcc, 0x168000, v62
	s_nop 1
	v_addc_co_u32_e32 v63, vcc, 0, v63, vcc
	global_load_dwordx4 v[62:65], v[62:63], off nt
	s_branch .LBB0_228

.LBB0_263:
	global_load_dwordx4 v[8:11], v[4:5], off offset:-16 nt
	global_load_dwordx4 v[12:15], v[4:5], off nt
	v_lshl_add_u64 v[2:3], v[2:3], 0, s[6:7]
	v_cmp_lt_u64_e32 vcc, s[16:17], v[2:3]
	v_lshl_add_u64 v[4:5], v[4:5], 0, s[8:9]
	s_or_b64 s[14:15], vcc, s[14:15]
	s_waitcnt vmcnt(1)
	v_cvt_pk_f16_f32 v8, v8, v9
	v_cvt_pk_f16_f32 v9, v10, v11
	s_waitcnt vmcnt(0)
	v_cvt_pk_f16_f32 v10, v12, v13
	v_cvt_pk_f16_f32 v11, v14, v15
	v_add_u32_e32 v8, 0x20002, v8
	v_add_u32_e32 v9, 0x20002, v9
	v_add_u32_e32 v10, 0x20002, v10
	v_add_u32_e32 v11, 0x20002, v11
	v_and_b32_e32 v8, 0xfffcfffc, v8
	v_and_b32_e32 v9, 0xfffcfffc, v9
	v_and_b32_e32 v10, 0xfffcfffc, v10
	v_and_b32_e32 v11, 0xfffcfffc, v11
	global_store_dwordx4 v[6:7], v[8:11], off
	v_lshl_add_u64 v[6:7], v[6:7], 0, s[12:13]
	s_andn2_b64 exec, exec, s[14:15]
	s_cbranch_execnz .LBB0_263

.LBB0_1562:
	v_ashrrev_i32_e32 v42, 31, v41
	v_lshrrev_b32_e32 v42, 28, v42
	v_add_u32_e32 v42, v41, v42
	v_ashrrev_i32_e32 v45, 4, v42
	v_ashrrev_i32_e32 v42, 6, v42
	v_lshlrev_b32_e32 v44, 5, v45
	v_ashrrev_i32_e32 v43, 31, v42
	v_lshlrev_b32_e32 v80, 11, v45
	v_mad_u64_u32 v[46:47], s[0:1], v45, s25, v[38:39]
	v_lshlrev_b64 v[42:43], 8, v[42:43]
	v_ashrrev_i32_e32 v45, 31, v44
	v_sub_u32_e32 v80, v40, v80
	v_ashrrev_i32_e32 v47, 31, v46
	v_lshl_add_u64 v[140:141], v[42:43], 0, s[16:17]
	v_lshl_add_u64 v[42:43], v[44:45], 2, v[36:37]
	v_ashrrev_i32_e32 v81, 31, v80
	v_lshl_add_u64 v[46:47], v[46:47], 2, v[42:43]
	v_lshl_add_u64 v[142:143], v[26:27], 0, v[80:81]
	v_add_co_u32_e64 v80, s[0:1], s26, v46
	v_and_or_b32 v148, v44, s24, v140
	s_nop 0
	v_addc_co_u32_e64 v81, s[0:1], 0, v47, s[0:1]
	v_add_co_u32_e64 v84, s[0:1], s27, v46
	global_load_dwordx4 v[42:45], v[46:47], off nt
	s_nop 0
	v_addc_co_u32_e64 v85, s[0:1], 0, v47, s[0:1]
	v_add_co_u32_e64 v88, s[0:1], s28, v46
	v_add_u32_e32 v76, 0x3de0, v25
	s_nop 0
	v_addc_co_u32_e64 v89, s[0:1], 0, v47, s[0:1]
	v_add_co_u32_e64 v92, s[0:1], s21, v46
	v_add_u32_e32 v77, 0x3de8, v25
	s_nop 0
	v_addc_co_u32_e64 v93, s[0:1], 0, v47, s[0:1]
	v_add_co_u32_e64 v96, s[0:1], s29, v46
	v_add_u32_e32 v78, 0x400, v19
	s_nop 0
	v_addc_co_u32_e64 v97, s[0:1], 0, v47, s[0:1]
	v_add_co_u32_e64 v100, s[0:1], s30, v46
	v_add_u32_e32 v79, 0x600, v19
	s_nop 0
	v_addc_co_u32_e64 v101, s[0:1], 0, v47, s[0:1]
	v_add_co_u32_e64 v104, s[0:1], s31, v46
	v_mov_b32_e32 v2, 0
	s_nop 0
	v_addc_co_u32_e64 v105, s[0:1], 0, v47, s[0:1]
	v_add_co_u32_e64 v108, s[0:1], s33, v46
	v_mov_b32_e32 v3, 0
	s_nop 0
	v_addc_co_u32_e64 v109, s[0:1], 0, v47, s[0:1]
	v_add_co_u32_e64 v112, s[0:1], s34, v46
	v_mov_b32_e32 v4, 0
	s_nop 0
	v_addc_co_u32_e64 v113, s[0:1], 0, v47, s[0:1]
	v_add_co_u32_e64 v116, s[0:1], s35, v46
	v_mov_b32_e32 v5, 0
	s_nop 0
	v_addc_co_u32_e64 v117, s[0:1], 0, v47, s[0:1]
	v_add_co_u32_e64 v120, s[0:1], s36, v46
	v_mov_b32_e32 v6, 0
	s_nop 0
	v_addc_co_u32_e64 v121, s[0:1], 0, v47, s[0:1]
	v_add_co_u32_e64 v124, s[0:1], s37, v46
	v_mov_b32_e32 v7, 0
	s_nop 0
	v_addc_co_u32_e64 v125, s[0:1], 0, v47, s[0:1]
	v_add_co_u32_e64 v128, s[0:1], s38, v46
	v_mov_b32_e32 v8, 0
	s_nop 0
	v_addc_co_u32_e64 v129, s[0:1], 0, v47, s[0:1]
	v_add_co_u32_e64 v132, s[0:1], s39, v46
	v_mov_b32_e32 v9, 0
	s_nop 0
	v_addc_co_u32_e64 v133, s[0:1], 0, v47, s[0:1]
	v_add_co_u32_e64 v46, s[0:1], s40, v46
	v_mov_b32_e32 v10, 0
	s_nop 0
	v_addc_co_u32_e64 v47, s[0:1], 0, v47, s[0:1]
	global_load_dwordx4 v[80:83], v[80:81], off nt
	s_nop 0
	global_load_dwordx4 v[84:87], v[84:85], off nt
	s_nop 0
	global_load_dwordx4 v[88:91], v[88:89], off nt
	s_nop 0
	global_load_dwordx4 v[92:95], v[92:93], off nt
	s_nop 0
	global_load_dwordx4 v[96:99], v[96:97], off nt
	s_nop 0
	global_load_dwordx4 v[100:103], v[100:101], off nt
	s_nop 0
	global_load_dwordx4 v[104:107], v[104:105], off nt
	s_nop 0
	global_load_dwordx4 v[108:111], v[108:109], off nt
	s_nop 0
	global_load_dwordx4 v[112:115], v[112:113], off nt
	s_nop 0
	global_load_dwordx4 v[116:119], v[116:117], off nt
	s_nop 0
	global_load_dwordx4 v[120:123], v[120:121], off nt
	s_nop 0
	global_load_dwordx4 v[124:127], v[124:125], off nt
	s_nop 0
	global_load_dwordx4 v[128:131], v[128:129], off nt
	s_nop 0
	global_load_dwordx4 v[132:135], v[132:133], off nt
	s_nop 0
	global_load_dwordx4 v[136:139], v[46:47], off nt
	v_mov_b32_e32 v11, 0
	v_mov_b32_e32 v12, 0
	v_mov_b32_e32 v13, 0
	v_mov_b32_e32 v14, 0
	v_mov_b32_e32 v15, 0
	v_mov_b32_e32 v16, 0
	v_mov_b32_e32 v17, 0
	v_or_b32_e32 v140, v148, v18
	v_lshlrev_b64 v[46:47], 11, v[140:141]
	v_or_b32_e32 v140, v148, v20
	v_lshlrev_b64 v[144:145], 11, v[140:141]
	v_or_b32_e32 v140, v148, v22
	v_lshlrev_b64 v[146:147], 11, v[140:141]
	v_or_b32_e32 v140, v148, v24
	v_lshl_add_u64 v[46:47], v[142:143], 0, v[46:47]
	v_lshlrev_b64 v[140:141], 11, v[140:141]
	v_lshl_add_u64 v[144:145], v[142:143], 0, v[144:145]
	v_lshl_add_u64 v[146:147], v[142:143], 0, v[146:147]
	v_lshl_add_u64 v[140:141], v[142:143], 0, v[140:141]
	v_add_u32_e32 v41, s3, v41
	v_cmp_lt_i32_e32 vcc, s42, v41
	v_add_u32_e32 v38, s22, v38
	s_waitcnt vmcnt(15)
	ds_write2_b32 v25, v42, v43 offset1:1
	ds_write2_b32 v25, v44, v45 offset0:2 offset1:3
	s_waitcnt vmcnt(14)
	ds_write2_b32 v39, v80, v81 offset1:1
	ds_write2_b32 v48, v82, v83 offset1:1
	s_waitcnt vmcnt(13)
	ds_write2_b32 v49, v84, v85 offset1:1
	ds_write2_b32 v50, v86, v87 offset1:1
	s_waitcnt vmcnt(12)
	ds_write2_b32 v51, v88, v89 offset1:1
	ds_write2_b32 v52, v90, v91 offset1:1
	s_waitcnt vmcnt(11)
	ds_write2_b32 v53, v92, v93 offset1:1
	ds_write2_b32 v54, v94, v95 offset1:1
	s_waitcnt vmcnt(10)
	ds_write2_b32 v55, v96, v97 offset1:1
	ds_write2_b32 v56, v98, v99 offset1:1
	s_waitcnt vmcnt(9)
	ds_write2_b32 v57, v100, v101 offset1:1
	ds_write2_b32 v58, v102, v103 offset1:1
	s_waitcnt vmcnt(8)
	ds_write2_b32 v59, v104, v105 offset1:1
	ds_write2_b32 v60, v106, v107 offset1:1
	s_waitcnt vmcnt(7)
	ds_write2_b32 v61, v108, v109 offset1:1
	ds_write2_b32 v62, v110, v111 offset1:1
	s_waitcnt vmcnt(6)
	ds_write2_b32 v63, v112, v113 offset1:1
	ds_write2_b32 v64, v114, v115 offset1:1
	s_waitcnt vmcnt(5)
	ds_write2_b32 v65, v116, v117 offset1:1
	ds_write2_b32 v66, v118, v119 offset1:1
	s_waitcnt vmcnt(4)
	ds_write2_b32 v67, v120, v121 offset1:1
	ds_write2_b32 v68, v122, v123 offset1:1
	s_waitcnt vmcnt(3)
	ds_write2_b32 v69, v124, v125 offset1:1
	ds_write2_b32 v70, v126, v127 offset1:1
	s_waitcnt vmcnt(2)
	ds_write2_b32 v71, v128, v129 offset1:1
	ds_write2_b32 v72, v130, v131 offset1:1
	s_waitcnt vmcnt(1)
	ds_write2_b32 v73, v132, v133 offset1:1
	ds_write2_b32 v74, v134, v135 offset1:1
	s_waitcnt vmcnt(0)
	ds_write2_b32 v76, v136, v137 offset1:1
	ds_write2_b32 v77, v138, v139 offset1:1
	s_waitcnt lgkmcnt(0)
	ds_read2_b32 v[42:43], v19 offset1:8
	ds_read2_b32 v[44:45], v19 offset0:33 offset1:41
	ds_read2_b32 v[80:81], v19 offset0:66 offset1:74
	ds_read2_b32 v[82:83], v19 offset0:99 offset1:107
	ds_read2_b32 v[84:85], v19 offset0:132 offset1:140
	ds_read2_b32 v[86:87], v19 offset0:165 offset1:173
	ds_read2_b32 v[88:89], v19 offset0:198 offset1:206
	ds_read2_b32 v[90:91], v19 offset0:231 offset1:239
	ds_read2_b32 v[92:93], v78 offset0:8 offset1:16
	ds_read2_b32 v[94:95], v78 offset0:41 offset1:49
	ds_read2_b32 v[96:97], v78 offset0:74 offset1:82
	ds_read2_b32 v[98:99], v78 offset0:107 offset1:115
	ds_read2_b32 v[100:101], v78 offset0:140 offset1:148
	ds_read2_b32 v[102:103], v78 offset0:173 offset1:181
	ds_read2_b32 v[104:105], v78 offset0:206 offset1:214
	ds_read2_b32 v[106:107], v78 offset0:239 offset1:247
	ds_read2_b32 v[108:109], v19 offset0:16 offset1:24
	ds_read2_b32 v[110:111], v19 offset0:49 offset1:57
	ds_read2_b32 v[112:113], v19 offset0:82 offset1:90
	ds_read2_b32 v[114:115], v19 offset0:115 offset1:123
	ds_read2_b32 v[116:117], v19 offset0:148 offset1:156
	ds_read2_b32 v[118:119], v19 offset0:181 offset1:189
	ds_read2_b32 v[120:121], v19 offset0:214 offset1:222
	ds_read2_b32 v[122:123], v19 offset0:247 offset1:255
	ds_read2_b32 v[124:125], v78 offset0:24 offset1:32
	ds_read2_b32 v[126:127], v78 offset0:57 offset1:65
	ds_read2_b32 v[128:129], v78 offset0:90 offset1:98
	ds_read2_b32 v[130:131], v78 offset0:123 offset1:131
	ds_read2_b32 v[132:133], v78 offset0:156 offset1:164
	ds_read2_b32 v[134:135], v78 offset0:189 offset1:197
	ds_read2_b32 v[136:137], v78 offset0:222 offset1:230
	ds_read2_b32 v[138:139], v79 offset0:127 offset1:135
	s_waitcnt lgkmcnt(14)
	v_mul_f32_e32 v42, 0x43800000, v42
	v_mul_f32_e32 v44, 0x43800000, v44
	v_mul_f32_e32 v84, 0x43800000, v84
	v_mul_f32_e32 v86, 0x43800000, v86
	v_mul_f32_e32 v92, 0x43800000, v92
	v_mul_f32_e32 v94, 0x43800000, v94
	v_mul_f32_e32 v100, 0x43800000, v100
	v_mul_f32_e32 v102, 0x43800000, v102
	v_mul_f32_e32 v43, 0x43800000, v43
	v_mul_f32_e32 v45, 0x43800000, v45
	v_mul_f32_e32 v85, 0x43800000, v85
	v_mul_f32_e32 v87, 0x43800000, v87
	v_mul_f32_e32 v93, 0x43800000, v93
	v_mul_f32_e32 v95, 0x43800000, v95
	v_mul_f32_e32 v101, 0x43800000, v101
	v_mul_f32_e32 v103, 0x43800000, v103
	v_med3_f32 v42, v42, s41, v75
	v_med3_f32 v44, v44, s41, v75
	v_med3_f32 v84, v84, s41, v75
	v_med3_f32 v86, v86, s41, v75
	v_med3_f32 v92, v92, s41, v75
	v_med3_f32 v94, v94, s41, v75
	v_med3_f32 v100, v100, s41, v75
	v_med3_f32 v102, v102, s41, v75
	v_mul_f32_e32 v108, 0x43800000, v108
	v_mul_f32_e32 v110, 0x43800000, v110
	s_waitcnt lgkmcnt(11)
	v_mul_f32_e32 v116, 0x43800000, v116
	s_waitcnt lgkmcnt(10)
	v_mul_f32_e32 v118, 0x43800000, v118
	s_waitcnt lgkmcnt(7)
	v_mul_f32_e32 v124, 0x43800000, v124
	s_waitcnt lgkmcnt(6)
	v_mul_f32_e32 v126, 0x43800000, v126
	s_waitcnt lgkmcnt(3)
	v_mul_f32_e32 v132, 0x43800000, v132
	s_waitcnt lgkmcnt(2)
	v_mul_f32_e32 v134, 0x43800000, v134
	v_med3_f32 v43, v43, s41, v75
	v_med3_f32 v45, v45, s41, v75
	v_med3_f32 v85, v85, s41, v75
	v_med3_f32 v87, v87, s41, v75
	v_med3_f32 v93, v93, s41, v75
	v_med3_f32 v95, v95, s41, v75
	v_med3_f32 v101, v101, s41, v75
	v_med3_f32 v103, v103, s41, v75
	v_cvt_pk_fp8_f32 v2, v42, v44
	v_cvt_pk_fp8_f32 v3, v84, v86
	v_cvt_pk_fp8_f32 v4, v92, v94
	v_cvt_pk_fp8_f32 v5, v100, v102
	v_mul_f32_e32 v109, 0x43800000, v109
	v_mul_f32_e32 v111, 0x43800000, v111
	v_mul_f32_e32 v117, 0x43800000, v117
	v_mul_f32_e32 v119, 0x43800000, v119
	v_mul_f32_e32 v125, 0x43800000, v125
	v_mul_f32_e32 v127, 0x43800000, v127
	v_mul_f32_e32 v133, 0x43800000, v133
	v_mul_f32_e32 v135, 0x43800000, v135
	v_med3_f32 v108, v108, s41, v75
	v_med3_f32 v110, v110, s41, v75
	v_med3_f32 v116, v116, s41, v75
	v_med3_f32 v118, v118, s41, v75
	v_med3_f32 v124, v124, s41, v75
	v_med3_f32 v126, v126, s41, v75
	v_med3_f32 v132, v132, s41, v75
	v_med3_f32 v134, v134, s41, v75
	v_cvt_pk_fp8_f32 v6, v43, v45
	v_cvt_pk_fp8_f32 v7, v85, v87
	v_cvt_pk_fp8_f32 v8, v93, v95
	v_cvt_pk_fp8_f32 v9, v101, v103
	v_mul_f32_e32 v80, 0x43800000, v80
	v_mul_f32_e32 v82, 0x43800000, v82
	v_mul_f32_e32 v88, 0x43800000, v88
	v_mul_f32_e32 v90, 0x43800000, v90
	v_mul_f32_e32 v96, 0x43800000, v96
	v_mul_f32_e32 v98, 0x43800000, v98
	v_mul_f32_e32 v104, 0x43800000, v104
	v_mul_f32_e32 v106, 0x43800000, v106
	v_med3_f32 v109, v109, s41, v75
	v_med3_f32 v111, v111, s41, v75
	v_med3_f32 v117, v117, s41, v75
	v_med3_f32 v119, v119, s41, v75
	v_med3_f32 v125, v125, s41, v75
	v_med3_f32 v127, v127, s41, v75
	v_med3_f32 v133, v133, s41, v75
	v_med3_f32 v135, v135, s41, v75
	v_cvt_pk_fp8_f32 v10, v108, v110
	v_cvt_pk_fp8_f32 v11, v116, v118
	v_cvt_pk_fp8_f32 v12, v124, v126
	v_cvt_pk_fp8_f32 v13, v132, v134
	v_mul_f32_e32 v81, 0x43800000, v81
	v_mul_f32_e32 v83, 0x43800000, v83
	v_mul_f32_e32 v89, 0x43800000, v89
	v_mul_f32_e32 v91, 0x43800000, v91
	v_mul_f32_e32 v97, 0x43800000, v97
	v_mul_f32_e32 v99, 0x43800000, v99
	v_mul_f32_e32 v105, 0x43800000, v105
	v_mul_f32_e32 v107, 0x43800000, v107
	v_med3_f32 v80, v80, s41, v75
	v_med3_f32 v82, v82, s41, v75
	v_med3_f32 v88, v88, s41, v75
	v_med3_f32 v90, v90, s41, v75
	v_med3_f32 v96, v96, s41, v75
	v_med3_f32 v98, v98, s41, v75
	v_med3_f32 v104, v104, s41, v75
	v_med3_f32 v106, v106, s41, v75
	v_cvt_pk_fp8_f32 v14, v109, v111
	v_cvt_pk_fp8_f32 v15, v117, v119
	v_cvt_pk_fp8_f32 v16, v125, v127
	v_cvt_pk_fp8_f32 v17, v133, v135
	v_mul_f32_e32 v112, 0x43800000, v112
	v_mul_f32_e32 v114, 0x43800000, v114
	v_mul_f32_e32 v120, 0x43800000, v120
	v_mul_f32_e32 v122, 0x43800000, v122
	v_mul_f32_e32 v128, 0x43800000, v128
	v_mul_f32_e32 v130, 0x43800000, v130
	s_waitcnt lgkmcnt(1)
	v_mul_f32_e32 v136, 0x43800000, v136
	s_waitcnt lgkmcnt(0)
	v_mul_f32_e32 v138, 0x43800000, v138
	v_med3_f32 v81, v81, s41, v75
	v_med3_f32 v83, v83, s41, v75
	v_med3_f32 v89, v89, s41, v75
	v_med3_f32 v91, v91, s41, v75
	v_med3_f32 v97, v97, s41, v75
	v_med3_f32 v99, v99, s41, v75
	v_med3_f32 v105, v105, s41, v75
	v_med3_f32 v107, v107, s41, v75
	v_cvt_pk_fp8_f32 v2, v80, v82 op_sel:[0,0,1]
	v_cvt_pk_fp8_f32 v3, v88, v90 op_sel:[0,0,1]
	v_cvt_pk_fp8_f32 v4, v96, v98 op_sel:[0,0,1]
	v_cvt_pk_fp8_f32 v5, v104, v106 op_sel:[0,0,1]
	v_mul_f32_e32 v113, 0x43800000, v113
	v_mul_f32_e32 v115, 0x43800000, v115
	v_mul_f32_e32 v121, 0x43800000, v121
	v_mul_f32_e32 v123, 0x43800000, v123
	v_mul_f32_e32 v129, 0x43800000, v129
	v_mul_f32_e32 v131, 0x43800000, v131
	v_mul_f32_e32 v137, 0x43800000, v137
	v_mul_f32_e32 v139, 0x43800000, v139
	v_med3_f32 v112, v112, s41, v75
	v_med3_f32 v114, v114, s41, v75
	v_med3_f32 v120, v120, s41, v75
	v_med3_f32 v122, v122, s41, v75
	v_med3_f32 v128, v128, s41, v75
	v_med3_f32 v130, v130, s41, v75
	v_med3_f32 v136, v136, s41, v75
	v_med3_f32 v138, v138, s41, v75
	v_cvt_pk_fp8_f32 v6, v81, v83 op_sel:[0,0,1]
	v_cvt_pk_fp8_f32 v7, v89, v91 op_sel:[0,0,1]
	v_cvt_pk_fp8_f32 v8, v97, v99 op_sel:[0,0,1]
	v_cvt_pk_fp8_f32 v9, v105, v107 op_sel:[0,0,1]
	v_med3_f32 v113, v113, s41, v75
	v_med3_f32 v115, v115, s41, v75
	v_med3_f32 v121, v121, s41, v75
	v_med3_f32 v123, v123, s41, v75
	v_med3_f32 v129, v129, s41, v75
	v_med3_f32 v131, v131, s41, v75
	v_med3_f32 v137, v137, s41, v75
	v_med3_f32 v139, v139, s41, v75
	v_cvt_pk_fp8_f32 v10, v112, v114 op_sel:[0,0,1]
	v_cvt_pk_fp8_f32 v11, v120, v122 op_sel:[0,0,1]
	v_cvt_pk_fp8_f32 v12, v128, v130 op_sel:[0,0,1]
	v_cvt_pk_fp8_f32 v13, v136, v138 op_sel:[0,0,1]
	v_cvt_pk_fp8_f32 v14, v113, v115 op_sel:[0,0,1]
	v_cvt_pk_fp8_f32 v15, v121, v123 op_sel:[0,0,1]
	v_cvt_pk_fp8_f32 v16, v129, v131 op_sel:[0,0,1]
	v_cvt_pk_fp8_f32 v17, v137, v139 op_sel:[0,0,1]
	global_store_dwordx4 v[46:47], v[2:5], off
	global_store_dwordx4 v[144:145], v[6:9], off
	global_store_dwordx4 v[146:147], v[10:13], off
	global_store_dwordx4 v[140:141], v[14:17], off
	s_waitcnt lgkmcnt(0)
	s_or_b64 s[18:19], vcc, s[18:19]
	v_add_u32_e32 v40, s23, v40
	s_andn2_b64 exec, exec, s[18:19]
	s_cbranch_execnz .LBB0_1562
	s_or_b64 exec, exec, s[18:19]
	s_bitset1_b32 s16, 7
	v_lshl_add_u64 v[36:37], s[6:7], 2, v[32:33]
	s_mov_b64 s[18:19], 0
	v_mov_b32_e32 v40, v23
	v_mov_b32_e32 v38, v21
	v_mov_b32_e32 v41, v1
.LBB0_1564:
	v_ashrrev_i32_e32 v42, 31, v41
	v_lshrrev_b32_e32 v42, 28, v42
	v_add_u32_e32 v42, v41, v42
	v_ashrrev_i32_e32 v45, 4, v42
	v_ashrrev_i32_e32 v42, 6, v42
	v_lshlrev_b32_e32 v44, 5, v45
	v_ashrrev_i32_e32 v43, 31, v42
	v_lshlrev_b32_e32 v80, 11, v45
	v_mad_u64_u32 v[46:47], s[0:1], v45, s25, v[38:39]
	v_lshlrev_b64 v[42:43], 8, v[42:43]
	v_ashrrev_i32_e32 v45, 31, v44
	v_sub_u32_e32 v80, v40, v80
	v_ashrrev_i32_e32 v47, 31, v46
	v_lshl_add_u64 v[140:141], s[16:17], 0, v[42:43]
	v_lshl_add_u64 v[42:43], v[44:45], 2, v[36:37]
	v_ashrrev_i32_e32 v81, 31, v80
	v_lshl_add_u64 v[46:47], v[46:47], 2, v[42:43]
	v_lshl_add_u64 v[142:143], v[26:27], 0, v[80:81]
	v_add_co_u32_e64 v80, s[0:1], s26, v46
	v_and_or_b32 v148, v44, s24, v140
	s_nop 0
	v_addc_co_u32_e64 v81, s[0:1], 0, v47, s[0:1]
	v_add_co_u32_e64 v84, s[0:1], s27, v46
	global_load_dwordx4 v[42:45], v[46:47], off nt
	s_nop 0
	v_addc_co_u32_e64 v85, s[0:1], 0, v47, s[0:1]
	v_add_co_u32_e64 v88, s[0:1], s28, v46
	v_mov_b32_e32 v2, 0
	s_nop 0
	v_addc_co_u32_e64 v89, s[0:1], 0, v47, s[0:1]
	v_add_co_u32_e64 v92, s[0:1], s21, v46
	v_mov_b32_e32 v3, 0
	s_nop 0
	v_addc_co_u32_e64 v93, s[0:1], 0, v47, s[0:1]
	v_add_co_u32_e64 v96, s[0:1], s29, v46
	v_mov_b32_e32 v4, 0
	s_nop 0
	v_addc_co_u32_e64 v97, s[0:1], 0, v47, s[0:1]
	v_add_co_u32_e64 v100, s[0:1], s30, v46
	v_mov_b32_e32 v5, 0
	s_nop 0
	v_addc_co_u32_e64 v101, s[0:1], 0, v47, s[0:1]
	v_add_co_u32_e64 v104, s[0:1], s31, v46
	v_mov_b32_e32 v6, 0
	s_nop 0
	v_addc_co_u32_e64 v105, s[0:1], 0, v47, s[0:1]
	v_add_co_u32_e64 v108, s[0:1], s33, v46
	v_mov_b32_e32 v7, 0
	s_nop 0
	v_addc_co_u32_e64 v109, s[0:1], 0, v47, s[0:1]
	v_add_co_u32_e64 v112, s[0:1], s34, v46
	v_mov_b32_e32 v8, 0
	s_nop 0
	v_addc_co_u32_e64 v113, s[0:1], 0, v47, s[0:1]
	v_add_co_u32_e64 v116, s[0:1], s35, v46
	v_mov_b32_e32 v9, 0
	s_nop 0
	v_addc_co_u32_e64 v117, s[0:1], 0, v47, s[0:1]
	v_add_co_u32_e64 v120, s[0:1], s36, v46
	v_mov_b32_e32 v10, 0
	s_nop 0
	v_addc_co_u32_e64 v121, s[0:1], 0, v47, s[0:1]
	v_add_co_u32_e64 v124, s[0:1], s37, v46
	v_mov_b32_e32 v11, 0
	s_nop 0
	v_addc_co_u32_e64 v125, s[0:1], 0, v47, s[0:1]
	v_add_co_u32_e64 v128, s[0:1], s38, v46
	v_mov_b32_e32 v12, 0
	s_nop 0
	v_addc_co_u32_e64 v129, s[0:1], 0, v47, s[0:1]
	v_add_co_u32_e64 v132, s[0:1], s39, v46
	v_mov_b32_e32 v13, 0
	s_nop 0
	v_addc_co_u32_e64 v133, s[0:1], 0, v47, s[0:1]
	v_add_co_u32_e64 v46, s[0:1], s40, v46
	v_mov_b32_e32 v14, 0
	s_nop 0
	v_addc_co_u32_e64 v47, s[0:1], 0, v47, s[0:1]
	global_load_dwordx4 v[80:83], v[80:81], off nt
	s_nop 0
	global_load_dwordx4 v[84:87], v[84:85], off nt
	s_nop 0
	global_load_dwordx4 v[88:91], v[88:89], off nt
	s_nop 0
	global_load_dwordx4 v[92:95], v[92:93], off nt
	s_nop 0
	global_load_dwordx4 v[96:99], v[96:97], off nt
	s_nop 0
	global_load_dwordx4 v[100:103], v[100:101], off nt
	s_nop 0
	global_load_dwordx4 v[104:107], v[104:105], off nt
	s_nop 0
	global_load_dwordx4 v[108:111], v[108:109], off nt
	s_nop 0
	global_load_dwordx4 v[112:115], v[112:113], off nt
	s_nop 0
	global_load_dwordx4 v[116:119], v[116:117], off nt
	s_nop 0
	global_load_dwordx4 v[120:123], v[120:121], off nt
	s_nop 0
	global_load_dwordx4 v[124:127], v[124:125], off nt
	s_nop 0
	global_load_dwordx4 v[128:131], v[128:129], off nt
	s_nop 0
	global_load_dwordx4 v[132:135], v[132:133], off nt
	s_nop 0
	global_load_dwordx4 v[136:139], v[46:47], off nt
	v_mov_b32_e32 v15, 0
	v_mov_b32_e32 v16, 0
	v_mov_b32_e32 v17, 0
	v_or_b32_e32 v140, v148, v18
	v_lshlrev_b64 v[46:47], 11, v[140:141]
	v_or_b32_e32 v140, v148, v20
	v_lshlrev_b64 v[144:145], 11, v[140:141]
	v_or_b32_e32 v140, v148, v22
	v_lshlrev_b64 v[146:147], 11, v[140:141]
	v_or_b32_e32 v140, v148, v24
	v_lshl_add_u64 v[46:47], v[142:143], 0, v[46:47]
	v_lshlrev_b64 v[140:141], 11, v[140:141]
	v_lshl_add_u64 v[144:145], v[142:143], 0, v[144:145]
	v_lshl_add_u64 v[146:147], v[142:143], 0, v[146:147]
	v_lshl_add_u64 v[140:141], v[142:143], 0, v[140:141]
	v_add_u32_e32 v41, s3, v41
	v_cmp_lt_i32_e32 vcc, s42, v41
	v_add_u32_e32 v38, s22, v38
	s_or_b64 s[18:19], vcc, s[18:19]
	v_add_u32_e32 v40, s23, v40
	s_waitcnt vmcnt(15)
	ds_write2_b32 v25, v42, v43 offset1:1
	ds_write2_b32 v25, v44, v45 offset0:2 offset1:3
	s_waitcnt vmcnt(14)
	ds_write2_b32 v39, v80, v81 offset1:1
	ds_write2_b32 v48, v82, v83 offset1:1
	s_waitcnt vmcnt(13)
	ds_write2_b32 v49, v84, v85 offset1:1
	ds_write2_b32 v50, v86, v87 offset1:1
	s_waitcnt vmcnt(12)
	ds_write2_b32 v51, v88, v89 offset1:1
	ds_write2_b32 v52, v90, v91 offset1:1
	s_waitcnt vmcnt(11)
	ds_write2_b32 v53, v92, v93 offset1:1
	ds_write2_b32 v54, v94, v95 offset1:1
	s_waitcnt vmcnt(10)
	ds_write2_b32 v55, v96, v97 offset1:1
	ds_write2_b32 v56, v98, v99 offset1:1
	s_waitcnt vmcnt(9)
	ds_write2_b32 v57, v100, v101 offset1:1
	ds_write2_b32 v58, v102, v103 offset1:1
	s_waitcnt vmcnt(8)
	ds_write2_b32 v59, v104, v105 offset1:1
	ds_write2_b32 v60, v106, v107 offset1:1
	s_waitcnt vmcnt(7)
	ds_write2_b32 v61, v108, v109 offset1:1
	ds_write2_b32 v62, v110, v111 offset1:1
	s_waitcnt vmcnt(6)
	ds_write2_b32 v63, v112, v113 offset1:1
	ds_write2_b32 v64, v114, v115 offset1:1
	s_waitcnt vmcnt(5)
	ds_write2_b32 v65, v116, v117 offset1:1
	ds_write2_b32 v66, v118, v119 offset1:1
	s_waitcnt vmcnt(4)
	ds_write2_b32 v67, v120, v121 offset1:1
	ds_write2_b32 v68, v122, v123 offset1:1
	s_waitcnt vmcnt(3)
	ds_write2_b32 v69, v124, v125 offset1:1
	ds_write2_b32 v70, v126, v127 offset1:1
	s_waitcnt vmcnt(2)
	ds_write2_b32 v71, v128, v129 offset1:1
	ds_write2_b32 v72, v130, v131 offset1:1
	s_waitcnt vmcnt(1)
	ds_write2_b32 v73, v132, v133 offset1:1
	ds_write2_b32 v74, v134, v135 offset1:1
	s_waitcnt vmcnt(0)
	ds_write2_b32 v76, v136, v137 offset1:1
	ds_write2_b32 v77, v138, v139 offset1:1
	s_waitcnt lgkmcnt(0)
	ds_read2_b32 v[42:43], v19 offset1:8
	ds_read2_b32 v[44:45], v19 offset0:33 offset1:41
	ds_read2_b32 v[80:81], v19 offset0:66 offset1:74
	ds_read2_b32 v[82:83], v19 offset0:99 offset1:107
	ds_read2_b32 v[84:85], v19 offset0:132 offset1:140
	ds_read2_b32 v[86:87], v19 offset0:165 offset1:173
	ds_read2_b32 v[88:89], v19 offset0:198 offset1:206
	ds_read2_b32 v[90:91], v19 offset0:231 offset1:239
	ds_read2_b32 v[92:93], v78 offset0:8 offset1:16
	ds_read2_b32 v[94:95], v78 offset0:41 offset1:49
	ds_read2_b32 v[96:97], v78 offset0:74 offset1:82
	ds_read2_b32 v[98:99], v78 offset0:107 offset1:115
	ds_read2_b32 v[100:101], v78 offset0:140 offset1:148
	ds_read2_b32 v[102:103], v78 offset0:173 offset1:181
	ds_read2_b32 v[104:105], v78 offset0:206 offset1:214
	ds_read2_b32 v[106:107], v78 offset0:239 offset1:247
	ds_read2_b32 v[108:109], v19 offset0:16 offset1:24
	ds_read2_b32 v[110:111], v19 offset0:49 offset1:57
	ds_read2_b32 v[112:113], v19 offset0:82 offset1:90
	ds_read2_b32 v[114:115], v19 offset0:115 offset1:123
	ds_read2_b32 v[116:117], v19 offset0:148 offset1:156
	ds_read2_b32 v[118:119], v19 offset0:181 offset1:189
	ds_read2_b32 v[120:121], v19 offset0:214 offset1:222
	ds_read2_b32 v[122:123], v19 offset0:247 offset1:255
	ds_read2_b32 v[124:125], v78 offset0:24 offset1:32
	ds_read2_b32 v[126:127], v78 offset0:57 offset1:65
	ds_read2_b32 v[128:129], v78 offset0:90 offset1:98
	ds_read2_b32 v[130:131], v78 offset0:123 offset1:131
	ds_read2_b32 v[132:133], v78 offset0:156 offset1:164
	ds_read2_b32 v[134:135], v78 offset0:189 offset1:197
	ds_read2_b32 v[136:137], v78 offset0:222 offset1:230
	ds_read2_b32 v[138:139], v79 offset0:127 offset1:135
	s_waitcnt lgkmcnt(14)
	v_mul_f32_e32 v42, 0x43800000, v42
	v_mul_f32_e32 v44, 0x43800000, v44
	v_mul_f32_e32 v84, 0x43800000, v84
	v_mul_f32_e32 v86, 0x43800000, v86
	v_mul_f32_e32 v92, 0x43800000, v92
	v_mul_f32_e32 v94, 0x43800000, v94
	v_mul_f32_e32 v100, 0x43800000, v100
	v_mul_f32_e32 v102, 0x43800000, v102
	v_mul_f32_e32 v43, 0x43800000, v43
	v_mul_f32_e32 v45, 0x43800000, v45
	v_mul_f32_e32 v85, 0x43800000, v85
	v_mul_f32_e32 v87, 0x43800000, v87
	v_mul_f32_e32 v93, 0x43800000, v93
	v_mul_f32_e32 v95, 0x43800000, v95
	v_mul_f32_e32 v101, 0x43800000, v101
	v_mul_f32_e32 v103, 0x43800000, v103
	v_med3_f32 v42, v42, s41, v75
	v_med3_f32 v44, v44, s41, v75
	v_med3_f32 v84, v84, s41, v75
	v_med3_f32 v86, v86, s41, v75
	v_med3_f32 v92, v92, s41, v75
	v_med3_f32 v94, v94, s41, v75
	v_med3_f32 v100, v100, s41, v75
	v_med3_f32 v102, v102, s41, v75
	v_mul_f32_e32 v108, 0x43800000, v108
	v_mul_f32_e32 v110, 0x43800000, v110
	s_waitcnt lgkmcnt(11)
	v_mul_f32_e32 v116, 0x43800000, v116
	s_waitcnt lgkmcnt(10)
	v_mul_f32_e32 v118, 0x43800000, v118
	s_waitcnt lgkmcnt(7)
	v_mul_f32_e32 v124, 0x43800000, v124
	s_waitcnt lgkmcnt(6)
	v_mul_f32_e32 v126, 0x43800000, v126
	s_waitcnt lgkmcnt(3)
	v_mul_f32_e32 v132, 0x43800000, v132
	s_waitcnt lgkmcnt(2)
	v_mul_f32_e32 v134, 0x43800000, v134
	v_med3_f32 v43, v43, s41, v75
	v_med3_f32 v45, v45, s41, v75
	v_med3_f32 v85, v85, s41, v75
	v_med3_f32 v87, v87, s41, v75
	v_med3_f32 v93, v93, s41, v75
	v_med3_f32 v95, v95, s41, v75
	v_med3_f32 v101, v101, s41, v75
	v_med3_f32 v103, v103, s41, v75
	v_cvt_pk_fp8_f32 v2, v42, v44
	v_cvt_pk_fp8_f32 v3, v84, v86
	v_cvt_pk_fp8_f32 v4, v92, v94
	v_cvt_pk_fp8_f32 v5, v100, v102
	v_mul_f32_e32 v109, 0x43800000, v109
	v_mul_f32_e32 v111, 0x43800000, v111
	v_mul_f32_e32 v117, 0x43800000, v117
	v_mul_f32_e32 v119, 0x43800000, v119
	v_mul_f32_e32 v125, 0x43800000, v125
	v_mul_f32_e32 v127, 0x43800000, v127
	v_mul_f32_e32 v133, 0x43800000, v133
	v_mul_f32_e32 v135, 0x43800000, v135
	v_med3_f32 v108, v108, s41, v75
	v_med3_f32 v110, v110, s41, v75
	v_med3_f32 v116, v116, s41, v75
	v_med3_f32 v118, v118, s41, v75
	v_med3_f32 v124, v124, s41, v75
	v_med3_f32 v126, v126, s41, v75
	v_med3_f32 v132, v132, s41, v75
	v_med3_f32 v134, v134, s41, v75
	v_cvt_pk_fp8_f32 v6, v43, v45
	v_cvt_pk_fp8_f32 v7, v85, v87
	v_cvt_pk_fp8_f32 v8, v93, v95
	v_cvt_pk_fp8_f32 v9, v101, v103
	v_mul_f32_e32 v80, 0x43800000, v80
	v_mul_f32_e32 v82, 0x43800000, v82
	v_mul_f32_e32 v88, 0x43800000, v88
	v_mul_f32_e32 v90, 0x43800000, v90
	v_mul_f32_e32 v96, 0x43800000, v96
	v_mul_f32_e32 v98, 0x43800000, v98
	v_mul_f32_e32 v104, 0x43800000, v104
	v_mul_f32_e32 v106, 0x43800000, v106
	v_med3_f32 v109, v109, s41, v75
	v_med3_f32 v111, v111, s41, v75
	v_med3_f32 v117, v117, s41, v75
	v_med3_f32 v119, v119, s41, v75
	v_med3_f32 v125, v125, s41, v75
	v_med3_f32 v127, v127, s41, v75
	v_med3_f32 v133, v133, s41, v75
	v_med3_f32 v135, v135, s41, v75
	v_cvt_pk_fp8_f32 v10, v108, v110
	v_cvt_pk_fp8_f32 v11, v116, v118
	v_cvt_pk_fp8_f32 v12, v124, v126
	v_cvt_pk_fp8_f32 v13, v132, v134
	v_mul_f32_e32 v81, 0x43800000, v81
	v_mul_f32_e32 v83, 0x43800000, v83
	v_mul_f32_e32 v89, 0x43800000, v89
	v_mul_f32_e32 v91, 0x43800000, v91
	v_mul_f32_e32 v97, 0x43800000, v97
	v_mul_f32_e32 v99, 0x43800000, v99
	v_mul_f32_e32 v105, 0x43800000, v105
	v_mul_f32_e32 v107, 0x43800000, v107
	v_med3_f32 v80, v80, s41, v75
	v_med3_f32 v82, v82, s41, v75
	v_med3_f32 v88, v88, s41, v75
	v_med3_f32 v90, v90, s41, v75
	v_med3_f32 v96, v96, s41, v75
	v_med3_f32 v98, v98, s41, v75
	v_med3_f32 v104, v104, s41, v75
	v_med3_f32 v106, v106, s41, v75
	v_cvt_pk_fp8_f32 v14, v109, v111
	v_cvt_pk_fp8_f32 v15, v117, v119
	v_cvt_pk_fp8_f32 v16, v125, v127
	v_cvt_pk_fp8_f32 v17, v133, v135
	v_mul_f32_e32 v112, 0x43800000, v112
	v_mul_f32_e32 v114, 0x43800000, v114
	v_mul_f32_e32 v120, 0x43800000, v120
	v_mul_f32_e32 v122, 0x43800000, v122
	v_mul_f32_e32 v128, 0x43800000, v128
	v_mul_f32_e32 v130, 0x43800000, v130
	s_waitcnt lgkmcnt(1)
	v_mul_f32_e32 v136, 0x43800000, v136
	s_waitcnt lgkmcnt(0)
	v_mul_f32_e32 v138, 0x43800000, v138
	v_med3_f32 v81, v81, s41, v75
	v_med3_f32 v83, v83, s41, v75
	v_med3_f32 v89, v89, s41, v75
	v_med3_f32 v91, v91, s41, v75
	v_med3_f32 v97, v97, s41, v75
	v_med3_f32 v99, v99, s41, v75
	v_med3_f32 v105, v105, s41, v75
	v_med3_f32 v107, v107, s41, v75
	v_cvt_pk_fp8_f32 v2, v80, v82 op_sel:[0,0,1]
	v_cvt_pk_fp8_f32 v3, v88, v90 op_sel:[0,0,1]
	v_cvt_pk_fp8_f32 v4, v96, v98 op_sel:[0,0,1]
	v_cvt_pk_fp8_f32 v5, v104, v106 op_sel:[0,0,1]
	v_mul_f32_e32 v113, 0x43800000, v113
	v_mul_f32_e32 v115, 0x43800000, v115
	v_mul_f32_e32 v121, 0x43800000, v121
	v_mul_f32_e32 v123, 0x43800000, v123
	v_mul_f32_e32 v129, 0x43800000, v129
	v_mul_f32_e32 v131, 0x43800000, v131
	v_mul_f32_e32 v137, 0x43800000, v137
	v_mul_f32_e32 v139, 0x43800000, v139
	v_med3_f32 v112, v112, s41, v75
	v_med3_f32 v114, v114, s41, v75
	v_med3_f32 v120, v120, s41, v75
	v_med3_f32 v122, v122, s41, v75
	v_med3_f32 v128, v128, s41, v75
	v_med3_f32 v130, v130, s41, v75
	v_med3_f32 v136, v136, s41, v75
	v_med3_f32 v138, v138, s41, v75
	v_cvt_pk_fp8_f32 v6, v81, v83 op_sel:[0,0,1]
	v_cvt_pk_fp8_f32 v7, v89, v91 op_sel:[0,0,1]
	v_cvt_pk_fp8_f32 v8, v97, v99 op_sel:[0,0,1]
	v_cvt_pk_fp8_f32 v9, v105, v107 op_sel:[0,0,1]
	v_med3_f32 v113, v113, s41, v75
	v_med3_f32 v115, v115, s41, v75
	v_med3_f32 v121, v121, s41, v75
	v_med3_f32 v123, v123, s41, v75
	v_med3_f32 v129, v129, s41, v75
	v_med3_f32 v131, v131, s41, v75
	v_med3_f32 v137, v137, s41, v75
	v_med3_f32 v139, v139, s41, v75
	v_cvt_pk_fp8_f32 v10, v112, v114 op_sel:[0,0,1]
	v_cvt_pk_fp8_f32 v11, v120, v122 op_sel:[0,0,1]
	v_cvt_pk_fp8_f32 v12, v128, v130 op_sel:[0,0,1]
	v_cvt_pk_fp8_f32 v13, v136, v138 op_sel:[0,0,1]
	v_cvt_pk_fp8_f32 v14, v113, v115 op_sel:[0,0,1]
	v_cvt_pk_fp8_f32 v15, v121, v123 op_sel:[0,0,1]
	v_cvt_pk_fp8_f32 v16, v129, v131 op_sel:[0,0,1]
	v_cvt_pk_fp8_f32 v17, v137, v139 op_sel:[0,0,1]
	global_store_dwordx4 v[46:47], v[2:5], off
	global_store_dwordx4 v[144:145], v[6:9], off
	global_store_dwordx4 v[146:147], v[10:13], off
	global_store_dwordx4 v[140:141], v[14:17], off
	s_waitcnt lgkmcnt(0)
	s_andn2_b64 exec, exec, s[18:19]
	s_cbranch_execnz .LBB0_1564
	s_or_b64 exec, exec, s[18:19]
	s_mul_i32 s6, s14, 0x3800000
	s_lshl_b64 s[0:1], s[14:15], 11
	v_lshl_add_u64 v[36:37], v[34:35], 0, s[6:7]
	s_mov_b64 s[14:15], 0
	v_mov_b32_e32 v38, v23
	v_mov_b32_e32 v80, v1
.LBB0_1566:
	v_mul_hi_i32 v40, v80, s43
	v_add_u32_e32 v40, v40, v80
	v_lshrrev_b32_e32 v41, 31, v40
	v_ashrrev_i32_e32 v40, 5, v40
	v_add_u32_e32 v41, v40, v41
	v_lshlrev_b32_e32 v40, 5, v41
	v_mad_u64_u32 v[42:43], s[16:17], v41, s44, v[38:39]
	v_ashrrev_i32_e32 v41, 31, v40
	v_add_u32_e32 v44, v42, v18
	v_ashrrev_i32_e32 v43, 31, v42
	v_lshl_add_u64 v[46:47], s[0:1], 0, v[40:41]
	v_lshl_add_u64 v[86:87], v[40:41], 2, v[36:37]
	v_ashrrev_i32_e32 v45, 31, v44
	v_add_u32_e32 v40, 8, v44
	v_add_u32_e32 v82, 16, v44
	v_add_u32_e32 v84, 24, v44
	v_add_u32_e32 v88, 32, v44
	v_add_u32_e32 v90, 40, v44
	v_add_u32_e32 v92, 48, v44
	v_add_u32_e32 v94, 56, v44
	v_add_u32_e32 v96, 64, v44
	v_add_u32_e32 v98, 0x48, v44
	v_add_u32_e32 v100, 0x50, v44
	v_add_u32_e32 v102, 0x58, v44
	v_add_u32_e32 v104, 0x60, v44
	v_add_u32_e32 v106, 0x68, v44
	v_add_u32_e32 v108, 0x70, v44
	v_add_u32_e32 v110, 0x78, v44
	v_lshl_add_u64 v[112:113], v[28:29], 0, v[42:43]
	v_lshlrev_b64 v[42:43], 13, v[44:45]
	v_ashrrev_i32_e32 v41, 31, v40
	v_ashrrev_i32_e32 v83, 31, v82
	v_ashrrev_i32_e32 v85, 31, v84
	v_ashrrev_i32_e32 v89, 31, v88
	v_ashrrev_i32_e32 v91, 31, v90
	v_ashrrev_i32_e32 v93, 31, v92
	v_ashrrev_i32_e32 v95, 31, v94
	v_ashrrev_i32_e32 v97, 31, v96
	v_ashrrev_i32_e32 v99, 31, v98
	v_ashrrev_i32_e32 v101, 31, v100
	v_ashrrev_i32_e32 v103, 31, v102
	v_ashrrev_i32_e32 v105, 31, v104
	v_ashrrev_i32_e32 v107, 31, v106
	v_ashrrev_i32_e32 v109, 31, v108
	v_ashrrev_i32_e32 v111, 31, v110
	v_or_b32_e32 v44, v46, v18
	v_or_b32_e32 v45, v46, v20
	v_or_b32_e32 v122, v46, v22
	v_or_b32_e32 v123, v46, v24
	v_lshl_add_u64 v[114:115], v[86:87], 0, v[42:43]
	v_lshlrev_b64 v[116:117], 13, v[40:41]
	v_lshlrev_b64 v[118:119], 13, v[82:83]
	v_lshlrev_b64 v[120:121], 13, v[84:85]
	v_lshlrev_b64 v[88:89], 13, v[88:89]
	v_lshlrev_b64 v[90:91], 13, v[90:91]
	v_lshlrev_b64 v[92:93], 13, v[92:93]
	v_lshlrev_b64 v[94:95], 13, v[94:95]
	v_lshlrev_b64 v[96:97], 13, v[96:97]
	v_lshlrev_b64 v[98:99], 13, v[98:99]
	v_lshlrev_b64 v[100:101], 13, v[100:101]
	v_lshlrev_b64 v[102:103], 13, v[102:103]
	v_lshlrev_b64 v[104:105], 13, v[104:105]
	v_lshlrev_b64 v[106:107], 13, v[106:107]
	v_lshlrev_b64 v[108:109], 13, v[108:109]
	v_lshlrev_b64 v[110:111], 13, v[110:111]
	v_mul_lo_u32 v81, v47, s20
	v_mad_u64_u32 v[46:47], s[16:17], v44, s20, v[112:113]
	v_mad_u64_u32 v[44:45], s[16:17], v45, s20, v[112:113]
	v_mad_u64_u32 v[42:43], s[16:17], v122, s20, v[112:113]
	v_mad_u64_u32 v[40:41], s[16:17], v123, s20, v[112:113]
	global_load_dwordx4 v[82:85], v[114:115], off nt
	v_lshl_add_u64 v[112:113], v[86:87], 0, v[116:117]
	v_lshl_add_u64 v[114:115], v[86:87], 0, v[118:119]
	v_lshl_add_u64 v[116:117], v[86:87], 0, v[120:121]
	v_lshl_add_u64 v[118:119], v[86:87], 0, v[88:89]
	v_lshl_add_u64 v[120:121], v[86:87], 0, v[90:91]
	v_lshl_add_u64 v[122:123], v[86:87], 0, v[92:93]
	v_lshl_add_u64 v[124:125], v[86:87], 0, v[94:95]
	v_lshl_add_u64 v[126:127], v[86:87], 0, v[96:97]
	v_lshl_add_u64 v[128:129], v[86:87], 0, v[98:99]
	v_lshl_add_u64 v[130:131], v[86:87], 0, v[100:101]
	v_lshl_add_u64 v[132:133], v[86:87], 0, v[102:103]
	v_lshl_add_u64 v[134:135], v[86:87], 0, v[104:105]
	v_lshl_add_u64 v[136:137], v[86:87], 0, v[106:107]
	v_lshl_add_u64 v[138:139], v[86:87], 0, v[108:109]
	v_lshl_add_u64 v[142:143], v[86:87], 0, v[110:111]
	global_load_dwordx4 v[86:89], v[112:113], off nt
	global_load_dwordx4 v[90:93], v[114:115], off nt
	global_load_dwordx4 v[94:97], v[116:117], off nt
	global_load_dwordx4 v[98:101], v[118:119], off nt
	global_load_dwordx4 v[102:105], v[120:121], off nt
	global_load_dwordx4 v[106:109], v[122:123], off nt
	global_load_dwordx4 v[110:113], v[124:125], off nt
	s_nop 0
	global_load_dwordx4 v[114:117], v[126:127], off nt
	global_load_dwordx4 v[118:121], v[128:129], off nt
	global_load_dwordx4 v[122:125], v[130:131], off nt
	s_nop 0
	global_load_dwordx4 v[126:129], v[132:133], off nt
	s_nop 0
	global_load_dwordx4 v[130:133], v[134:135], off nt
	s_nop 0
	global_load_dwordx4 v[134:137], v[136:137], off nt
	s_nop 0
	global_load_dwordx4 v[138:141], v[138:139], off nt
	s_nop 0
	global_load_dwordx4 v[142:145], v[142:143], off nt
	s_waitcnt vmcnt(15)
	ds_write2_b32 v25, v82, v83 offset1:1
	ds_write2_b32 v25, v84, v85 offset0:2 offset1:3
	s_waitcnt vmcnt(14)
	ds_write2_b32 v39, v86, v87 offset1:1
	ds_write2_b32 v48, v88, v89 offset1:1
	s_waitcnt vmcnt(13)
	ds_write2_b32 v49, v90, v91 offset1:1
	ds_write2_b32 v50, v92, v93 offset1:1
	s_waitcnt vmcnt(12)
	ds_write2_b32 v51, v94, v95 offset1:1
	ds_write2_b32 v52, v96, v97 offset1:1
	s_waitcnt vmcnt(11)
	ds_write2_b32 v53, v98, v99 offset1:1
	ds_write2_b32 v54, v100, v101 offset1:1
	s_waitcnt vmcnt(10)
	ds_write2_b32 v55, v102, v103 offset1:1
	ds_write2_b32 v56, v104, v105 offset1:1
	s_waitcnt vmcnt(9)
	ds_write2_b32 v57, v106, v107 offset1:1
	ds_write2_b32 v58, v108, v109 offset1:1
	s_waitcnt vmcnt(8)
	ds_write2_b32 v59, v110, v111 offset1:1
	ds_write2_b32 v60, v112, v113 offset1:1
	s_waitcnt vmcnt(7)
	ds_write2_b32 v61, v114, v115 offset1:1
	ds_write2_b32 v62, v116, v117 offset1:1
	s_waitcnt vmcnt(6)
	ds_write2_b32 v63, v118, v119 offset1:1
	ds_write2_b32 v64, v120, v121 offset1:1
	s_waitcnt vmcnt(5)
	ds_write2_b32 v65, v122, v123 offset1:1
	ds_write2_b32 v66, v124, v125 offset1:1
	s_waitcnt vmcnt(4)
	ds_write2_b32 v67, v126, v127 offset1:1
	ds_write2_b32 v68, v128, v129 offset1:1
	s_waitcnt vmcnt(3)
	ds_write2_b32 v69, v130, v131 offset1:1
	ds_write2_b32 v70, v132, v133 offset1:1
	s_waitcnt vmcnt(2)
	ds_write2_b32 v71, v134, v135 offset1:1
	ds_write2_b32 v72, v136, v137 offset1:1
	s_waitcnt vmcnt(1)
	ds_write2_b32 v73, v138, v139 offset1:1
	ds_write2_b32 v74, v140, v141 offset1:1
	s_waitcnt vmcnt(0)
	ds_write2_b32 v76, v142, v143 offset1:1
	ds_write2_b32 v77, v144, v145 offset1:1
	s_waitcnt lgkmcnt(0)
	ds_read2_b32 v[82:83], v19 offset1:8
	ds_read2_b32 v[84:85], v19 offset0:33 offset1:41
	ds_read2_b32 v[86:87], v19 offset0:66 offset1:74
	ds_read2_b32 v[88:89], v19 offset0:99 offset1:107
	ds_read2_b32 v[90:91], v19 offset0:132 offset1:140
	ds_read2_b32 v[92:93], v19 offset0:165 offset1:173
	ds_read2_b32 v[94:95], v19 offset0:198 offset1:206
	ds_read2_b32 v[96:97], v19 offset0:231 offset1:239
	ds_read2_b32 v[98:99], v78 offset0:8 offset1:16
	ds_read2_b32 v[100:101], v78 offset0:41 offset1:49
	ds_read2_b32 v[102:103], v78 offset0:74 offset1:82
	ds_read2_b32 v[104:105], v78 offset0:107 offset1:115
	ds_read2_b32 v[106:107], v78 offset0:140 offset1:148
	ds_read2_b32 v[108:109], v78 offset0:173 offset1:181
	ds_read2_b32 v[110:111], v78 offset0:206 offset1:214
	ds_read2_b32 v[112:113], v78 offset0:239 offset1:247
	ds_read2_b32 v[114:115], v19 offset0:16 offset1:24
	ds_read2_b32 v[116:117], v19 offset0:49 offset1:57
	ds_read2_b32 v[118:119], v19 offset0:82 offset1:90
	ds_read2_b32 v[120:121], v19 offset0:115 offset1:123
	ds_read2_b32 v[122:123], v19 offset0:148 offset1:156
	ds_read2_b32 v[124:125], v19 offset0:181 offset1:189
	ds_read2_b32 v[126:127], v19 offset0:214 offset1:222
	ds_read2_b32 v[128:129], v19 offset0:247 offset1:255
	ds_read2_b32 v[130:131], v78 offset0:24 offset1:32
	ds_read2_b32 v[132:133], v78 offset0:57 offset1:65
	ds_read2_b32 v[134:135], v78 offset0:90 offset1:98
	ds_read2_b32 v[136:137], v78 offset0:123 offset1:131
	ds_read2_b32 v[138:139], v78 offset0:156 offset1:164
	ds_read2_b32 v[140:141], v78 offset0:189 offset1:197
	ds_read2_b32 v[142:143], v78 offset0:222 offset1:230
	ds_read2_b32 v[144:145], v79 offset0:127 offset1:135
	v_add_u32_e32 v47, v81, v47
	v_add_u32_e32 v45, v81, v45
	v_add_u32_e32 v43, v81, v43
	v_add_u32_e32 v41, v81, v41
	s_waitcnt lgkmcnt(14)
	v_mul_f32_e32 v81, 0x43800000, v82
	v_mul_f32_e32 v82, 0x43800000, v84
	v_mul_f32_e32 v84, 0x43800000, v86
	v_mul_f32_e32 v86, 0x43800000, v88
	v_mul_f32_e32 v88, 0x43800000, v90
	v_mul_f32_e32 v90, 0x43800000, v92
	v_mul_f32_e32 v92, 0x43800000, v94
	v_mul_f32_e32 v94, 0x43800000, v96
	v_mul_f32_e32 v96, 0x43800000, v98
	v_mul_f32_e32 v98, 0x43800000, v100
	v_mul_f32_e32 v100, 0x43800000, v102
	v_mul_f32_e32 v102, 0x43800000, v104
	v_mul_f32_e32 v104, 0x43800000, v106
	v_mul_f32_e32 v106, 0x43800000, v108
	v_mov_b32_e32 v2, 0
	v_mov_b32_e32 v3, 0
	v_mov_b32_e32 v4, 0
	v_mov_b32_e32 v5, 0
	v_mul_f32_e32 v83, 0x43800000, v83
	v_mul_f32_e32 v85, 0x43800000, v85
	v_mul_f32_e32 v91, 0x43800000, v91
	v_mul_f32_e32 v93, 0x43800000, v93
	v_mul_f32_e32 v99, 0x43800000, v99
	v_mul_f32_e32 v101, 0x43800000, v101
	v_mul_f32_e32 v107, 0x43800000, v107
	v_mul_f32_e32 v109, 0x43800000, v109
	v_med3_f32 v81, v81, s41, v75
	v_med3_f32 v82, v82, s41, v75
	v_med3_f32 v88, v88, s41, v75
	v_med3_f32 v90, v90, s41, v75
	v_med3_f32 v96, v96, s41, v75
	v_med3_f32 v98, v98, s41, v75
	v_med3_f32 v104, v104, s41, v75
	v_med3_f32 v106, v106, s41, v75
	v_mov_b32_e32 v6, 0
	v_mov_b32_e32 v7, 0
	v_mov_b32_e32 v8, 0
	v_mov_b32_e32 v9, 0
	v_mul_f32_e32 v108, 0x43800000, v110
	v_mul_f32_e32 v110, 0x43800000, v112
	v_mul_f32_e32 v112, 0x43800000, v113
	v_mul_f32_e32 v113, 0x43800000, v114
	v_mul_f32_e32 v114, 0x43800000, v116
	s_waitcnt lgkmcnt(13)
	v_mul_f32_e32 v116, 0x43800000, v118
	s_waitcnt lgkmcnt(12)
	v_mul_f32_e32 v118, 0x43800000, v120
	s_waitcnt lgkmcnt(11)
	v_mul_f32_e32 v120, 0x43800000, v122
	s_waitcnt lgkmcnt(10)
	v_mul_f32_e32 v122, 0x43800000, v124
	s_waitcnt lgkmcnt(9)
	v_mul_f32_e32 v124, 0x43800000, v126
	s_waitcnt lgkmcnt(8)
	v_mul_f32_e32 v126, 0x43800000, v128
	s_waitcnt lgkmcnt(7)
	v_mul_f32_e32 v128, 0x43800000, v130
	s_waitcnt lgkmcnt(6)
	v_mul_f32_e32 v130, 0x43800000, v132
	s_waitcnt lgkmcnt(5)
	v_mul_f32_e32 v132, 0x43800000, v134
	s_waitcnt lgkmcnt(4)
	v_mul_f32_e32 v134, 0x43800000, v136
	s_waitcnt lgkmcnt(3)
	v_mul_f32_e32 v136, 0x43800000, v138
	s_waitcnt lgkmcnt(2)
	v_mul_f32_e32 v138, 0x43800000, v140
	v_med3_f32 v83, v83, s41, v75
	v_med3_f32 v85, v85, s41, v75
	v_med3_f32 v91, v91, s41, v75
	v_med3_f32 v93, v93, s41, v75
	v_med3_f32 v99, v99, s41, v75
	v_med3_f32 v101, v101, s41, v75
	v_med3_f32 v107, v107, s41, v75
	v_med3_f32 v109, v109, s41, v75
	v_cvt_pk_fp8_f32 v2, v81, v82
	v_cvt_pk_fp8_f32 v3, v88, v90
	v_cvt_pk_fp8_f32 v4, v96, v98
	v_cvt_pk_fp8_f32 v5, v104, v106
	v_mov_b32_e32 v10, 0
	v_mov_b32_e32 v11, 0
	v_mov_b32_e32 v12, 0
	v_mov_b32_e32 v13, 0
	v_mul_f32_e32 v115, 0x43800000, v115
	v_mul_f32_e32 v117, 0x43800000, v117
	v_mul_f32_e32 v123, 0x43800000, v123
	v_mul_f32_e32 v125, 0x43800000, v125
	v_mul_f32_e32 v131, 0x43800000, v131
	v_mul_f32_e32 v133, 0x43800000, v133
	v_mul_f32_e32 v139, 0x43800000, v139
	v_mul_f32_e32 v141, 0x43800000, v141
	v_med3_f32 v113, v113, s41, v75
	v_med3_f32 v114, v114, s41, v75
	v_med3_f32 v120, v120, s41, v75
	v_med3_f32 v122, v122, s41, v75
	v_med3_f32 v128, v128, s41, v75
	v_med3_f32 v130, v130, s41, v75
	v_med3_f32 v136, v136, s41, v75
	v_med3_f32 v138, v138, s41, v75
	v_cvt_pk_fp8_f32 v6, v83, v85
	v_cvt_pk_fp8_f32 v7, v91, v93
	v_cvt_pk_fp8_f32 v8, v99, v101
	v_cvt_pk_fp8_f32 v9, v107, v109
	v_mov_b32_e32 v14, 0
	v_mov_b32_e32 v15, 0
	v_mov_b32_e32 v16, 0
	v_mov_b32_e32 v17, 0
	v_med3_f32 v115, v115, s41, v75
	v_med3_f32 v117, v117, s41, v75
	v_med3_f32 v123, v123, s41, v75
	v_med3_f32 v125, v125, s41, v75
	v_med3_f32 v131, v131, s41, v75
	v_med3_f32 v133, v133, s41, v75
	v_med3_f32 v139, v139, s41, v75
	v_med3_f32 v141, v141, s41, v75
	v_cvt_pk_fp8_f32 v10, v113, v114
	v_cvt_pk_fp8_f32 v11, v120, v122
	v_cvt_pk_fp8_f32 v12, v128, v130
	v_cvt_pk_fp8_f32 v13, v136, v138
	v_mul_f32_e32 v87, 0x43800000, v87
	v_mul_f32_e32 v89, 0x43800000, v89
	v_mul_f32_e32 v95, 0x43800000, v95
	v_mul_f32_e32 v97, 0x43800000, v97
	v_mul_f32_e32 v103, 0x43800000, v103
	v_mul_f32_e32 v105, 0x43800000, v105
	v_mul_f32_e32 v111, 0x43800000, v111
	v_med3_f32 v84, v84, s41, v75
	v_med3_f32 v86, v86, s41, v75
	v_med3_f32 v92, v92, s41, v75
	v_med3_f32 v94, v94, s41, v75
	v_med3_f32 v100, v100, s41, v75
	v_med3_f32 v102, v102, s41, v75
	v_med3_f32 v108, v108, s41, v75
	v_med3_f32 v110, v110, s41, v75
	v_cvt_pk_fp8_f32 v14, v115, v117
	v_cvt_pk_fp8_f32 v15, v123, v125
	v_cvt_pk_fp8_f32 v16, v131, v133
	v_cvt_pk_fp8_f32 v17, v139, v141
	s_waitcnt lgkmcnt(1)
	v_mul_f32_e32 v140, 0x43800000, v142
	s_waitcnt lgkmcnt(0)
	v_mul_f32_e32 v142, 0x43800000, v144
	v_med3_f32 v87, v87, s41, v75
	v_med3_f32 v89, v89, s41, v75
	v_med3_f32 v95, v95, s41, v75
	v_med3_f32 v97, v97, s41, v75
	v_med3_f32 v103, v103, s41, v75
	v_med3_f32 v105, v105, s41, v75
	v_med3_f32 v111, v111, s41, v75
	v_med3_f32 v112, v112, s41, v75
	v_cvt_pk_fp8_f32 v2, v84, v86 op_sel:[0,0,1]
	v_cvt_pk_fp8_f32 v3, v92, v94 op_sel:[0,0,1]
	v_cvt_pk_fp8_f32 v4, v100, v102 op_sel:[0,0,1]
	v_cvt_pk_fp8_f32 v5, v108, v110 op_sel:[0,0,1]
	v_mul_f32_e32 v119, 0x43800000, v119
	v_mul_f32_e32 v121, 0x43800000, v121
	v_mul_f32_e32 v127, 0x43800000, v127
	v_mul_f32_e32 v129, 0x43800000, v129
	v_mul_f32_e32 v135, 0x43800000, v135
	v_mul_f32_e32 v137, 0x43800000, v137
	v_mul_f32_e32 v143, 0x43800000, v143
	v_mul_f32_e32 v144, 0x43800000, v145
	v_med3_f32 v116, v116, s41, v75
	v_med3_f32 v118, v118, s41, v75
	v_med3_f32 v124, v124, s41, v75
	v_med3_f32 v126, v126, s41, v75
	v_med3_f32 v132, v132, s41, v75
	v_med3_f32 v134, v134, s41, v75
	v_med3_f32 v140, v140, s41, v75
	v_med3_f32 v142, v142, s41, v75
	v_cvt_pk_fp8_f32 v6, v87, v89 op_sel:[0,0,1]
	v_cvt_pk_fp8_f32 v7, v95, v97 op_sel:[0,0,1]
	v_cvt_pk_fp8_f32 v8, v103, v105 op_sel:[0,0,1]
	v_cvt_pk_fp8_f32 v9, v111, v112 op_sel:[0,0,1]
	v_med3_f32 v119, v119, s41, v75
	v_med3_f32 v121, v121, s41, v75
	v_med3_f32 v127, v127, s41, v75
	v_med3_f32 v129, v129, s41, v75
	v_med3_f32 v135, v135, s41, v75
	v_med3_f32 v137, v137, s41, v75
	v_med3_f32 v143, v143, s41, v75
	v_med3_f32 v144, v144, s41, v75
	v_cvt_pk_fp8_f32 v10, v116, v118 op_sel:[0,0,1]
	v_cvt_pk_fp8_f32 v11, v124, v126 op_sel:[0,0,1]
	v_cvt_pk_fp8_f32 v12, v132, v134 op_sel:[0,0,1]
	v_cvt_pk_fp8_f32 v13, v140, v142 op_sel:[0,0,1]
	v_cvt_pk_fp8_f32 v14, v119, v121 op_sel:[0,0,1]
	v_cvt_pk_fp8_f32 v15, v127, v129 op_sel:[0,0,1]
	v_cvt_pk_fp8_f32 v16, v135, v137 op_sel:[0,0,1]
	v_cvt_pk_fp8_f32 v17, v143, v144 op_sel:[0,0,1]
	global_store_dwordx4 v[46:47], v[2:5], off
	global_store_dwordx4 v[44:45], v[6:9], off
	global_store_dwordx4 v[42:43], v[10:13], off
	global_store_dwordx4 v[40:41], v[14:17], off
	v_add_u32_e32 v80, s3, v80
	s_waitcnt lgkmcnt(0)
	v_cmp_lt_i32_e32 vcc, s42, v80
	s_or_b64 s[14:15], vcc, s[14:15]
	v_add_u32_e32 v38, s23, v38
	s_andn2_b64 exec, exec, s[14:15]
	s_cbranch_execnz .LBB0_1566
	s_branch .LBB0_1559
